# dead zero-initialisations in front of v_cvt_pk_fp8_f32 pairs removed (224 sites; VALU-bound epilogues of P8, P9, P4, P3)
# speedup vs baseline: 1.0069x; 1.0069x over previous
; __device__ __forceinline__ void p0_prologue(Frame& F, const Args& A) {
;     ...
; #pragma unroll 1
;         for (int rep0 = 0; rep0 < P0_REP; ++rep0) {
;             f32x4 va[8], vb[8]; int r = F.c;
;             if (r < NT2) P0T_ISSUE(r, va);
; #pragma unroll 1
;             while (r < NT2) {
;                 int rn = r + F.G; if (rn < NT2) P0T_ISSUE(rn, vb);
;                 P0T_PROCESS(r, va); r = rn; if (r >= NT2) break;
;                 rn = r + F.G; if (rn < NT2) P0T_ISSUE(rn, va);
;                 P0T_PROCESS(r, vb); r = rn; }
.LBB0_84:
	s_ashr_i32 s2, s40, 31
	s_lshr_b32 s2, s2, 21
	s_add_i32 s2, s40, s2
	s_ashr_i32 s44, s2, 11
	s_and_b32 s2, s2, 0xfffff800
	s_lshl_b32 s3, s40, 7
	s_sub_i32 s2, s40, s2
	s_and_b32 s3, s3, 0x380
	s_waitcnt vmcnt(0)
	v_pk_mul_f32 v[98:99], v[30:31], v[80:81] op_sel_hi:[1,0]
	v_add_u32_e32 v105, 0x1428, v92
	s_ashr_i32 s2, s2, 6
	s_add_i32 s40, s3, s7
	ds_write2_b32 v105, v98, v99 offset1:1
	v_pk_mul_f32 v[98:99], v[32:33], v[80:81] op_sel_hi:[1,0]
	v_add_u32_e32 v106, 0x1430, v92
	s_ashr_i32 s3, s2, 31
	s_lshl_b32 s45, s40, 1
	s_lshl_b32 s44, s44, 3
	ds_write2_b32 v106, v98, v99 offset1:1
	s_lshl_b64 s[18:19], s[2:3], 11
	s_and_b32 s45, s45, 0x7fffff00
	s_ashr_i32 s50, s44, 31
	v_add_u32_e32 v98, 0x400, v86
	v_add_u32_e32 v99, 0x800, v86
	s_waitcnt lgkmcnt(0)
	s_barrier
	s_add_u32 s44, s44, s20
	ds_read2_b32 v[108:109], v86 offset0:129 offset1:133
	ds_read2_b32 v[110:111], v86 offset1:4
	ds_read2_b32 v[112:113], v98 offset0:2 offset1:6
	ds_read2_b32 v[114:115], v98 offset0:131 offset1:135
	ds_read2_b32 v[118:119], v99 offset0:4 offset1:8
	ds_read2_b32 v[120:121], v99 offset0:133 offset1:137
	s_addc_u32 s50, s50, 0
	s_add_u32 s18, s44, s18
	s_addc_u32 s19, s50, s19
	v_add_u32_e32 v100, 0xc00, v86
	s_add_u32 s18, s18, s45
	ds_read2_b32 v[122:123], v100 offset0:6 offset1:10
	ds_read2_b32 v[124:125], v100 offset0:135 offset1:139
	s_addc_u32 s19, s19, 0
	s_lshl_b64 s[2:3], s[2:3], 10
	s_addk_i32 s40, 0x4000
	s_waitcnt lgkmcnt(6)
	v_cvt_pk_fp8_f32 v116, v110, v108
	s_waitcnt lgkmcnt(2)
	v_cvt_pk_fp8_f32 v117, v118, v120
	s_add_u32 s40, s2, s40
	s_addc_u32 s44, s3, 0
	s_and_b64 s[2:3], exec, s[12:13]
	s_cselect_b32 s3, s44, s19
	s_cselect_b32 s2, s40, s18
	v_cvt_pk_fp8_f32 v116, v112, v114 op_sel:[0,0,1]
	s_waitcnt lgkmcnt(0)
	v_cvt_pk_fp8_f32 v117, v122, v124 op_sel:[0,0,1]
	v_cvt_pk_fp8_f32 v108, v111, v109
	v_lshl_add_u64 v[128:129], s[2:3], 0, v[72:73]
	v_cvt_pk_fp8_f32 v109, v119, v121
	v_lshl_add_u64 v[126:127], v[74:75], 0, s[4:5]
	v_lshlrev_b64 v[128:129], 10, v[128:129]
	v_lshl_add_u64 v[110:111], v[126:127], 0, v[128:129]
	global_store_dwordx2 v[110:111], v[116:117], off
	v_cvt_pk_fp8_f32 v108, v113, v115 op_sel:[0,0,1]
	v_cvt_pk_fp8_f32 v109, v123, v125 op_sel:[0,0,1]
	ds_read2_b32 v[112:113], v86 offset0:137 offset1:141
	ds_read2_b32 v[114:115], v98 offset0:10 offset1:14
	ds_read2_b32 v[116:117], v86 offset0:8 offset1:12
	ds_read2_b32 v[118:119], v98 offset0:139 offset1:143
	ds_read2_b32 v[122:123], v99 offset0:12 offset1:16
	ds_read2_b32 v[124:125], v99 offset0:141 offset1:145
	v_lshl_add_u64 v[110:111], s[2:3], 0, v[76:77]
	v_lshlrev_b64 v[110:111], 10, v[110:111]
	v_lshl_add_u64 v[110:111], v[126:127], 0, v[110:111]
	ds_read2_b32 v[128:129], v100 offset0:14 offset1:18
	ds_read2_b32 v[130:131], v100 offset0:143 offset1:147
	global_store_dwordx2 v[110:111], v[108:109], off
	s_waitcnt lgkmcnt(5)
	v_cvt_pk_fp8_f32 v120, v116, v112
	s_waitcnt lgkmcnt(2)
	v_cvt_pk_fp8_f32 v121, v122, v124
	v_cvt_pk_fp8_f32 v110, v117, v113
	v_cvt_pk_fp8_f32 v111, v123, v125
	v_cvt_pk_fp8_f32 v120, v114, v118 op_sel:[0,0,1]
	s_waitcnt lgkmcnt(0)
	v_cvt_pk_fp8_f32 v121, v128, v130 op_sel:[0,0,1]
	v_cvt_pk_fp8_f32 v110, v115, v119 op_sel:[0,0,1]
	v_cvt_pk_fp8_f32 v111, v129, v131 op_sel:[0,0,1]
	v_mov_b32_e32 v79, v69
	v_lshl_add_u64 v[108:109], s[2:3], 0, v[68:69]
	v_lshl_add_u64 v[78:79], s[2:3], 0, v[78:79]
	v_lshlrev_b64 v[108:109], 10, v[108:109]
	v_lshlrev_b64 v[78:79], 10, v[78:79]
	v_lshl_add_u64 v[108:109], v[126:127], 0, v[108:109]
	v_lshl_add_u64 v[78:79], v[126:127], 0, v[78:79]
	s_andn2_b64 vcc, exec, s[10:11]
	global_store_dwordx2 v[108:109], v[120:121], off
	global_store_dwordx2 v[78:79], v[110:111], off
	s_barrier
	s_cbranch_vccnz .LBB0_63
	s_add_i32 s40, s41, s92
	s_cmpk_gt_i32 s40, 0x17ff
	s_cbranch_scc1 .LBB0_87
	s_ashr_i32 s2, s40, 31
	s_lshr_b32 s2, s2, 21
	s_add_i32 s2, s40, s2
	s_and_b32 s2, s2, 0xfffff800
	s_sub_i32 s2, s40, s2
	s_ashr_i32 s2, s2, 6
	s_and_b32 s3, s40, 0xfffff800
	s_cmpk_eq_i32 s3, 0x800
	s_cselect_b32 s4, s86, s82
	s_cselect_b32 s10, s87, s83
	s_cmpk_eq_i32 s3, 0x1000
	s_cselect_b32 s10, s91, s10
	s_cselect_b32 s4, s90, s4
	s_ashr_i32 s3, s2, 31
	s_lshl_b64 s[2:3], s[2:3], 22
	s_add_u32 s2, s4, s2
	s_addc_u32 s3, s10, s3
	s_lshl_b32 s4, s40, 4
	s_and_b32 s4, s4, 0x380
	v_add_u32_e32 v68, s4, v67
	v_lshlrev_b64 v[2:3], 12, v[68:69]
	v_lshl_add_u64 v[2:3], s[2:3], 0, v[2:3]
	s_lshl_b32 s2, s40, 9
	s_and_b32 s4, s2, 0xe00
	v_lshl_add_u64 v[2:3], v[2:3], 0, s[4:5]
	v_mov_b32_e32 v71, v69
	v_lshl_add_u64 v[26:27], v[2:3], 0, v[70:71]
	v_add_co_u32_e32 v6, vcc, s21, v26
	s_nop 1
	v_addc_co_u32_e32 v7, vcc, 0, v27, vcc
	v_add_co_u32_e32 v10, vcc, s24, v26
	global_load_dwordx4 v[2:5], v[26:27], off nt
	s_nop 0
	global_load_dwordx4 v[6:9], v[6:7], off nt
	v_addc_co_u32_e32 v11, vcc, 0, v27, vcc
	v_add_co_u32_e32 v14, vcc, s25, v26
	s_nop 1
	v_addc_co_u32_e32 v15, vcc, 0, v27, vcc
	v_add_co_u32_e32 v18, vcc, s35, v26
	global_load_dwordx4 v[10:13], v[10:11], off nt
	s_nop 0
	global_load_dwordx4 v[14:17], v[14:15], off nt
	v_addc_co_u32_e32 v19, vcc, 0, v27, vcc
	v_add_co_u32_e32 v22, vcc, 0xa000, v26
	s_nop 1
	v_addc_co_u32_e32 v23, vcc, 0, v27, vcc
	v_add_co_u32_e32 v28, vcc, 0xc000, v26
	global_load_dwordx4 v[18:21], v[18:19], off nt
	s_nop 0
	global_load_dwordx4 v[22:25], v[22:23], off nt
	v_addc_co_u32_e32 v29, vcc, 0, v27, vcc
	v_add_co_u32_e32 v30, vcc, 0xe000, v26
	s_nop 1
	v_addc_co_u32_e32 v31, vcc, 0, v27, vcc
	global_load_dwordx4 v[26:29], v[28:29], off nt
	s_nop 0
	global_load_dwordx4 v[30:33], v[30:31], off nt

; __device__ __forceinline__ void p0_prologue(Frame& F, const Args& A) {
;     ...
; #pragma unroll 1
;         for (int rep0 = 0; rep0 < P0_REP; ++rep0) {
;             f32x4 va[8], vb[8]; int r = F.c;
;             if (r < NT2) P0T_ISSUE(r, va);
; #pragma unroll 1
;             while (r < NT2) {
;                 int rn = r + F.G; if (rn < NT2) P0T_ISSUE(rn, vb);
;                 P0T_PROCESS(r, va); r = rn; if (r >= NT2) break;
;                 rn = r + F.G; if (rn < NT2) P0T_ISSUE(rn, va);
;                 P0T_PROCESS(r, vb); r = rn; }
.LBB0_103:
	s_ashr_i32 s2, s41, 31
	s_lshr_b32 s2, s2, 21
	s_add_i32 s2, s41, s2
	s_ashr_i32 s18, s2, 11
	s_and_b32 s2, s2, 0xfffff800
	s_lshl_b32 s3, s41, 7
	s_sub_i32 s2, s41, s2
	s_and_b32 s3, s3, 0x380
	s_ashr_i32 s2, s2, 6
	s_add_i32 s19, s3, s7
	v_pk_mul_f32 v[94:95], v[62:63], v[80:81] op_sel_hi:[1,0]
	s_ashr_i32 s3, s2, 31
	s_lshl_b32 s41, s19, 1
	s_lshl_b32 s18, s18, 3
	ds_write2_b32 v105, v94, v95 offset1:1
	v_pk_mul_f32 v[94:95], v[64:65], v[80:81] op_sel_hi:[1,0]
	s_lshl_b64 s[12:13], s[2:3], 11
	s_and_b32 s41, s41, 0x7fffff00
	s_ashr_i32 s44, s18, 31
	ds_write2_b32 v106, v94, v95 offset1:1
	s_waitcnt lgkmcnt(0)
	s_barrier
	s_add_u32 s18, s18, s20
	ds_read2_b32 v[94:95], v86 offset0:129 offset1:133
	ds_read2_b32 v[96:97], v98 offset0:2 offset1:6
	ds_read2_b32 v[102:103], v86 offset1:4
	ds_read2_b32 v[104:105], v98 offset0:131 offset1:135
	ds_read2_b32 v[108:109], v99 offset0:4 offset1:8
	ds_read2_b32 v[110:111], v99 offset0:133 offset1:137
	s_addc_u32 s44, s44, 0
	s_add_u32 s12, s18, s12
	s_addc_u32 s13, s44, s13
	s_add_u32 s12, s12, s41
	ds_read2_b32 v[112:113], v100 offset0:6 offset1:10
	ds_read2_b32 v[114:115], v100 offset0:135 offset1:139
	s_addc_u32 s13, s13, 0
	s_lshl_b64 s[2:3], s[2:3], 10
	s_addk_i32 s19, 0x4000
	s_waitcnt lgkmcnt(5)
	v_cvt_pk_fp8_f32 v106, v102, v94
	s_waitcnt lgkmcnt(2)
	v_cvt_pk_fp8_f32 v107, v108, v110
	s_add_u32 s18, s2, s19
	s_addc_u32 s19, s3, 0
	s_and_b64 s[2:3], exec, s[10:11]
	s_cselect_b32 s3, s19, s13
	s_cselect_b32 s2, s18, s12
	v_cvt_pk_fp8_f32 v106, v96, v104 op_sel:[0,0,1]
	s_waitcnt lgkmcnt(0)
	v_cvt_pk_fp8_f32 v107, v112, v114 op_sel:[0,0,1]
	v_cvt_pk_fp8_f32 v94, v103, v95
	v_lshl_add_u64 v[118:119], s[2:3], 0, v[72:73]
	v_cvt_pk_fp8_f32 v95, v109, v111
	v_lshl_add_u64 v[116:117], v[74:75], 0, s[4:5]
	v_lshlrev_b64 v[118:119], 10, v[118:119]
	v_lshl_add_u64 v[102:103], v[116:117], 0, v[118:119]
	global_store_dwordx2 v[102:103], v[106:107], off
	v_cvt_pk_fp8_f32 v94, v97, v105 op_sel:[0,0,1]
	v_cvt_pk_fp8_f32 v95, v113, v115 op_sel:[0,0,1]
	ds_read2_b32 v[102:103], v86 offset0:137 offset1:141
	ds_read2_b32 v[104:105], v98 offset0:10 offset1:14
	ds_read2_b32 v[106:107], v86 offset0:8 offset1:12
	ds_read2_b32 v[108:109], v98 offset0:139 offset1:143
	ds_read2_b32 v[110:111], v99 offset0:12 offset1:16
	ds_read2_b32 v[112:113], v99 offset0:141 offset1:145
	v_lshl_add_u64 v[96:97], s[2:3], 0, v[76:77]
	v_lshlrev_b64 v[96:97], 10, v[96:97]
	v_lshl_add_u64 v[96:97], v[116:117], 0, v[96:97]
	ds_read2_b32 v[114:115], v100 offset0:14 offset1:18
	ds_read2_b32 v[100:101], v100 offset0:143 offset1:147
	global_store_dwordx2 v[96:97], v[94:95], off
	s_waitcnt lgkmcnt(5)
	v_cvt_pk_fp8_f32 v98, v106, v102
	s_waitcnt lgkmcnt(2)
	v_cvt_pk_fp8_f32 v99, v110, v112
	v_cvt_pk_fp8_f32 v96, v107, v103
	v_cvt_pk_fp8_f32 v97, v111, v113
	v_cvt_pk_fp8_f32 v98, v104, v108 op_sel:[0,0,1]
	s_waitcnt lgkmcnt(0)
	v_cvt_pk_fp8_f32 v99, v114, v100 op_sel:[0,0,1]
	v_cvt_pk_fp8_f32 v96, v105, v109 op_sel:[0,0,1]
	v_cvt_pk_fp8_f32 v97, v115, v101 op_sel:[0,0,1]
	v_mov_b32_e32 v79, v69
	v_lshl_add_u64 v[94:95], s[2:3], 0, v[68:69]
	v_lshl_add_u64 v[78:79], s[2:3], 0, v[78:79]
	v_lshlrev_b64 v[94:95], 10, v[94:95]
	v_lshlrev_b64 v[78:79], 10, v[78:79]
	v_lshl_add_u64 v[94:95], v[116:117], 0, v[94:95]
	v_lshl_add_u64 v[78:79], v[116:117], 0, v[78:79]
	global_store_dwordx2 v[94:95], v[98:99], off
	global_store_dwordx2 v[78:79], v[96:97], off
	s_barrier
	s_branch .LBB0_64

; __device__ __forceinline__ unsigned pk4_fp8(float a, float b, float c, float d) { int w = __builtin_amdgcn_cvt_pk_fp8_f32(a, b, 0, false); w = __builtin_amdgcn_cvt_pk_fp8_f32(c, d, w, true); return (unsigned)w; }
;     __device__ __forceinline__ void operator()(const f32x4 (&acc)[2][2][4][2], const pg8::Unit& u, int wr, int wc, int fr, int fq) const {
;         const int rt = WHICH == 0 ? u.pn : u.pm, ct = WHICH == 0 ? u.pm : u.pn; const float sc = WHICH == 0 ? 64.0f : 1.0f;
;         unsigned char* base = out + ((size_t)u.aux * 1024 + rt * 256 + wr * 64 + fr) * 1024 + ct * 256 + wc * 64 + 16 * fq;
; #pragma unroll
;         for (int ai = 0; ai < 2; ++ai)
; #pragma unroll
;             for (int m = 0; m < 4; ++m)
;             { const f32x4 v0 = acc[ai][0][m][0] * sc, v1 = acc[ai][0][m][1] * sc, v2 = acc[ai][1][m][0] * sc, v3 = acc[ai][1][m][1] * sc;
;                     *(u32x4*)(base + (size_t)(ai * 128 + m * 16) * 1024) = (u32x4){pk4_fp8(v0[0], v0[1], v0[2], v0[3]), pk4_fp8(v1[0], v1[1], v1[2], v1[3]), pk4_fp8(v2[0], v2[1], v2[2], v2[3]), pk4_fp8(v3[0], v3[1], v3[2], v3[3])}; }
.LBB0_454:
	s_lshl_b32 s15, s15, 8
	s_ashr_i32 s29, s28, 31
	s_ashr_i32 s30, s15, 31
	v_pk_mul_f32 v[118:119], v[118:119], s[26:27] op_sel_hi:[1,0]
	v_pk_mul_f32 v[140:141], v[116:117], s[26:27] op_sel_hi:[1,0]
	s_add_u32 s15, s15, s68
	v_pk_mul_f32 v[114:115], v[114:115], s[26:27] op_sel_hi:[1,0]
	v_pk_mul_f32 v[126:127], v[126:127], s[26:27] op_sel_hi:[1,0]
	v_pk_mul_f32 v[122:123], v[122:123], s[26:27] op_sel_hi:[1,0]
	v_cvt_pk_fp8_f32 v116, v118, v119
	v_mov_b32_e32 v137, v0
	s_addc_u32 s30, s30, s69
	s_lshl_b64 s[28:29], s[28:29], 20
	v_cvt_pk_fp8_f32 v117, v114, v115
	v_cvt_pk_fp8_f32 v118, v126, v127
	v_cvt_pk_fp8_f32 v119, v122, v123
	v_mov_b32_e32 v139, s30
	v_and_or_b32 v138, v137, 15, s15
	s_add_u32 s28, s56, s28
	v_lshlrev_b64 v[138:139], 10, v[138:139]
	s_addc_u32 s29, s57, s29
	v_lshl_add_u64 v[138:139], s[28:29], 0, v[138:139]
	s_lshl_b32 s28, s13, 8
	v_pk_mul_f32 v[120:121], v[120:121], s[26:27] op_sel_hi:[1,0]
	v_pk_mul_f32 v[128:129], v[128:129], s[26:27] op_sel_hi:[1,0]
	v_pk_mul_f32 v[124:125], v[124:125], s[26:27] op_sel_hi:[1,0]
	s_ashr_i32 s29, s28, 31
	v_cvt_pk_fp8_f32 v116, v120, v121 op_sel:[0,0,1]
	v_cvt_pk_fp8_f32 v117, v140, v141 op_sel:[0,0,1]
	v_cvt_pk_fp8_f32 v118, v128, v129 op_sel:[0,0,1]
	v_cvt_pk_fp8_f32 v119, v124, v125 op_sel:[0,0,1]
	v_lshl_add_u64 v[114:115], v[138:139], 0, s[28:29]
	v_and_b32_e32 v130, 48, v137
	v_lshl_add_u64 v[114:115], v[114:115], 0, s[20:21]
	v_lshl_add_u64 v[114:115], v[114:115], 0, v[130:131]
	global_store_dwordx4 v[114:115], v[116:119], off
	v_pk_mul_f32 v[102:103], v[102:103], s[26:27] op_sel_hi:[1,0]
	v_pk_mul_f32 v[110:111], v[110:111], s[26:27] op_sel_hi:[1,0]
	v_pk_mul_f32 v[116:117], v[100:101], s[26:27] op_sel_hi:[1,0]
	v_pk_mul_f32 v[100:101], v[98:99], s[26:27] op_sel_hi:[1,0]
	v_pk_mul_f32 v[106:107], v[106:107], s[26:27] op_sel_hi:[1,0]
	v_cvt_pk_fp8_f32 v99, v100, v101
	v_cvt_pk_fp8_f32 v98, v102, v103
	v_cvt_pk_fp8_f32 v100, v110, v111
	v_cvt_pk_fp8_f32 v101, v106, v107
	v_pk_mul_f32 v[104:105], v[104:105], s[26:27] op_sel_hi:[1,0]
	v_pk_mul_f32 v[112:113], v[112:113], s[26:27] op_sel_hi:[1,0]
	v_pk_mul_f32 v[108:109], v[108:109], s[26:27] op_sel_hi:[1,0]
	v_cvt_pk_fp8_f32 v98, v104, v105 op_sel:[0,0,1]
	v_cvt_pk_fp8_f32 v99, v116, v117 op_sel:[0,0,1]
	v_cvt_pk_fp8_f32 v100, v112, v113 op_sel:[0,0,1]
	v_cvt_pk_fp8_f32 v101, v108, v109 op_sel:[0,0,1]
	s_movk_i32 s13, 0x4000
	v_add_co_u32_e32 v102, vcc, s13, v114
	v_pk_mul_f32 v[86:87], v[86:87], s[26:27] op_sel_hi:[1,0]
	s_nop 0
	v_addc_co_u32_e32 v103, vcc, 0, v115, vcc
	global_store_dwordx4 v[102:103], v[98:101], off
	v_pk_mul_f32 v[94:95], v[94:95], s[26:27] op_sel_hi:[1,0]
	v_pk_mul_f32 v[90:91], v[90:91], s[26:27] op_sel_hi:[1,0]
	v_pk_mul_f32 v[98:99], v[84:85], s[26:27] op_sel_hi:[1,0]
	v_pk_mul_f32 v[84:85], v[82:83], s[26:27] op_sel_hi:[1,0]
	v_cvt_pk_fp8_f32 v83, v84, v85
	v_cvt_pk_fp8_f32 v82, v86, v87
	v_cvt_pk_fp8_f32 v84, v94, v95
	v_cvt_pk_fp8_f32 v85, v90, v91
	v_pk_mul_f32 v[88:89], v[88:89], s[26:27] op_sel_hi:[1,0]
	v_pk_mul_f32 v[96:97], v[96:97], s[26:27] op_sel_hi:[1,0]
	v_pk_mul_f32 v[92:93], v[92:93], s[26:27] op_sel_hi:[1,0]
	v_cvt_pk_fp8_f32 v82, v88, v89 op_sel:[0,0,1]
	v_cvt_pk_fp8_f32 v83, v98, v99 op_sel:[0,0,1]
	v_cvt_pk_fp8_f32 v84, v96, v97 op_sel:[0,0,1]
	v_cvt_pk_fp8_f32 v85, v92, v93 op_sel:[0,0,1]
	s_mov_b32 s13, 0x8000
	v_add_co_u32_e32 v86, vcc, s13, v114
	v_pk_mul_f32 v[66:67], v[66:67], s[26:27] op_sel_hi:[1,0]
	s_nop 0
	v_addc_co_u32_e32 v87, vcc, 0, v115, vcc
	global_store_dwordx4 v[86:87], v[82:85], off
	v_pk_mul_f32 v[78:79], v[78:79], s[26:27] op_sel_hi:[1,0]
	v_pk_mul_f32 v[74:75], v[74:75], s[26:27] op_sel_hi:[1,0]
	v_pk_mul_f32 v[82:83], v[60:61], s[26:27] op_sel_hi:[1,0]
	v_pk_mul_f32 v[60:61], v[58:59], s[26:27] op_sel_hi:[1,0]
	v_cvt_pk_fp8_f32 v59, v60, v61
	v_cvt_pk_fp8_f32 v58, v66, v67
	v_cvt_pk_fp8_f32 v60, v78, v79
	v_cvt_pk_fp8_f32 v61, v74, v75
	v_pk_mul_f32 v[68:69], v[68:69], s[26:27] op_sel_hi:[1,0]
	v_pk_mul_f32 v[80:81], v[80:81], s[26:27] op_sel_hi:[1,0]
	v_pk_mul_f32 v[76:77], v[76:77], s[26:27] op_sel_hi:[1,0]
	v_cvt_pk_fp8_f32 v58, v68, v69 op_sel:[0,0,1]
	v_cvt_pk_fp8_f32 v59, v82, v83 op_sel:[0,0,1]
	v_cvt_pk_fp8_f32 v60, v80, v81 op_sel:[0,0,1]
	v_cvt_pk_fp8_f32 v61, v76, v77 op_sel:[0,0,1]
	s_mov_b32 s13, 0xc000
	v_add_co_u32_e32 v66, vcc, s13, v114
	v_pk_mul_f32 v[54:55], v[54:55], s[26:27] op_sel_hi:[1,0]
; __device__ __forceinline__ unsigned pk4_fp8(float a, float b, float c, float d) { int w = __builtin_amdgcn_cvt_pk_fp8_f32(a, b, 0, false); w = __builtin_amdgcn_cvt_pk_fp8_f32(c, d, w, true); return (unsigned)w; }
;     __device__ __forceinline__ void operator()(const f32x4 (&acc)[2][2][4][2], const pg8::Unit& u, int wr, int wc, int fr, int fq) const {
;         const int rt = WHICH == 0 ? u.pn : u.pm, ct = WHICH == 0 ? u.pm : u.pn; const float sc = WHICH == 0 ? 64.0f : 1.0f;
;         unsigned char* base = out + ((size_t)u.aux * 1024 + rt * 256 + wr * 64 + fr) * 1024 + ct * 256 + wc * 64 + 16 * fq;
; #pragma unroll
;         for (int ai = 0; ai < 2; ++ai)
; #pragma unroll
;             for (int m = 0; m < 4; ++m)
;             { const f32x4 v0 = acc[ai][0][m][0] * sc, v1 = acc[ai][0][m][1] * sc, v2 = acc[ai][1][m][0] * sc, v3 = acc[ai][1][m][1] * sc;
;                     *(u32x4*)(base + (size_t)(ai * 128 + m * 16) * 1024) = (u32x4){pk4_fp8(v0[0], v0[1], v0[2], v0[3]), pk4_fp8(v1[0], v1[1], v1[2], v1[3]), pk4_fp8(v2[0], v2[1], v2[2], v2[3]), pk4_fp8(v3[0], v3[1], v3[2], v3[3])}; }
	s_nop 0
	v_addc_co_u32_e32 v67, vcc, 0, v115, vcc
	global_store_dwordx4 v[66:67], v[58:61], off
	v_pk_mul_f32 v[66:67], v[70:71], s[26:27] op_sel_hi:[1,0]
	v_pk_mul_f32 v[62:63], v[62:63], s[26:27] op_sel_hi:[1,0]
	v_pk_mul_f32 v[58:59], v[52:53], s[26:27] op_sel_hi:[1,0]
	v_pk_mul_f32 v[52:53], v[50:51], s[26:27] op_sel_hi:[1,0]
	v_cvt_pk_fp8_f32 v51, v52, v53
	v_cvt_pk_fp8_f32 v50, v54, v55
	v_cvt_pk_fp8_f32 v52, v66, v67
	v_cvt_pk_fp8_f32 v53, v62, v63
	v_pk_mul_f32 v[56:57], v[56:57], s[26:27] op_sel_hi:[1,0]
	v_pk_mul_f32 v[60:61], v[72:73], s[26:27] op_sel_hi:[1,0]
	v_pk_mul_f32 v[64:65], v[64:65], s[26:27] op_sel_hi:[1,0]
	v_cvt_pk_fp8_f32 v50, v56, v57 op_sel:[0,0,1]
	v_cvt_pk_fp8_f32 v51, v58, v59 op_sel:[0,0,1]
	v_cvt_pk_fp8_f32 v52, v60, v61 op_sel:[0,0,1]
	v_cvt_pk_fp8_f32 v53, v64, v65 op_sel:[0,0,1]
	s_mov_b32 s13, 0x20000
	v_add_co_u32_e32 v54, vcc, s13, v114
	v_pk_mul_f32 v[38:39], v[38:39], s[26:27] op_sel_hi:[1,0]
	s_nop 0
	v_addc_co_u32_e32 v55, vcc, 0, v115, vcc
	global_store_dwordx4 v[54:55], v[50:53], off
	v_pk_mul_f32 v[46:47], v[46:47], s[26:27] op_sel_hi:[1,0]
	v_pk_mul_f32 v[42:43], v[42:43], s[26:27] op_sel_hi:[1,0]
	v_pk_mul_f32 v[50:51], v[36:37], s[26:27] op_sel_hi:[1,0]
	v_pk_mul_f32 v[36:37], v[34:35], s[26:27] op_sel_hi:[1,0]
	v_cvt_pk_fp8_f32 v35, v36, v37
	v_cvt_pk_fp8_f32 v34, v38, v39
	v_cvt_pk_fp8_f32 v36, v46, v47
	v_cvt_pk_fp8_f32 v37, v42, v43
	v_pk_mul_f32 v[40:41], v[40:41], s[26:27] op_sel_hi:[1,0]
	v_pk_mul_f32 v[48:49], v[48:49], s[26:27] op_sel_hi:[1,0]
	v_pk_mul_f32 v[44:45], v[44:45], s[26:27] op_sel_hi:[1,0]
	v_cvt_pk_fp8_f32 v34, v40, v41 op_sel:[0,0,1]
	v_cvt_pk_fp8_f32 v35, v50, v51 op_sel:[0,0,1]
	v_cvt_pk_fp8_f32 v36, v48, v49 op_sel:[0,0,1]
	v_cvt_pk_fp8_f32 v37, v44, v45 op_sel:[0,0,1]
	s_mov_b32 s13, 0x24000
	v_add_co_u32_e32 v38, vcc, s13, v114
	v_pk_mul_f32 v[22:23], v[22:23], s[26:27] op_sel_hi:[1,0]
	s_nop 0
	v_addc_co_u32_e32 v39, vcc, 0, v115, vcc
	global_store_dwordx4 v[38:39], v[34:37], off
	v_pk_mul_f32 v[30:31], v[30:31], s[26:27] op_sel_hi:[1,0]
	v_pk_mul_f32 v[26:27], v[26:27], s[26:27] op_sel_hi:[1,0]
	v_pk_mul_f32 v[34:35], v[20:21], s[26:27] op_sel_hi:[1,0]
	v_pk_mul_f32 v[20:21], v[18:19], s[26:27] op_sel_hi:[1,0]
	v_cvt_pk_fp8_f32 v19, v20, v21
	v_cvt_pk_fp8_f32 v18, v22, v23
	v_cvt_pk_fp8_f32 v20, v30, v31
	v_cvt_pk_fp8_f32 v21, v26, v27
	v_pk_mul_f32 v[24:25], v[24:25], s[26:27] op_sel_hi:[1,0]
	v_pk_mul_f32 v[32:33], v[32:33], s[26:27] op_sel_hi:[1,0]
	v_pk_mul_f32 v[28:29], v[28:29], s[26:27] op_sel_hi:[1,0]
	v_cvt_pk_fp8_f32 v18, v24, v25 op_sel:[0,0,1]
	v_cvt_pk_fp8_f32 v19, v34, v35 op_sel:[0,0,1]
	v_cvt_pk_fp8_f32 v20, v32, v33 op_sel:[0,0,1]
	v_cvt_pk_fp8_f32 v21, v28, v29 op_sel:[0,0,1]
	s_mov_b32 s13, 0x28000
	v_add_co_u32_e32 v22, vcc, s13, v114
	v_pk_mul_f32 v[6:7], v[6:7], s[26:27] op_sel_hi:[1,0]
	s_nop 0
	v_addc_co_u32_e32 v23, vcc, 0, v115, vcc
	global_store_dwordx4 v[22:23], v[18:21], off
	v_pk_mul_f32 v[14:15], v[14:15], s[26:27] op_sel_hi:[1,0]
	v_pk_mul_f32 v[10:11], v[10:11], s[26:27] op_sel_hi:[1,0]
	v_pk_mul_f32 v[18:19], v[4:5], s[26:27] op_sel_hi:[1,0]
	v_pk_mul_f32 v[4:5], v[2:3], s[26:27] op_sel_hi:[1,0]
	v_cvt_pk_fp8_f32 v3, v4, v5
	v_cvt_pk_fp8_f32 v2, v6, v7
	v_cvt_pk_fp8_f32 v4, v14, v15
	v_cvt_pk_fp8_f32 v5, v10, v11
	v_pk_mul_f32 v[8:9], v[8:9], s[26:27] op_sel_hi:[1,0]
	v_pk_mul_f32 v[16:17], v[16:17], s[26:27] op_sel_hi:[1,0]
	v_pk_mul_f32 v[12:13], v[12:13], s[26:27] op_sel_hi:[1,0]
	v_cvt_pk_fp8_f32 v2, v8, v9 op_sel:[0,0,1]
	v_cvt_pk_fp8_f32 v3, v18, v19 op_sel:[0,0,1]
	v_cvt_pk_fp8_f32 v4, v16, v17 op_sel:[0,0,1]
	v_cvt_pk_fp8_f32 v5, v12, v13 op_sel:[0,0,1]
	v_add_co_u32_e32 v6, vcc, 0x2c000, v114
	s_mov_b64 s[30:31], -1
	s_nop 0
	v_addc_co_u32_e32 v7, vcc, 0, v115, vcc
	s_and_b64 vcc, exec, s[2:3]
	global_store_dwordx4 v[6:7], v[2:5], off
	s_cbranch_vccnz .LBB0_446
	s_andn2_b64 vcc, exec, s[18:19]
	s_mov_b64 s[28:29], s[10:11]
	s_mov_b64 s[2:3], s[8:9]
	s_cbranch_vccnz .LBB0_457
	s_ashr_i32 s13, s12, 31
	s_lshl_b64 s[2:3], s[12:13], 20
	s_add_u32 s2, s61, s2
	s_addc_u32 s3, s63, s3
	s_lshl_b32 s13, s66, 9
	s_ashr_i32 s30, s13, 31
	s_add_u32 s2, s2, s13
	s_addc_u32 s3, s3, s30
	s_ashr_i32 s15, s14, 31
	s_lshl_b64 s[28:29], s[14:15], 19
	s_add_u32 s15, s7, s28
	s_addc_u32 s29, s65, s29
	s_add_u32 s28, s15, s13
	s_addc_u32 s29, s29, s30

; __device__ __forceinline__ unsigned pk4_fp8(float a, float b, float c, float d) { int w = __builtin_amdgcn_cvt_pk_fp8_f32(a, b, 0, false); w = __builtin_amdgcn_cvt_pk_fp8_f32(c, d, w, true); return (unsigned)w; }
;     __device__ __forceinline__ void operator()(const f32x4 (&acc)[2][2][4][2], const pg8::Unit& u, int wr, int wc, int fr, int fq) const {
;         const int rt = WHICH == 0 ? u.pn : u.pm, ct = WHICH == 0 ? u.pm : u.pn; const float sc = WHICH == 0 ? 64.0f : 1.0f;
;         unsigned char* base = out + ((size_t)u.aux * 1024 + rt * 256 + wr * 64 + fr) * 1024 + ct * 256 + wc * 64 + 16 * fq;
; #pragma unroll
;         for (int ai = 0; ai < 2; ++ai)
; #pragma unroll
;             for (int m = 0; m < 4; ++m)
;             { const f32x4 v0 = acc[ai][0][m][0] * sc, v1 = acc[ai][0][m][1] * sc, v2 = acc[ai][1][m][0] * sc, v3 = acc[ai][1][m][1] * sc;
;                     *(u32x4*)(base + (size_t)(ai * 128 + m * 16) * 1024) = (u32x4){pk4_fp8(v0[0], v0[1], v0[2], v0[3]), pk4_fp8(v1[0], v1[1], v1[2], v1[3]), pk4_fp8(v2[0], v2[1], v2[2], v2[3]), pk4_fp8(v3[0], v3[1], v3[2], v3[3])}; }
.LBB0_475:
	s_lshl_b32 s13, s13, 8
	s_ashr_i32 s25, s24, 31
	s_ashr_i32 s26, s13, 31
	s_add_u32 s13, s13, s62
	v_mov_b32_e32 v137, v0
	s_addc_u32 s26, s26, s65
	s_lshl_b64 s[24:25], s[24:25], 20
	v_mov_b32_e32 v139, s26
	v_and_or_b32 v138, v137, 15, s13
	s_add_u32 s24, s63, s24
	v_lshlrev_b64 v[138:139], 10, v[138:139]
	s_addc_u32 s25, s64, s25
	v_lshl_add_u64 v[142:143], s[24:25], 0, v[138:139]
	s_lshl_b32 s24, s11, 8
	v_cvt_pk_fp8_f32 v138, v106, v107
	s_ashr_i32 s25, s24, 31
	v_lshl_add_u64 v[106:107], v[142:143], 0, s[24:25]
	v_and_b32_e32 v130, 48, v137
	v_lshl_add_u64 v[106:107], v[106:107], 0, s[18:19]
	v_cvt_pk_fp8_f32 v139, v114, v115
	v_cvt_pk_fp8_f32 v138, v108, v109 op_sel:[0,0,1]
	v_lshl_add_u64 v[114:115], v[106:107], 0, v[130:131]
	v_cvt_pk_fp8_f32 v106, v94, v95
	v_cvt_pk_fp8_f32 v107, v102, v103
	v_cvt_pk_fp8_f32 v108, v110, v111
	v_cvt_pk_fp8_f32 v109, v118, v119
	v_cvt_pk_fp8_f32 v106, v96, v97 op_sel:[0,0,1]
	v_cvt_pk_fp8_f32 v107, v104, v105 op_sel:[0,0,1]
	v_cvt_pk_fp8_f32 v108, v112, v113 op_sel:[0,0,1]
	v_cvt_pk_fp8_f32 v109, v120, v121 op_sel:[0,0,1]
	s_movk_i32 s11, 0x4000
	v_add_co_u32_e32 v94, vcc, s11, v114
	s_nop 0
	v_addc_co_u32_e32 v95, vcc, 0, v115, vcc
	global_store_dwordx4 v[94:95], v[106:109], off
	v_cvt_pk_fp8_f32 v94, v74, v75
	v_cvt_pk_fp8_f32 v95, v86, v87
	v_cvt_pk_fp8_f32 v96, v90, v91
	v_cvt_pk_fp8_f32 v97, v98, v99
	v_cvt_pk_fp8_f32 v94, v76, v77 op_sel:[0,0,1]
	v_cvt_pk_fp8_f32 v95, v88, v89 op_sel:[0,0,1]
	v_cvt_pk_fp8_f32 v96, v92, v93 op_sel:[0,0,1]
	v_cvt_pk_fp8_f32 v97, v100, v101 op_sel:[0,0,1]
	s_mov_b32 s11, 0x8000
	v_add_co_u32_e32 v74, vcc, s11, v114
	s_nop 0
	v_addc_co_u32_e32 v75, vcc, 0, v115, vcc
	global_store_dwordx4 v[74:75], v[94:97], off
	v_cvt_pk_fp8_f32 v74, v42, v43
	v_cvt_pk_fp8_f32 v75, v58, v59
	v_cvt_pk_fp8_f32 v76, v66, v67
	v_cvt_pk_fp8_f32 v77, v78, v79
	v_cvt_pk_fp8_f32 v74, v44, v45 op_sel:[0,0,1]
	v_cvt_pk_fp8_f32 v75, v60, v61 op_sel:[0,0,1]
	v_cvt_pk_fp8_f32 v76, v68, v69 op_sel:[0,0,1]
	v_cvt_pk_fp8_f32 v77, v80, v81 op_sel:[0,0,1]
	s_mov_b32 s11, 0xc000
	v_add_co_u32_e32 v42, vcc, s11, v114
	s_nop 0
	v_addc_co_u32_e32 v43, vcc, 0, v115, vcc
	global_store_dwordx4 v[42:43], v[74:77], off
	v_cvt_pk_fp8_f32 v42, v46, v47
	v_cvt_pk_fp8_f32 v43, v62, v63
	v_cvt_pk_fp8_f32 v44, v70, v71
	v_cvt_pk_fp8_f32 v45, v82, v83
	v_cvt_pk_fp8_f32 v42, v48, v49 op_sel:[0,0,1]
	v_cvt_pk_fp8_f32 v43, v64, v65 op_sel:[0,0,1]
	v_cvt_pk_fp8_f32 v44, v72, v73 op_sel:[0,0,1]
	v_cvt_pk_fp8_f32 v45, v84, v85 op_sel:[0,0,1]
	v_add_co_u32_e32 v46, vcc, s66, v114
	s_nop 0
	v_addc_co_u32_e32 v47, vcc, 0, v115, vcc
	global_store_dwordx4 v[46:47], v[42:45], off
	v_cvt_pk_fp8_f32 v140, v122, v123
	v_cvt_pk_fp8_f32 v42, v26, v27
	v_cvt_pk_fp8_f32 v43, v38, v39
	v_cvt_pk_fp8_f32 v44, v50, v51
	v_cvt_pk_fp8_f32 v45, v54, v55
	v_cvt_pk_fp8_f32 v42, v28, v29 op_sel:[0,0,1]
	v_cvt_pk_fp8_f32 v43, v40, v41 op_sel:[0,0,1]
	v_cvt_pk_fp8_f32 v44, v52, v53 op_sel:[0,0,1]
	v_cvt_pk_fp8_f32 v45, v56, v57 op_sel:[0,0,1]
	v_add_co_u32_e32 v26, vcc, s67, v114
	s_nop 0
	v_addc_co_u32_e32 v27, vcc, 0, v115, vcc
	global_store_dwordx4 v[26:27], v[42:45], off
	v_cvt_pk_fp8_f32 v26, v14, v15
	v_cvt_pk_fp8_f32 v27, v22, v23
	v_cvt_pk_fp8_f32 v28, v30, v31
	v_cvt_pk_fp8_f32 v29, v34, v35
	v_cvt_pk_fp8_f32 v26, v16, v17 op_sel:[0,0,1]
	v_cvt_pk_fp8_f32 v27, v24, v25 op_sel:[0,0,1]
	v_cvt_pk_fp8_f32 v28, v32, v33 op_sel:[0,0,1]
	v_cvt_pk_fp8_f32 v29, v36, v37 op_sel:[0,0,1]
	v_add_co_u32_e32 v14, vcc, s68, v114
	s_nop 0
	v_addc_co_u32_e32 v15, vcc, 0, v115, vcc
	global_store_dwordx4 v[14:15], v[26:29], off
	v_cvt_pk_fp8_f32 v141, v126, v127
	v_cvt_pk_fp8_f32 v14, v2, v3
	v_cvt_pk_fp8_f32 v15, v6, v7
	v_cvt_pk_fp8_f32 v16, v10, v11
	v_cvt_pk_fp8_f32 v17, v18, v19
	v_cvt_pk_fp8_f32 v139, v116, v117 op_sel:[0,0,1]
	v_cvt_pk_fp8_f32 v140, v124, v125 op_sel:[0,0,1]
	v_cvt_pk_fp8_f32 v141, v128, v129 op_sel:[0,0,1]
	v_cvt_pk_fp8_f32 v14, v4, v5 op_sel:[0,0,1]
	v_cvt_pk_fp8_f32 v15, v8, v9 op_sel:[0,0,1]
	v_cvt_pk_fp8_f32 v16, v12, v13 op_sel:[0,0,1]
	v_cvt_pk_fp8_f32 v17, v20, v21 op_sel:[0,0,1]
	v_add_co_u32_e32 v2, vcc, 0x2c000, v114
	s_mov_b64 s[26:27], -1
	s_nop 0
	v_addc_co_u32_e32 v3, vcc, 0, v115, vcc
	s_and_b64 vcc, exec, s[2:3]
	global_store_dwordx4 v[114:115], v[138:141], off
	global_store_dwordx4 v[2:3], v[14:17], off
	s_cbranch_vccnz .LBB0_467
	s_andn2_b64 vcc, exec, s[14:15]
	s_mov_b64 s[24:25], s[8:9]
	s_mov_b64 s[2:3], s[6:7]
	s_cbranch_vccnz .LBB0_478
	s_ashr_i32 s13, s12, 31
	s_lshl_b64 s[2:3], s[12:13], 19
	s_add_u32 s2, s48, s2
	s_addc_u32 s3, s51, s3
	s_lshl_b32 s13, s5, 9
	s_ashr_i32 s26, s13, 31
	s_add_u32 s2, s2, s13
	s_addc_u32 s3, s3, s26
	s_ashr_i32 s11, s10, 31
	s_lshl_b64 s[24:25], s[10:11], 20
	s_add_u32 s11, s58, s24
	s_addc_u32 s24, s59, s25
	s_add_u32 s11, s11, s13
	s_addc_u32 s13, s24, s26
	s_add_u32 s24, s11, 0x25000800
	s_addc_u32 s25, s13, 0

; __device__ __forceinline__ unsigned cvt_pk_bf16(float lo, float hi) { unsigned r; asm volatile("v_cvt_pk_bf16_f32 %0, %1, %2" : "=v"(r) : "v"(lo), "v"(hi)); return r; }
;     __device__ __forceinline__ void operator()(const f32x4 (&acc)[2][2][4][2], const pg8::Unit& u, int wr, int wc, int fr, int fq) const {
;         const int row0 = u.pm * 256 + wr * 64 + fr, col0 = u.pn * 256 + wc * 64 + 16 * fq;
; #pragma unroll
;         for (int ai = 0; ai < 2; ++ai) {
;             f32x4 b0[4][2], b1[4][2];
; #pragma unroll
;             for (int m = 0; m < 4; ++m)
; #pragma unroll
;                 for (int bj = 0; bj < 2; ++bj) { const size_t off = (size_t)(row0 + ai * 128 + m * 16) * D + col0 + bj * 8;
;                     if (BASE_F32) { b0[m][bj] = *(const f32x4*)((const float*)base + off); b1[m][bj] = *(const f32x4*)((const float*)base + off + 4); }
;                     else { const u32x4 w = *(const u32x4*)((const bf16*)base + off); b0[m][bj] = (f32x4){bflo(w.x), bfhi(w.x), bflo(w.y), bfhi(w.y)}; b1[m][bj] = (f32x4){bflo(w.z), bfhi(w.z), bflo(w.w), bfhi(w.w)}; } }
;             asm volatile("" ::: "memory");
; #pragma unroll
;             for (int m = 0; m < 4; ++m) { const int row = row0 + ai * 128 + m * 16; float ss = 0.f;
;                 u32x4 q;
; #pragma unroll
;                 for (int bj = 0; bj < 2; ++bj) { const size_t off = (size_t)row * D + col0 + bj * 8;
;                     const float asc = BASE_F32 ? 1.0f : (1.0f / 256.0f);
;                     const f32x4 v0 = acc[ai][bj][m][0] * asc + b0[m][bj], v1 = acc[ai][bj][m][1] * asc + b1[m][bj];
;                     ss += (v0[0] * v0[0] + v0[1] * v0[1]) + (v0[2] * v0[2] + v0[3] * v0[3]) + (v1[0] * v1[0] + v1[1] * v1[1]) + (v1[2] * v1[2] + v1[3] * v1[3]);
;                     u32x4 w; w.x = cvt_pk_bf16(v0[0], v0[1]); w.y = cvt_pk_bf16(v0[2], v0[3]); w.z = cvt_pk_bf16(v1[0], v1[1]); w.w = cvt_pk_bf16(v1[2], v1[3]);
;                     *(u32x4*)(out + off) = w;
;                     if (BASE_F32) { const unsigned qa = pk4_fp8(v0[0], v0[1], v0[2], v0[3]), qb = pk4_fp8(v1[0], v1[1], v1[2], v1[3]); if (bj == 0) { q.x = qa; q.y = qb; } else { q.z = qa; q.w = qb; } } }
;                 if (BASE_F32) *(u32x4*)(q8 + (size_t)row * D + col0) = q;
;                 ss += __shfl_xor(ss, 16); ss += __shfl_xor(ss, 32);
;                 if (fq == 0) ssq[(size_t)row * 16 + u.pn * 4 + wc] = ss; }
.LBB0_554:
	s_lshl_b32 s2, s19, 8
	v_mov_b32_e32 v130, v0
	s_add_i32 s2, s2, s42
	v_and_or_b32 v182, v130, 15, s2
	s_lshl_b32 s2, s15, 8
	v_bfe_u32 v179, v130, 4, 2
	s_or_b32 s2, s2, s43
	v_lshl_or_b32 v180, v179, 4, s2
	v_ashrrev_i32_e32 v181, 31, v180
	v_ashrrev_i32_e32 v183, 31, v182
	v_lshl_add_u64 v[184:185], v[180:181], 2, s[16:17]
	v_lshlrev_b64 v[130:131], 12, v[182:183]
	v_lshl_add_u64 v[130:131], v[184:185], 0, v[130:131]
	global_load_dwordx4 v[198:201], v[130:131], off
	global_load_dwordx4 v[202:205], v[130:131], off offset:16
	global_load_dwordx4 v[206:209], v[130:131], off offset:32
	global_load_dwordx4 v[210:213], v[130:131], off offset:48
	v_or_b32_e32 v190, 16, v182
	v_or_b32_e32 v188, 32, v182
	v_or_b32_e32 v186, 48, v182
	v_ashrrev_i32_e32 v191, 31, v190
	v_ashrrev_i32_e32 v189, 31, v188
	v_ashrrev_i32_e32 v187, 31, v186
	v_lshlrev_b64 v[130:131], 12, v[190:191]
	v_lshlrev_b64 v[132:133], 12, v[188:189]
	v_lshlrev_b64 v[134:135], 12, v[186:187]
	v_lshl_add_u64 v[130:131], v[184:185], 0, v[130:131]
	v_lshl_add_u64 v[132:133], v[184:185], 0, v[132:133]
	v_lshl_add_u64 v[142:143], v[184:185], 0, v[134:135]
	global_load_dwordx4 v[162:165], v[130:131], off offset:48
	global_load_dwordx4 v[166:169], v[130:131], off offset:32
	global_load_dwordx4 v[170:173], v[130:131], off offset:16
	global_load_dwordx4 v[174:177], v[130:131], off
	global_load_dwordx4 v[146:149], v[132:133], off offset:48
	global_load_dwordx4 v[150:153], v[132:133], off offset:32
	global_load_dwordx4 v[154:157], v[132:133], off offset:16
	global_load_dwordx4 v[158:161], v[132:133], off
	s_nop 0
	global_load_dwordx4 v[130:133], v[142:143], off offset:48
	global_load_dwordx4 v[134:137], v[142:143], off offset:32
	global_load_dwordx4 v[138:141], v[142:143], off offset:16
	s_nop 0
	global_load_dwordx4 v[142:145], v[142:143], off
	v_lshlrev_b64 v[216:217], 11, v[182:183]
	v_cmp_eq_u32_e32 vcc, 0, v179
	v_lshl_add_u64 v[216:217], s[24:25], 0, v[216:217]
	v_lshl_add_u64 v[218:219], v[180:181], 1, v[216:217]
	s_lshl_b32 s34, s15, 2
	s_ashr_i32 s35, s34, 31
	s_waitcnt vmcnt(15)
	v_pk_add_f32 v[200:201], v[116:117], v[200:201]
	v_pk_add_f32 v[198:199], v[114:115], v[198:199]
	s_waitcnt vmcnt(14)
	v_pk_add_f32 v[118:119], v[118:119], v[202:203]
	s_waitcnt vmcnt(13)
	v_pk_add_f32 v[128:129], v[128:129], v[208:209]
	v_pk_add_f32 v[126:127], v[126:127], v[206:207]
	s_waitcnt vmcnt(12)
	v_pk_add_f32 v[122:123], v[122:123], v[210:211]
	v_mul_f32_e32 v179, v199, v199
	v_mul_f32_e32 v202, v201, v201
	v_mul_f32_e32 v203, v119, v119
	v_cvt_pk_bf16_f32 v114, v198, v199
	v_cvt_pk_bf16_f32 v115, v200, v201
	v_cvt_pk_bf16_f32 v116, v118, v119
	v_cvt_pk_fp8_f32 v214, v198, v199
	v_cvt_pk_fp8_f32 v215, v118, v119
	v_mul_f32_e32 v119, v127, v127
	v_mul_f32_e32 v199, v129, v129
	v_pk_add_f32 v[120:121], v[120:121], v[204:205]
	v_pk_add_f32 v[124:125], v[124:125], v[212:213]
	v_cvt_pk_bf16_f32 v117, v120, v121
	v_mul_f32_e32 v205, v123, v123
	v_fmac_f32_e32 v179, v198, v198
	v_fmac_f32_e32 v202, v200, v200
	v_fmac_f32_e32 v119, v126, v126
	v_fmac_f32_e32 v199, v128, v128
	v_mul_f32_e32 v204, v121, v121
	v_mul_f32_e32 v206, v125, v125
	v_fmac_f32_e32 v203, v118, v118
	global_store_dwordx4 v[218:219], v[114:117], off
	v_fmac_f32_e32 v205, v122, v122
	v_add_f32_e32 v118, v119, v199
	v_add_f32_e32 v117, v179, v202
	v_fmac_f32_e32 v204, v120, v120
	v_fmac_f32_e32 v206, v124, v124
	v_add_f32_e32 v117, v117, v203
	v_add_f32_e32 v118, v118, v205
	v_add_f32_e32 v117, v204, v117
	v_add_f32_e32 v118, v206, v118
	v_and_b32_e32 v119, 64, v197
	v_add_f32_e32 v118, v117, v118
	v_xor_b32_e32 v117, 16, v197
	v_add_u32_e32 v119, 64, v119
	v_cmp_lt_i32_e64 s[2:3], v117, v119
	v_cvt_pk_bf16_f32 v114, v126, v127
	v_cvt_pk_bf16_f32 v115, v128, v129
	v_cvt_pk_bf16_f32 v116, v122, v123
	v_cvt_pk_fp8_f32 v217, v122, v123
	v_cvt_pk_fp8_f32 v215, v120, v121 op_sel:[0,0,1]
	v_cndmask_b32_e64 v117, v197, v117, s[2:3]
	v_lshlrev_b32_e32 v122, 2, v117
	ds_bpermute_b32 v120, v122, v118
	v_cvt_pk_bf16_f32 v117, v124, v125
	global_store_dwordx4 v[218:219], v[114:117], off offset:16
	v_cvt_pk_fp8_f32 v216, v126, v127
	v_cvt_pk_fp8_f32 v214, v200, v201 op_sel:[0,0,1]
	v_xor_b32_e32 v115, 32, v197
	v_cmp_lt_i32_e64 s[2:3], v115, v119
	s_waitcnt lgkmcnt(0)
	v_add_f32_e32 v114, v118, v120
	v_cvt_pk_fp8_f32 v216, v128, v129 op_sel:[0,0,1]
	v_cndmask_b32_e64 v115, v197, v115, s[2:3]
	v_lshlrev_b32_e32 v123, 2, v115
	ds_bpermute_b32 v115, v123, v114
	v_cvt_pk_fp8_f32 v217, v124, v125 op_sel:[0,0,1]
	v_lshlrev_b64 v[116:117], 10, v[182:183]
	v_lshl_add_u64 v[116:117], s[28:29], 0, v[116:117]
	v_lshl_add_u64 v[116:117], v[116:117], 0, v[180:181]
	global_store_dwordx4 v[116:117], v[214:217], off
	s_and_saveexec_b64 s[2:3], vcc
	s_cbranch_execz .LBB0_556
	v_lshlrev_b64 v[116:117], 6, v[182:183]
	v_lshl_add_u64 v[116:117], s[26:27], 0, v[116:117]
	v_lshl_add_u64 v[116:117], s[34:35], 2, v[116:117]
	s_lshl_b32 s20, s7, 2
	v_lshl_add_u64 v[116:117], v[116:117], 0, s[20:21]
	s_waitcnt lgkmcnt(0)
	v_add_f32_e32 v114, v114, v115
	global_store_dword v[116:117], v114, off
; __device__ __forceinline__ unsigned cvt_pk_bf16(float lo, float hi) { unsigned r; asm volatile("v_cvt_pk_bf16_f32 %0, %1, %2" : "=v"(r) : "v"(lo), "v"(hi)); return r; }
;     __device__ __forceinline__ void operator()(const f32x4 (&acc)[2][2][4][2], const pg8::Unit& u, int wr, int wc, int fr, int fq) const {
;         const int row0 = u.pm * 256 + wr * 64 + fr, col0 = u.pn * 256 + wc * 64 + 16 * fq;
; #pragma unroll
;         for (int ai = 0; ai < 2; ++ai) {
;             f32x4 b0[4][2], b1[4][2];
; #pragma unroll
;             for (int m = 0; m < 4; ++m)
; #pragma unroll
;                 for (int bj = 0; bj < 2; ++bj) { const size_t off = (size_t)(row0 + ai * 128 + m * 16) * D + col0 + bj * 8;
;                     if (BASE_F32) { b0[m][bj] = *(const f32x4*)((const float*)base + off); b1[m][bj] = *(const f32x4*)((const float*)base + off + 4); }
;                     else { const u32x4 w = *(const u32x4*)((const bf16*)base + off); b0[m][bj] = (f32x4){bflo(w.x), bfhi(w.x), bflo(w.y), bfhi(w.y)}; b1[m][bj] = (f32x4){bflo(w.z), bfhi(w.z), bflo(w.w), bfhi(w.w)}; } }
;             asm volatile("" ::: "memory");
; #pragma unroll
;             for (int m = 0; m < 4; ++m) { const int row = row0 + ai * 128 + m * 16; float ss = 0.f;
;                 u32x4 q;
; #pragma unroll
;                 for (int bj = 0; bj < 2; ++bj) { const size_t off = (size_t)row * D + col0 + bj * 8;
;                     const float asc = BASE_F32 ? 1.0f : (1.0f / 256.0f);
;                     const f32x4 v0 = acc[ai][bj][m][0] * asc + b0[m][bj], v1 = acc[ai][bj][m][1] * asc + b1[m][bj];
;                     ss += (v0[0] * v0[0] + v0[1] * v0[1]) + (v0[2] * v0[2] + v0[3] * v0[3]) + (v1[0] * v1[0] + v1[1] * v1[1]) + (v1[2] * v1[2] + v1[3] * v1[3]);
;                     u32x4 w; w.x = cvt_pk_bf16(v0[0], v0[1]); w.y = cvt_pk_bf16(v0[2], v0[3]); w.z = cvt_pk_bf16(v1[0], v1[1]); w.w = cvt_pk_bf16(v1[2], v1[3]);
;                     *(u32x4*)(out + off) = w;
;                     if (BASE_F32) { const unsigned qa = pk4_fp8(v0[0], v0[1], v0[2], v0[3]), qb = pk4_fp8(v1[0], v1[1], v1[2], v1[3]); if (bj == 0) { q.x = qa; q.y = qb; } else { q.z = qa; q.w = qb; } } }
;                 if (BASE_F32) *(u32x4*)(q8 + (size_t)row * D + col0) = q;
;                 ss += __shfl_xor(ss, 16); ss += __shfl_xor(ss, 32);
;                 if (fq == 0) ssq[(size_t)row * 16 + u.pn * 4 + wc] = ss; }
.LBB0_556:
	s_or_b64 exec, exec, s[2:3]
	s_waitcnt vmcnt(11)
	v_pk_add_f32 v[112:113], v[112:113], v[176:177]
	v_pk_add_f32 v[116:117], v[110:111], v[174:175]
	v_pk_add_f32 v[120:121], v[106:107], v[170:171]
	v_mul_f32_e32 v106, v117, v117
	v_mul_f32_e32 v107, v113, v113
	v_fmac_f32_e32 v106, v116, v116
	v_fmac_f32_e32 v107, v112, v112
	v_add_f32_e32 v106, v106, v107
	v_mul_f32_e32 v107, v121, v121
	v_pk_add_f32 v[118:119], v[108:109], v[172:173]
	v_fmac_f32_e32 v107, v120, v120
	s_waitcnt lgkmcnt(0)
	v_lshlrev_b64 v[114:115], 11, v[190:191]
	v_add_f32_e32 v106, v106, v107
	v_mul_f32_e32 v107, v119, v119
	v_fmac_f32_e32 v107, v118, v118
	v_lshl_add_u64 v[114:115], s[24:25], 0, v[114:115]
	v_add_f32_e32 v124, v107, v106
	v_cvt_pk_bf16_f32 v106, v116, v117
	v_cvt_pk_bf16_f32 v107, v112, v113
	v_cvt_pk_bf16_f32 v108, v120, v121
	v_cvt_pk_bf16_f32 v109, v118, v119
	v_lshl_add_u64 v[114:115], v[180:181], 1, v[114:115]
	v_pk_add_f32 v[104:105], v[104:105], v[168:169]
	v_pk_add_f32 v[102:103], v[102:103], v[166:167]
	global_store_dwordx4 v[114:115], v[106:109], off
	v_cvt_pk_fp8_f32 v110, v116, v117
	v_pk_add_f32 v[108:109], v[98:99], v[162:163]
	v_mul_f32_e32 v98, v103, v103
	v_mul_f32_e32 v99, v105, v105
	v_fmac_f32_e32 v98, v102, v102
	v_fmac_f32_e32 v99, v104, v104
	v_add_f32_e32 v98, v98, v99
	v_mul_f32_e32 v99, v109, v109
	v_pk_add_f32 v[106:107], v[100:101], v[164:165]
	v_fmac_f32_e32 v99, v108, v108
	v_add_f32_e32 v98, v98, v99
	v_mul_f32_e32 v99, v107, v107
	v_fmac_f32_e32 v99, v106, v106
	v_add_f32_e32 v98, v99, v98
	v_cvt_pk_fp8_f32 v110, v112, v113 op_sel:[0,0,1]
	v_add_f32_e32 v116, v124, v98
	v_cvt_pk_bf16_f32 v98, v102, v103
	v_cvt_pk_fp8_f32 v112, v102, v103
	ds_bpermute_b32 v102, v122, v116
	v_cvt_pk_fp8_f32 v111, v120, v121
	v_cvt_pk_fp8_f32 v113, v108, v109
	v_cvt_pk_bf16_f32 v99, v104, v105
	v_cvt_pk_bf16_f32 v100, v108, v109
	v_cvt_pk_bf16_f32 v101, v106, v107
	global_store_dwordx4 v[114:115], v[98:101], off offset:16
	v_cvt_pk_fp8_f32 v111, v118, v119 op_sel:[0,0,1]
	v_cvt_pk_fp8_f32 v112, v104, v105 op_sel:[0,0,1]
	s_waitcnt lgkmcnt(0)
	v_add_f32_e32 v98, v116, v102
	ds_bpermute_b32 v99, v123, v98
	v_cvt_pk_fp8_f32 v113, v106, v107 op_sel:[0,0,1]
	v_lshlrev_b64 v[100:101], 10, v[190:191]
	v_lshl_add_u64 v[100:101], s[28:29], 0, v[100:101]
	v_lshl_add_u64 v[100:101], v[100:101], 0, v[180:181]
	global_store_dwordx4 v[100:101], v[110:113], off
	s_and_saveexec_b64 s[2:3], vcc
	s_cbranch_execz .LBB0_558
	v_lshlrev_b64 v[100:101], 6, v[190:191]
	v_lshl_add_u64 v[100:101], s[26:27], 0, v[100:101]
	v_lshl_add_u64 v[100:101], s[34:35], 2, v[100:101]
	s_lshl_b32 s20, s7, 2
	v_lshl_add_u64 v[100:101], v[100:101], 0, s[20:21]
	s_waitcnt lgkmcnt(0)
	v_add_f32_e32 v98, v98, v99
	global_store_dword v[100:101], v98, off
.LBB0_558:
	s_or_b64 exec, exec, s[2:3]
	s_waitcnt vmcnt(10)
	v_pk_add_f32 v[96:97], v[96:97], v[160:161]
	v_pk_add_f32 v[100:101], v[94:95], v[158:159]
	v_pk_add_f32 v[104:105], v[90:91], v[154:155]
	v_mul_f32_e32 v90, v101, v101
	v_mul_f32_e32 v91, v97, v97
	v_fmac_f32_e32 v90, v100, v100
	v_fmac_f32_e32 v91, v96, v96
	v_add_f32_e32 v90, v90, v91
	v_mul_f32_e32 v91, v105, v105
	v_pk_add_f32 v[102:103], v[92:93], v[156:157]
	v_fmac_f32_e32 v91, v104, v104
	s_waitcnt lgkmcnt(0)
	v_lshlrev_b64 v[98:99], 11, v[188:189]
	v_add_f32_e32 v90, v90, v91
	v_mul_f32_e32 v91, v103, v103
	v_fmac_f32_e32 v91, v102, v102
	v_lshl_add_u64 v[98:99], s[24:25], 0, v[98:99]
	v_add_f32_e32 v106, v91, v90
	v_cvt_pk_bf16_f32 v90, v100, v101
	v_cvt_pk_bf16_f32 v91, v96, v97
	v_cvt_pk_bf16_f32 v92, v104, v105
	v_cvt_pk_bf16_f32 v93, v102, v103
	v_lshl_add_u64 v[98:99], v[180:181], 1, v[98:99]
	v_pk_add_f32 v[88:89], v[88:89], v[152:153]
	v_pk_add_f32 v[86:87], v[86:87], v[150:151]
	global_store_dwordx4 v[98:99], v[90:93], off
	v_cvt_pk_fp8_f32 v94, v100, v101
	v_pk_add_f32 v[92:93], v[82:83], v[146:147]
	v_mul_f32_e32 v82, v87, v87
	v_mul_f32_e32 v83, v89, v89
	v_fmac_f32_e32 v82, v86, v86
	v_fmac_f32_e32 v83, v88, v88
	v_add_f32_e32 v82, v82, v83
	v_mul_f32_e32 v83, v93, v93
	v_pk_add_f32 v[90:91], v[84:85], v[148:149]
	v_fmac_f32_e32 v83, v92, v92
	v_add_f32_e32 v82, v82, v83
	v_mul_f32_e32 v83, v91, v91
	v_fmac_f32_e32 v83, v90, v90
	v_add_f32_e32 v82, v83, v82
	v_cvt_pk_fp8_f32 v94, v96, v97 op_sel:[0,0,1]
	v_add_f32_e32 v100, v106, v82
	v_cvt_pk_bf16_f32 v82, v86, v87
	v_cvt_pk_fp8_f32 v96, v86, v87
	ds_bpermute_b32 v86, v122, v100
	v_cvt_pk_fp8_f32 v95, v104, v105
	v_cvt_pk_fp8_f32 v97, v92, v93
	v_cvt_pk_bf16_f32 v83, v88, v89
	v_cvt_pk_bf16_f32 v84, v92, v93
	v_cvt_pk_bf16_f32 v85, v90, v91
	global_store_dwordx4 v[98:99], v[82:85], off offset:16
	v_cvt_pk_fp8_f32 v95, v102, v103 op_sel:[0,0,1]
	v_cvt_pk_fp8_f32 v96, v88, v89 op_sel:[0,0,1]
	s_waitcnt lgkmcnt(0)
	v_add_f32_e32 v82, v100, v86
	ds_bpermute_b32 v83, v123, v82
	v_cvt_pk_fp8_f32 v97, v90, v91 op_sel:[0,0,1]
	v_lshlrev_b64 v[84:85], 10, v[188:189]
	v_lshl_add_u64 v[84:85], s[28:29], 0, v[84:85]
	v_lshl_add_u64 v[84:85], v[84:85], 0, v[180:181]
	global_store_dwordx4 v[84:85], v[94:97], off
	s_and_saveexec_b64 s[2:3], vcc
	s_cbranch_execz .LBB0_560
	v_lshlrev_b64 v[84:85], 6, v[188:189]
	v_lshl_add_u64 v[84:85], s[26:27], 0, v[84:85]
	v_lshl_add_u64 v[84:85], s[34:35], 2, v[84:85]
	s_lshl_b32 s20, s7, 2
	v_lshl_add_u64 v[84:85], v[84:85], 0, s[20:21]
	s_waitcnt lgkmcnt(0)
	v_add_f32_e32 v82, v82, v83
	global_store_dword v[84:85], v82, off
; __device__ __forceinline__ unsigned cvt_pk_bf16(float lo, float hi) { unsigned r; asm volatile("v_cvt_pk_bf16_f32 %0, %1, %2" : "=v"(r) : "v"(lo), "v"(hi)); return r; }
;     __device__ __forceinline__ void operator()(const f32x4 (&acc)[2][2][4][2], const pg8::Unit& u, int wr, int wc, int fr, int fq) const {
;         const int row0 = u.pm * 256 + wr * 64 + fr, col0 = u.pn * 256 + wc * 64 + 16 * fq;
; #pragma unroll
;         for (int ai = 0; ai < 2; ++ai) {
;             f32x4 b0[4][2], b1[4][2];
; #pragma unroll
;             for (int m = 0; m < 4; ++m)
; #pragma unroll
;                 for (int bj = 0; bj < 2; ++bj) { const size_t off = (size_t)(row0 + ai * 128 + m * 16) * D + col0 + bj * 8;
;                     if (BASE_F32) { b0[m][bj] = *(const f32x4*)((const float*)base + off); b1[m][bj] = *(const f32x4*)((const float*)base + off + 4); }
;                     else { const u32x4 w = *(const u32x4*)((const bf16*)base + off); b0[m][bj] = (f32x4){bflo(w.x), bfhi(w.x), bflo(w.y), bfhi(w.y)}; b1[m][bj] = (f32x4){bflo(w.z), bfhi(w.z), bflo(w.w), bfhi(w.w)}; } }
;             asm volatile("" ::: "memory");
; #pragma unroll
;             for (int m = 0; m < 4; ++m) { const int row = row0 + ai * 128 + m * 16; float ss = 0.f;
;                 u32x4 q;
; #pragma unroll
;                 for (int bj = 0; bj < 2; ++bj) { const size_t off = (size_t)row * D + col0 + bj * 8;
;                     const float asc = BASE_F32 ? 1.0f : (1.0f / 256.0f);
;                     const f32x4 v0 = acc[ai][bj][m][0] * asc + b0[m][bj], v1 = acc[ai][bj][m][1] * asc + b1[m][bj];
;                     ss += (v0[0] * v0[0] + v0[1] * v0[1]) + (v0[2] * v0[2] + v0[3] * v0[3]) + (v1[0] * v1[0] + v1[1] * v1[1]) + (v1[2] * v1[2] + v1[3] * v1[3]);
;                     u32x4 w; w.x = cvt_pk_bf16(v0[0], v0[1]); w.y = cvt_pk_bf16(v0[2], v0[3]); w.z = cvt_pk_bf16(v1[0], v1[1]); w.w = cvt_pk_bf16(v1[2], v1[3]);
;                     *(u32x4*)(out + off) = w;
;                     if (BASE_F32) { const unsigned qa = pk4_fp8(v0[0], v0[1], v0[2], v0[3]), qb = pk4_fp8(v1[0], v1[1], v1[2], v1[3]); if (bj == 0) { q.x = qa; q.y = qb; } else { q.z = qa; q.w = qb; } } }
;                 if (BASE_F32) *(u32x4*)(q8 + (size_t)row * D + col0) = q;
;                 ss += __shfl_xor(ss, 16); ss += __shfl_xor(ss, 32);
;                 if (fq == 0) ssq[(size_t)row * 16 + u.pn * 4 + wc] = ss; }
.LBB0_560:
	s_or_b64 exec, exec, s[2:3]
	s_waitcnt vmcnt(9)
	v_pk_add_f32 v[80:81], v[80:81], v[144:145]
	v_pk_add_f32 v[84:85], v[78:79], v[142:143]
	v_pk_add_f32 v[88:89], v[74:75], v[138:139]
	v_mul_f32_e32 v74, v85, v85
	v_mul_f32_e32 v75, v81, v81
	v_fmac_f32_e32 v74, v84, v84
	v_fmac_f32_e32 v75, v80, v80
	v_add_f32_e32 v74, v74, v75
	v_mul_f32_e32 v75, v89, v89
	v_pk_add_f32 v[86:87], v[76:77], v[140:141]
	v_fmac_f32_e32 v75, v88, v88
	s_waitcnt lgkmcnt(0)
	v_lshlrev_b64 v[82:83], 11, v[186:187]
	v_add_f32_e32 v74, v74, v75
	v_mul_f32_e32 v75, v87, v87
	v_fmac_f32_e32 v75, v86, v86
	v_lshl_add_u64 v[82:83], s[24:25], 0, v[82:83]
	v_add_f32_e32 v90, v75, v74
	v_cvt_pk_bf16_f32 v74, v84, v85
	v_cvt_pk_bf16_f32 v75, v80, v81
	v_cvt_pk_bf16_f32 v76, v88, v89
	v_cvt_pk_bf16_f32 v77, v86, v87
	v_lshl_add_u64 v[82:83], v[180:181], 1, v[82:83]
	v_pk_add_f32 v[72:73], v[72:73], v[136:137]
	v_pk_add_f32 v[70:71], v[70:71], v[134:135]
	global_store_dwordx4 v[82:83], v[74:77], off
	v_cvt_pk_fp8_f32 v78, v84, v85
	v_pk_add_f32 v[76:77], v[66:67], v[130:131]
	v_mul_f32_e32 v66, v71, v71
	v_mul_f32_e32 v67, v73, v73
	v_fmac_f32_e32 v66, v70, v70
	v_fmac_f32_e32 v67, v72, v72
	v_add_f32_e32 v66, v66, v67
	v_mul_f32_e32 v67, v77, v77
	v_pk_add_f32 v[74:75], v[68:69], v[132:133]
	v_fmac_f32_e32 v67, v76, v76
	v_add_f32_e32 v66, v66, v67
	v_mul_f32_e32 v67, v75, v75
	v_fmac_f32_e32 v67, v74, v74
	v_add_f32_e32 v66, v67, v66
	v_cvt_pk_fp8_f32 v78, v80, v81 op_sel:[0,0,1]
	v_add_f32_e32 v84, v90, v66
	v_cvt_pk_bf16_f32 v66, v70, v71
	v_cvt_pk_fp8_f32 v80, v70, v71
	ds_bpermute_b32 v70, v122, v84
	v_cvt_pk_fp8_f32 v79, v88, v89
	v_cvt_pk_fp8_f32 v81, v76, v77
	v_cvt_pk_bf16_f32 v67, v72, v73
	v_cvt_pk_bf16_f32 v68, v76, v77
	v_cvt_pk_bf16_f32 v69, v74, v75
	global_store_dwordx4 v[82:83], v[66:69], off offset:16
	v_cvt_pk_fp8_f32 v79, v86, v87 op_sel:[0,0,1]
	v_cvt_pk_fp8_f32 v80, v72, v73 op_sel:[0,0,1]
	s_waitcnt lgkmcnt(0)
	v_add_f32_e32 v66, v84, v70
	ds_bpermute_b32 v67, v123, v66
	v_cvt_pk_fp8_f32 v81, v74, v75 op_sel:[0,0,1]
	v_lshlrev_b64 v[68:69], 10, v[186:187]
	v_lshl_add_u64 v[68:69], s[28:29], 0, v[68:69]
	v_lshl_add_u64 v[68:69], v[68:69], 0, v[180:181]
	global_store_dwordx4 v[68:69], v[78:81], off
	s_and_saveexec_b64 s[2:3], vcc
	s_cbranch_execz .LBB0_562
	v_lshlrev_b64 v[68:69], 6, v[186:187]
	v_lshl_add_u64 v[68:69], s[26:27], 0, v[68:69]
	v_lshl_add_u64 v[68:69], s[34:35], 2, v[68:69]
	s_lshl_b32 s20, s7, 2
	v_lshl_add_u64 v[68:69], v[68:69], 0, s[20:21]
	s_waitcnt lgkmcnt(0)
	v_add_f32_e32 v66, v66, v67
	global_store_dword v[68:69], v66, off
.LBB0_562:
	s_or_b64 exec, exec, s[2:3]
	v_add_u32_e32 v120, 0x80, v182
	v_ashrrev_i32_e32 v121, 31, v120
	s_waitcnt lgkmcnt(0)
	v_lshlrev_b64 v[66:67], 12, v[120:121]
	v_lshl_add_u64 v[66:67], v[184:185], 0, v[66:67]
	global_load_dwordx4 v[124:127], v[66:67], off
	global_load_dwordx4 v[128:131], v[66:67], off offset:16
	global_load_dwordx4 v[132:135], v[66:67], off offset:32
	global_load_dwordx4 v[136:139], v[66:67], off offset:48
	v_add_u32_e32 v118, 0x90, v182
	v_add_u32_e32 v116, 0xa0, v182
	v_add_u32_e32 v114, 0xb0, v182
	v_ashrrev_i32_e32 v119, 31, v118
	v_ashrrev_i32_e32 v117, 31, v116
	v_ashrrev_i32_e32 v115, 31, v114
	v_lshlrev_b64 v[66:67], 12, v[118:119]
	v_lshlrev_b64 v[68:69], 12, v[116:117]
	v_lshlrev_b64 v[70:71], 12, v[114:115]
	v_lshl_add_u64 v[66:67], v[184:185], 0, v[66:67]
	v_lshl_add_u64 v[68:69], v[184:185], 0, v[68:69]
	v_lshl_add_u64 v[78:79], v[184:185], 0, v[70:71]
	global_load_dwordx4 v[98:101], v[66:67], off offset:48
	global_load_dwordx4 v[102:105], v[66:67], off offset:32
	global_load_dwordx4 v[106:109], v[66:67], off offset:16
	global_load_dwordx4 v[110:113], v[66:67], off
	global_load_dwordx4 v[82:85], v[68:69], off offset:48
	global_load_dwordx4 v[86:89], v[68:69], off offset:32
	global_load_dwordx4 v[90:93], v[68:69], off offset:16
	global_load_dwordx4 v[94:97], v[68:69], off
	s_nop 0
	global_load_dwordx4 v[66:69], v[78:79], off offset:48
	global_load_dwordx4 v[70:73], v[78:79], off offset:32
	global_load_dwordx4 v[74:77], v[78:79], off offset:16
	s_nop 0
	global_load_dwordx4 v[78:81], v[78:79], off
	v_lshlrev_b64 v[144:145], 11, v[120:121]
	v_lshl_add_u64 v[144:145], s[24:25], 0, v[144:145]
	v_lshl_add_u64 v[144:145], v[180:181], 1, v[144:145]
	s_waitcnt vmcnt(15)
	v_pk_add_f32 v[126:127], v[52:53], v[126:127]
	v_pk_add_f32 v[124:125], v[50:51], v[124:125]
	s_waitcnt vmcnt(14)
	v_pk_add_f32 v[54:55], v[54:55], v[128:129]
	s_waitcnt vmcnt(13)
	v_pk_add_f32 v[60:61], v[60:61], v[134:135]
	v_pk_add_f32 v[58:59], v[58:59], v[132:133]
	v_pk_add_f32 v[56:57], v[56:57], v[130:131]
	s_waitcnt vmcnt(12)
	v_pk_add_f32 v[62:63], v[62:63], v[136:137]
	v_mul_f32_e32 v128, v125, v125
	v_mul_f32_e32 v129, v127, v127
	v_mul_f32_e32 v130, v55, v55
	v_cvt_pk_bf16_f32 v50, v124, v125
	v_cvt_pk_bf16_f32 v51, v126, v127
	v_cvt_pk_bf16_f32 v52, v54, v55
	v_cvt_pk_fp8_f32 v140, v124, v125
	v_cvt_pk_fp8_f32 v141, v54, v55
	v_mul_f32_e32 v55, v59, v59
	v_mul_f32_e32 v125, v61, v61
	v_pk_add_f32 v[64:65], v[64:65], v[138:139]
	v_cvt_pk_bf16_f32 v53, v56, v57
	v_mul_f32_e32 v132, v63, v63
	v_fmac_f32_e32 v128, v124, v124
	v_fmac_f32_e32 v129, v126, v126
	v_fmac_f32_e32 v55, v58, v58
	v_fmac_f32_e32 v125, v60, v60
	v_mul_f32_e32 v131, v57, v57
	v_mul_f32_e32 v133, v65, v65
	v_fmac_f32_e32 v130, v54, v54
	global_store_dwordx4 v[144:145], v[50:53], off
	v_fmac_f32_e32 v132, v62, v62
	v_add_f32_e32 v54, v55, v125
	v_add_f32_e32 v53, v128, v129
	v_fmac_f32_e32 v131, v56, v56
	v_fmac_f32_e32 v133, v64, v64
	v_add_f32_e32 v53, v53, v130
	v_add_f32_e32 v54, v54, v132
	v_add_f32_e32 v53, v131, v53
	v_add_f32_e32 v54, v133, v54
	v_add_f32_e32 v54, v53, v54
	ds_bpermute_b32 v55, v122, v54
	v_cvt_pk_fp8_f32 v142, v58, v59
	v_cvt_pk_fp8_f32 v143, v62, v63
	v_cvt_pk_bf16_f32 v50, v58, v59
	v_cvt_pk_bf16_f32 v51, v60, v61
	v_cvt_pk_bf16_f32 v52, v62, v63
	v_cvt_pk_bf16_f32 v53, v64, v65
	global_store_dwordx4 v[144:145], v[50:53], off offset:16
	v_cvt_pk_fp8_f32 v140, v126, v127 op_sel:[0,0,1]
	v_cvt_pk_fp8_f32 v141, v56, v57 op_sel:[0,0,1]
	s_waitcnt lgkmcnt(0)
	v_add_f32_e32 v50, v54, v55
	ds_bpermute_b32 v51, v123, v50
	v_cvt_pk_fp8_f32 v142, v60, v61 op_sel:[0,0,1]
	v_cvt_pk_fp8_f32 v143, v64, v65 op_sel:[0,0,1]
	v_lshlrev_b64 v[52:53], 10, v[120:121]
	v_lshl_add_u64 v[52:53], s[28:29], 0, v[52:53]
	v_lshl_add_u64 v[52:53], v[52:53], 0, v[180:181]
	global_store_dwordx4 v[52:53], v[140:143], off
	s_and_saveexec_b64 s[2:3], vcc
	s_cbranch_execz .LBB0_564
	v_lshlrev_b64 v[52:53], 6, v[120:121]
	v_lshl_add_u64 v[52:53], s[26:27], 0, v[52:53]
	v_lshl_add_u64 v[52:53], s[34:35], 2, v[52:53]
	s_lshl_b32 s20, s7, 2
	v_lshl_add_u64 v[52:53], v[52:53], 0, s[20:21]
	s_waitcnt lgkmcnt(0)
	v_add_f32_e32 v50, v50, v51
	global_store_dword v[52:53], v50, off
; __device__ __forceinline__ unsigned cvt_pk_bf16(float lo, float hi) { unsigned r; asm volatile("v_cvt_pk_bf16_f32 %0, %1, %2" : "=v"(r) : "v"(lo), "v"(hi)); return r; }
;     __device__ __forceinline__ void operator()(const f32x4 (&acc)[2][2][4][2], const pg8::Unit& u, int wr, int wc, int fr, int fq) const {
;         const int row0 = u.pm * 256 + wr * 64 + fr, col0 = u.pn * 256 + wc * 64 + 16 * fq;
; #pragma unroll
;         for (int ai = 0; ai < 2; ++ai) {
;             f32x4 b0[4][2], b1[4][2];
; #pragma unroll
;             for (int m = 0; m < 4; ++m)
; #pragma unroll
;                 for (int bj = 0; bj < 2; ++bj) { const size_t off = (size_t)(row0 + ai * 128 + m * 16) * D + col0 + bj * 8;
;                     if (BASE_F32) { b0[m][bj] = *(const f32x4*)((const float*)base + off); b1[m][bj] = *(const f32x4*)((const float*)base + off + 4); }
;                     else { const u32x4 w = *(const u32x4*)((const bf16*)base + off); b0[m][bj] = (f32x4){bflo(w.x), bfhi(w.x), bflo(w.y), bfhi(w.y)}; b1[m][bj] = (f32x4){bflo(w.z), bfhi(w.z), bflo(w.w), bfhi(w.w)}; } }
;             asm volatile("" ::: "memory");
; #pragma unroll
;             for (int m = 0; m < 4; ++m) { const int row = row0 + ai * 128 + m * 16; float ss = 0.f;
;                 u32x4 q;
; #pragma unroll
;                 for (int bj = 0; bj < 2; ++bj) { const size_t off = (size_t)row * D + col0 + bj * 8;
;                     const float asc = BASE_F32 ? 1.0f : (1.0f / 256.0f);
;                     const f32x4 v0 = acc[ai][bj][m][0] * asc + b0[m][bj], v1 = acc[ai][bj][m][1] * asc + b1[m][bj];
;                     ss += (v0[0] * v0[0] + v0[1] * v0[1]) + (v0[2] * v0[2] + v0[3] * v0[3]) + (v1[0] * v1[0] + v1[1] * v1[1]) + (v1[2] * v1[2] + v1[3] * v1[3]);
;                     u32x4 w; w.x = cvt_pk_bf16(v0[0], v0[1]); w.y = cvt_pk_bf16(v0[2], v0[3]); w.z = cvt_pk_bf16(v1[0], v1[1]); w.w = cvt_pk_bf16(v1[2], v1[3]);
;                     *(u32x4*)(out + off) = w;
;                     if (BASE_F32) { const unsigned qa = pk4_fp8(v0[0], v0[1], v0[2], v0[3]), qb = pk4_fp8(v1[0], v1[1], v1[2], v1[3]); if (bj == 0) { q.x = qa; q.y = qb; } else { q.z = qa; q.w = qb; } } }
;                 if (BASE_F32) *(u32x4*)(q8 + (size_t)row * D + col0) = q;
;                 ss += __shfl_xor(ss, 16); ss += __shfl_xor(ss, 32);
;                 if (fq == 0) ssq[(size_t)row * 16 + u.pn * 4 + wc] = ss; }
.LBB0_564:
	s_or_b64 exec, exec, s[2:3]
	s_waitcnt vmcnt(11)
	v_pk_add_f32 v[48:49], v[48:49], v[112:113]
	v_pk_add_f32 v[52:53], v[46:47], v[110:111]
	v_pk_add_f32 v[56:57], v[42:43], v[106:107]
	v_mul_f32_e32 v42, v53, v53
	v_mul_f32_e32 v43, v49, v49
	v_fmac_f32_e32 v42, v52, v52
	v_fmac_f32_e32 v43, v48, v48
	v_add_f32_e32 v42, v42, v43
	v_mul_f32_e32 v43, v57, v57
	v_pk_add_f32 v[54:55], v[44:45], v[108:109]
	v_fmac_f32_e32 v43, v56, v56
	s_waitcnt lgkmcnt(0)
	v_lshlrev_b64 v[50:51], 11, v[118:119]
	v_add_f32_e32 v42, v42, v43
	v_mul_f32_e32 v43, v55, v55
	v_fmac_f32_e32 v43, v54, v54
	v_lshl_add_u64 v[50:51], s[24:25], 0, v[50:51]
	v_add_f32_e32 v58, v43, v42
	v_cvt_pk_bf16_f32 v42, v52, v53
	v_cvt_pk_bf16_f32 v43, v48, v49
	v_cvt_pk_bf16_f32 v44, v56, v57
	v_cvt_pk_bf16_f32 v45, v54, v55
	v_lshl_add_u64 v[50:51], v[180:181], 1, v[50:51]
	v_pk_add_f32 v[40:41], v[40:41], v[104:105]
	v_pk_add_f32 v[38:39], v[38:39], v[102:103]
	global_store_dwordx4 v[50:51], v[42:45], off
	v_cvt_pk_fp8_f32 v46, v52, v53
	v_pk_add_f32 v[44:45], v[34:35], v[98:99]
	v_mul_f32_e32 v34, v39, v39
	v_mul_f32_e32 v35, v41, v41
	v_fmac_f32_e32 v34, v38, v38
	v_fmac_f32_e32 v35, v40, v40
	v_add_f32_e32 v34, v34, v35
	v_mul_f32_e32 v35, v45, v45
	v_pk_add_f32 v[42:43], v[36:37], v[100:101]
	v_fmac_f32_e32 v35, v44, v44
	v_add_f32_e32 v34, v34, v35
	v_mul_f32_e32 v35, v43, v43
	v_fmac_f32_e32 v35, v42, v42
	v_add_f32_e32 v34, v35, v34
	v_cvt_pk_fp8_f32 v46, v48, v49 op_sel:[0,0,1]
	v_add_f32_e32 v52, v58, v34
	v_cvt_pk_bf16_f32 v34, v38, v39
	v_cvt_pk_fp8_f32 v48, v38, v39
	ds_bpermute_b32 v38, v122, v52
	v_cvt_pk_fp8_f32 v47, v56, v57
	v_cvt_pk_fp8_f32 v49, v44, v45
	v_cvt_pk_bf16_f32 v35, v40, v41
	v_cvt_pk_bf16_f32 v36, v44, v45
	v_cvt_pk_bf16_f32 v37, v42, v43
	global_store_dwordx4 v[50:51], v[34:37], off offset:16
	v_cvt_pk_fp8_f32 v47, v54, v55 op_sel:[0,0,1]
	v_cvt_pk_fp8_f32 v48, v40, v41 op_sel:[0,0,1]
	s_waitcnt lgkmcnt(0)
	v_add_f32_e32 v34, v52, v38
	ds_bpermute_b32 v35, v123, v34
	v_cvt_pk_fp8_f32 v49, v42, v43 op_sel:[0,0,1]
	v_lshlrev_b64 v[36:37], 10, v[118:119]
	v_lshl_add_u64 v[36:37], s[28:29], 0, v[36:37]
	v_lshl_add_u64 v[36:37], v[36:37], 0, v[180:181]
	global_store_dwordx4 v[36:37], v[46:49], off
	s_and_saveexec_b64 s[2:3], vcc
	s_cbranch_execz .LBB0_566
	v_lshlrev_b64 v[36:37], 6, v[118:119]
	v_lshl_add_u64 v[36:37], s[26:27], 0, v[36:37]
	v_lshl_add_u64 v[36:37], s[34:35], 2, v[36:37]
	s_lshl_b32 s20, s7, 2
	v_lshl_add_u64 v[36:37], v[36:37], 0, s[20:21]
	s_waitcnt lgkmcnt(0)
	v_add_f32_e32 v34, v34, v35
	global_store_dword v[36:37], v34, off
; __device__ __forceinline__ unsigned cvt_pk_bf16(float lo, float hi) { unsigned r; asm volatile("v_cvt_pk_bf16_f32 %0, %1, %2" : "=v"(r) : "v"(lo), "v"(hi)); return r; }
;     __device__ __forceinline__ void operator()(const f32x4 (&acc)[2][2][4][2], const pg8::Unit& u, int wr, int wc, int fr, int fq) const {
;         const int row0 = u.pm * 256 + wr * 64 + fr, col0 = u.pn * 256 + wc * 64 + 16 * fq;
; #pragma unroll
;         for (int ai = 0; ai < 2; ++ai) {
;             f32x4 b0[4][2], b1[4][2];
; #pragma unroll
;             for (int m = 0; m < 4; ++m)
; #pragma unroll
;                 for (int bj = 0; bj < 2; ++bj) { const size_t off = (size_t)(row0 + ai * 128 + m * 16) * D + col0 + bj * 8;
;                     if (BASE_F32) { b0[m][bj] = *(const f32x4*)((const float*)base + off); b1[m][bj] = *(const f32x4*)((const float*)base + off + 4); }
;                     else { const u32x4 w = *(const u32x4*)((const bf16*)base + off); b0[m][bj] = (f32x4){bflo(w.x), bfhi(w.x), bflo(w.y), bfhi(w.y)}; b1[m][bj] = (f32x4){bflo(w.z), bfhi(w.z), bflo(w.w), bfhi(w.w)}; } }
;             asm volatile("" ::: "memory");
; #pragma unroll
;             for (int m = 0; m < 4; ++m) { const int row = row0 + ai * 128 + m * 16; float ss = 0.f;
;                 u32x4 q;
; #pragma unroll
;                 for (int bj = 0; bj < 2; ++bj) { const size_t off = (size_t)row * D + col0 + bj * 8;
;                     const float asc = BASE_F32 ? 1.0f : (1.0f / 256.0f);
;                     const f32x4 v0 = acc[ai][bj][m][0] * asc + b0[m][bj], v1 = acc[ai][bj][m][1] * asc + b1[m][bj];
;                     ss += (v0[0] * v0[0] + v0[1] * v0[1]) + (v0[2] * v0[2] + v0[3] * v0[3]) + (v1[0] * v1[0] + v1[1] * v1[1]) + (v1[2] * v1[2] + v1[3] * v1[3]);
;                     u32x4 w; w.x = cvt_pk_bf16(v0[0], v0[1]); w.y = cvt_pk_bf16(v0[2], v0[3]); w.z = cvt_pk_bf16(v1[0], v1[1]); w.w = cvt_pk_bf16(v1[2], v1[3]);
;                     *(u32x4*)(out + off) = w;
;                     if (BASE_F32) { const unsigned qa = pk4_fp8(v0[0], v0[1], v0[2], v0[3]), qb = pk4_fp8(v1[0], v1[1], v1[2], v1[3]); if (bj == 0) { q.x = qa; q.y = qb; } else { q.z = qa; q.w = qb; } } }
;                 if (BASE_F32) *(u32x4*)(q8 + (size_t)row * D + col0) = q;
;                 ss += __shfl_xor(ss, 16); ss += __shfl_xor(ss, 32);
;                 if (fq == 0) ssq[(size_t)row * 16 + u.pn * 4 + wc] = ss; }
.LBB0_566:
	s_or_b64 exec, exec, s[2:3]
	s_waitcnt vmcnt(10)
	v_pk_add_f32 v[32:33], v[32:33], v[96:97]
	v_pk_add_f32 v[36:37], v[30:31], v[94:95]
	v_pk_add_f32 v[40:41], v[26:27], v[90:91]
	v_mul_f32_e32 v26, v37, v37
	v_mul_f32_e32 v27, v33, v33
	v_fmac_f32_e32 v26, v36, v36
	v_fmac_f32_e32 v27, v32, v32
	v_add_f32_e32 v26, v26, v27
	v_mul_f32_e32 v27, v41, v41
	v_pk_add_f32 v[38:39], v[28:29], v[92:93]
	v_fmac_f32_e32 v27, v40, v40
	s_waitcnt lgkmcnt(0)
	v_lshlrev_b64 v[34:35], 11, v[116:117]
	v_add_f32_e32 v26, v26, v27
	v_mul_f32_e32 v27, v39, v39
	v_fmac_f32_e32 v27, v38, v38
	v_lshl_add_u64 v[34:35], s[24:25], 0, v[34:35]
	v_add_f32_e32 v42, v27, v26
	v_cvt_pk_bf16_f32 v26, v36, v37
	v_cvt_pk_bf16_f32 v27, v32, v33
	v_cvt_pk_bf16_f32 v28, v40, v41
	v_cvt_pk_bf16_f32 v29, v38, v39
	v_lshl_add_u64 v[34:35], v[180:181], 1, v[34:35]
	v_pk_add_f32 v[24:25], v[24:25], v[88:89]
	v_pk_add_f32 v[22:23], v[22:23], v[86:87]
	global_store_dwordx4 v[34:35], v[26:29], off
	v_cvt_pk_fp8_f32 v30, v36, v37
	v_pk_add_f32 v[28:29], v[18:19], v[82:83]
	v_mul_f32_e32 v18, v23, v23
	v_mul_f32_e32 v19, v25, v25
	v_fmac_f32_e32 v18, v22, v22
	v_fmac_f32_e32 v19, v24, v24
	v_add_f32_e32 v18, v18, v19
	v_mul_f32_e32 v19, v29, v29
	v_pk_add_f32 v[26:27], v[20:21], v[84:85]
	v_fmac_f32_e32 v19, v28, v28
	v_add_f32_e32 v18, v18, v19
	v_mul_f32_e32 v19, v27, v27
	v_fmac_f32_e32 v19, v26, v26
	v_add_f32_e32 v18, v19, v18
	v_cvt_pk_fp8_f32 v30, v32, v33 op_sel:[0,0,1]
	v_add_f32_e32 v36, v42, v18
	v_cvt_pk_bf16_f32 v18, v22, v23
	v_cvt_pk_fp8_f32 v32, v22, v23
	ds_bpermute_b32 v22, v122, v36
	v_cvt_pk_fp8_f32 v31, v40, v41
	v_cvt_pk_fp8_f32 v33, v28, v29
	v_cvt_pk_bf16_f32 v19, v24, v25
	v_cvt_pk_bf16_f32 v20, v28, v29
	v_cvt_pk_bf16_f32 v21, v26, v27
	global_store_dwordx4 v[34:35], v[18:21], off offset:16
	v_cvt_pk_fp8_f32 v31, v38, v39 op_sel:[0,0,1]
	v_cvt_pk_fp8_f32 v32, v24, v25 op_sel:[0,0,1]
	s_waitcnt lgkmcnt(0)
	v_add_f32_e32 v18, v36, v22
	ds_bpermute_b32 v19, v123, v18
	v_cvt_pk_fp8_f32 v33, v26, v27 op_sel:[0,0,1]
	v_lshlrev_b64 v[20:21], 10, v[116:117]
	v_lshl_add_u64 v[20:21], s[28:29], 0, v[20:21]
	v_lshl_add_u64 v[20:21], v[20:21], 0, v[180:181]
	global_store_dwordx4 v[20:21], v[30:33], off
	s_and_saveexec_b64 s[2:3], vcc
	s_cbranch_execz .LBB0_568
	v_lshlrev_b64 v[20:21], 6, v[116:117]
	v_lshl_add_u64 v[20:21], s[26:27], 0, v[20:21]
	v_lshl_add_u64 v[20:21], s[34:35], 2, v[20:21]
	s_lshl_b32 s20, s7, 2
	v_lshl_add_u64 v[20:21], v[20:21], 0, s[20:21]
	s_waitcnt lgkmcnt(0)
	v_add_f32_e32 v18, v18, v19
	global_store_dword v[20:21], v18, off
.LBB0_568:
	s_or_b64 exec, exec, s[2:3]
	s_waitcnt vmcnt(9)
	v_pk_add_f32 v[16:17], v[16:17], v[80:81]
	v_pk_add_f32 v[20:21], v[14:15], v[78:79]
	v_pk_add_f32 v[24:25], v[10:11], v[74:75]
	v_mul_f32_e32 v10, v21, v21
	v_mul_f32_e32 v11, v17, v17
	v_fmac_f32_e32 v10, v20, v20
	v_fmac_f32_e32 v11, v16, v16
	v_add_f32_e32 v10, v10, v11
	v_mul_f32_e32 v11, v25, v25
	v_pk_add_f32 v[22:23], v[12:13], v[76:77]
	v_fmac_f32_e32 v11, v24, v24
	s_waitcnt lgkmcnt(0)
	v_lshlrev_b64 v[18:19], 11, v[114:115]
	v_add_f32_e32 v10, v10, v11
	v_mul_f32_e32 v11, v23, v23
	v_fmac_f32_e32 v11, v22, v22
	v_lshl_add_u64 v[18:19], s[24:25], 0, v[18:19]
	v_add_f32_e32 v26, v11, v10
	v_cvt_pk_bf16_f32 v10, v20, v21
	v_cvt_pk_bf16_f32 v11, v16, v17
	v_cvt_pk_bf16_f32 v12, v24, v25
	v_cvt_pk_bf16_f32 v13, v22, v23
	v_lshl_add_u64 v[18:19], v[180:181], 1, v[18:19]
	v_pk_add_f32 v[8:9], v[8:9], v[72:73]
	v_pk_add_f32 v[6:7], v[6:7], v[70:71]
	global_store_dwordx4 v[18:19], v[10:13], off
	v_cvt_pk_fp8_f32 v14, v20, v21
	v_pk_add_f32 v[12:13], v[2:3], v[66:67]
	v_mul_f32_e32 v2, v7, v7
	v_mul_f32_e32 v3, v9, v9
	v_fmac_f32_e32 v2, v6, v6
	v_fmac_f32_e32 v3, v8, v8
	v_add_f32_e32 v2, v2, v3
	v_mul_f32_e32 v3, v13, v13
	v_pk_add_f32 v[10:11], v[4:5], v[68:69]
	v_fmac_f32_e32 v3, v12, v12
	v_add_f32_e32 v2, v2, v3
	v_mul_f32_e32 v3, v11, v11
	v_fmac_f32_e32 v3, v10, v10
	v_add_f32_e32 v2, v3, v2
	v_cvt_pk_fp8_f32 v14, v16, v17 op_sel:[0,0,1]
	v_add_f32_e32 v20, v26, v2
	v_cvt_pk_bf16_f32 v2, v6, v7
	v_cvt_pk_fp8_f32 v16, v6, v7
	ds_bpermute_b32 v6, v122, v20
	v_cvt_pk_fp8_f32 v15, v24, v25
	v_cvt_pk_fp8_f32 v17, v12, v13
	v_cvt_pk_bf16_f32 v3, v8, v9
	v_cvt_pk_bf16_f32 v4, v12, v13
	v_cvt_pk_bf16_f32 v5, v10, v11
	global_store_dwordx4 v[18:19], v[2:5], off offset:16
	v_cvt_pk_fp8_f32 v15, v22, v23 op_sel:[0,0,1]
	v_cvt_pk_fp8_f32 v16, v8, v9 op_sel:[0,0,1]
	s_waitcnt lgkmcnt(0)
	v_add_f32_e32 v2, v20, v6
	ds_bpermute_b32 v3, v123, v2
	v_cvt_pk_fp8_f32 v17, v10, v11 op_sel:[0,0,1]
	v_lshlrev_b64 v[4:5], 10, v[114:115]
	v_lshl_add_u64 v[4:5], s[28:29], 0, v[4:5]
	v_lshl_add_u64 v[4:5], v[4:5], 0, v[180:181]
	global_store_dwordx4 v[4:5], v[14:17], off
	s_and_saveexec_b64 s[2:3], vcc
	s_cbranch_execz .LBB0_570
	v_lshlrev_b64 v[4:5], 6, v[114:115]
	v_lshl_add_u64 v[4:5], s[26:27], 0, v[4:5]
	v_lshl_add_u64 v[4:5], s[34:35], 2, v[4:5]
	s_lshl_b32 s20, s7, 2
	v_lshl_add_u64 v[4:5], v[4:5], 0, s[20:21]
	s_waitcnt lgkmcnt(0)
	v_add_f32_e32 v2, v2, v3
	global_store_dword v[4:5], v2, off

; #define LAS __attribute__((address_space(3)))
; __device__ __forceinline__ unsigned pk4_fp8(float a, float b, float c, float d) { int w = __builtin_amdgcn_cvt_pk_fp8_f32(a, b, 0, false); w = __builtin_amdgcn_cvt_pk_fp8_f32(c, d, w, true); return (unsigned)w; }
;     __device__ __forceinline__ void operator()(f32x4 (&acc)[2][2][4][2], const pg8::Unit& u, int wr, int wc, int fr, int fq) const {
;     ...
; #pragma unroll
;         for (int ai = 0; ai < 2; ++ai)
; #pragma unroll
;             for (int m = 0; m < 4; ++m) { const int rl = ai * 128 + wr * 64 + m * 16 + fr; const f32x4 q = *(const LAS f32x4*)(xch + 1024 + rl * 4); const float inv = 256.0f / ((q[0] + q[1]) + (q[2] + q[3]));
;                 { const f32x4 v0 = acc[ai][0][m][0] * inv, v1 = acc[ai][0][m][1] * inv, v2 = acc[ai][1][m][0] * inv, v3 = acc[ai][1][m][1] * inv;
;                     *(u32x4*)(out + (size_t)(row0 + ai * 128 + m * 16) * D + col0) = (u32x4){pk4_fp8(v0[0], v0[1], v0[2], v0[3]), pk4_fp8(v1[0], v1[1], v1[2], v1[3]), pk4_fp8(v2[0], v2[1], v2[2], v2[3]), pk4_fp8(v3[0], v3[1], v3[2], v3[3])}; } }
.LBB0_682:
	s_or_b64 exec, exec, s[2:3]
	s_waitcnt lgkmcnt(0)
	s_barrier
	v_add_u32_e32 v112, s39, v205
	ds_read_b128 v[144:147], v112
	v_add_u32_e32 v112, 0x21900, v204
	ds_read_b128 v[148:151], v112
	s_lshl_b32 s4, s15, 8
	s_waitcnt lgkmcnt(1)
	v_mov_b32_e32 v112, v145
	v_mov_b32_e32 v113, v146
	v_mov_b32_e32 v145, v147
	v_pk_add_f32 v[112:113], v[112:113], v[144:145]
	s_nop 0
	v_add_f32_e32 v144, v112, v113
	v_div_scale_f32 v145, s[2:3], v144, v144, s40
	v_rcp_f32_e32 v146, v145
	s_or_b32 s2, s4, s35
	v_lshl_or_b32 v112, v131, 4, s2
	v_ashrrev_i32_e32 v113, 31, v112
	v_fma_f32 v131, -v145, v146, 1.0
	v_fmac_f32_e32 v146, v131, v146
	v_div_scale_f32 v131, vcc, s40, v144, s40
	v_mul_f32_e32 v147, v131, v146
	v_fma_f32 v152, -v145, v147, v131
	v_fmac_f32_e32 v147, v152, v146
	v_fma_f32 v131, -v145, v147, v131
	v_div_fmas_f32 v131, v131, v146, v147
	v_div_fixup_f32 v144, v131, v144, s40
	v_pk_mul_f32 v[138:139], v[138:139], v[144:145] op_sel_hi:[1,0]
	v_pk_mul_f32 v[140:141], v[140:141], v[144:145] op_sel_hi:[1,0]
	v_pk_mul_f32 v[134:135], v[134:135], v[144:145] op_sel_hi:[1,0]
	v_pk_mul_f32 v[136:137], v[136:137], v[144:145] op_sel_hi:[1,0]
	v_pk_mul_f32 v[146:147], v[120:121], v[144:145] op_sel_hi:[1,0]
	v_pk_mul_f32 v[122:123], v[122:123], v[144:145] op_sel_hi:[1,0]
	v_pk_mul_f32 v[152:153], v[164:165], v[144:145] op_sel_hi:[1,0]
	v_pk_mul_f32 v[144:145], v[118:119], v[144:145] op_sel_hi:[1,0]
	v_cvt_pk_fp8_f32 v118, v140, v141
	v_cvt_pk_fp8_f32 v119, v136, v137
	v_cvt_pk_fp8_f32 v120, v122, v123
	v_cvt_pk_fp8_f32 v121, v144, v145
	v_lshlrev_b64 v[122:123], 10, v[132:133]
	s_waitcnt lgkmcnt(0)
	v_mov_b32_e32 v132, v149
	v_mov_b32_e32 v133, v150
	v_mov_b32_e32 v149, v151
	v_pk_add_f32 v[132:133], v[132:133], v[148:149]
	v_cvt_pk_fp8_f32 v118, v138, v139 op_sel:[0,0,1]
	v_add_f32_e32 v131, v132, v133
	v_div_scale_f32 v132, s[2:3], v131, v131, s40
	v_cvt_pk_fp8_f32 v119, v134, v135 op_sel:[0,0,1]
	v_cvt_pk_fp8_f32 v120, v146, v147 op_sel:[0,0,1]
	v_cvt_pk_fp8_f32 v121, v152, v153 op_sel:[0,0,1]
	v_rcp_f32_e32 v133, v132
	v_lshl_add_u64 v[122:123], s[18:19], 0, v[122:123]
	v_lshl_add_u64 v[122:123], v[122:123], 0, v[112:113]
	global_store_dwordx4 v[122:123], v[118:121], off
	s_mov_b64 s[4:5], -1
	s_nop 0
	v_fma_f32 v118, -v132, v133, 1.0
	v_fmac_f32_e32 v133, v118, v133
	v_div_scale_f32 v118, vcc, s40, v131, s40
	v_mul_f32_e32 v119, v118, v133
	v_fma_f32 v120, -v132, v119, v118
	v_fmac_f32_e32 v119, v120, v133
	v_fma_f32 v118, -v132, v119, v118
	v_div_fmas_f32 v118, v118, v133, v119
	v_div_fixup_f32 v118, v118, v131, s40
	v_pk_mul_f32 v[122:123], v[116:117], v[118:119] op_sel_hi:[1,0]
	v_cvt_pk_fp8_f32 v116, v122, v123
	v_pk_mul_f32 v[120:121], v[128:129], v[118:119] op_sel_hi:[1,0]
	v_pk_mul_f32 v[124:125], v[124:125], v[118:119] op_sel_hi:[1,0]
	v_pk_mul_f32 v[126:127], v[126:127], v[118:119] op_sel_hi:[1,0]
	v_pk_mul_f32 v[128:129], v[170:171], v[118:119] op_sel_hi:[1,0]
	v_pk_mul_f32 v[110:111], v[110:111], v[118:119] op_sel_hi:[1,0]
	v_pk_mul_f32 v[132:133], v[174:175], v[118:119] op_sel_hi:[1,0]
	v_pk_mul_f32 v[122:123], v[142:143], v[118:119] op_sel_hi:[1,0]
	v_cvt_pk_fp8_f32 v118, v110, v111
	v_add_u32_e32 v110, 0x21a00, v204
	v_cvt_pk_fp8_f32 v116, v120, v121 op_sel:[0,0,1]
	v_cvt_pk_fp8_f32 v119, v122, v123
	ds_read_b128 v[120:123], v110
	v_cvt_pk_fp8_f32 v117, v126, v127
	v_lshlrev_b64 v[110:111], 10, v[114:115]
	v_add_u32_e32 v114, 0x21b00, v204
	v_cvt_pk_fp8_f32 v118, v128, v129 op_sel:[0,0,1]
	v_cvt_pk_fp8_f32 v117, v124, v125 op_sel:[0,0,1]
	ds_read_b128 v[124:127], v114
	s_waitcnt lgkmcnt(1)
	v_mov_b32_e32 v114, v121
	v_mov_b32_e32 v115, v122
	v_mov_b32_e32 v121, v123
	v_pk_add_f32 v[114:115], v[114:115], v[120:121]
	v_cvt_pk_fp8_f32 v119, v132, v133 op_sel:[0,0,1]
	v_add_f32_e32 v114, v114, v115
	v_div_scale_f32 v115, s[2:3], v114, v114, s40
	v_rcp_f32_e32 v120, v115
	v_lshl_add_u64 v[110:111], s[18:19], 0, v[110:111]
	v_lshl_add_u64 v[110:111], v[110:111], 0, v[112:113]
	global_store_dwordx4 v[110:111], v[116:119], off
	v_fma_f32 v110, -v115, v120, 1.0
	v_fmac_f32_e32 v120, v110, v120
	v_div_scale_f32 v110, vcc, s40, v114, s40
	v_mul_f32_e32 v111, v110, v120
	v_fma_f32 v116, -v115, v111, v110
	v_fmac_f32_e32 v111, v116, v120
	v_fma_f32 v110, -v115, v111, v110
	v_div_fmas_f32 v110, v110, v120, v111
	v_div_fixup_f32 v110, v110, v114, s40
	v_pk_mul_f32 v[58:59], v[58:59], v[110:111] op_sel_hi:[1,0]
	v_pk_mul_f32 v[114:115], v[76:77], v[110:111] op_sel_hi:[1,0]
	v_pk_mul_f32 v[76:77], v[74:75], v[110:111] op_sel_hi:[1,0]
	v_cvt_pk_fp8_f32 v74, v58, v59
	v_pk_mul_f32 v[62:63], v[62:63], v[110:111] op_sel_hi:[1,0]
	v_pk_mul_f32 v[80:81], v[80:81], v[110:111] op_sel_hi:[1,0]
	v_pk_mul_f32 v[94:95], v[94:95], v[110:111] op_sel_hi:[1,0]
	v_cvt_pk_fp8_f32 v75, v76, v77
	v_cvt_pk_fp8_f32 v76, v80, v81
	v_cvt_pk_fp8_f32 v77, v94, v95
	v_cvt_pk_fp8_f32 v74, v62, v63 op_sel:[0,0,1]
	s_waitcnt lgkmcnt(0)
; #define LAS __attribute__((address_space(3)))
; __device__ __forceinline__ unsigned pk4_fp8(float a, float b, float c, float d) { int w = __builtin_amdgcn_cvt_pk_fp8_f32(a, b, 0, false); w = __builtin_amdgcn_cvt_pk_fp8_f32(c, d, w, true); return (unsigned)w; }
;     __device__ __forceinline__ void operator()(f32x4 (&acc)[2][2][4][2], const pg8::Unit& u, int wr, int wc, int fr, int fq) const {
;     ...
; #pragma unroll
;         for (int ai = 0; ai < 2; ++ai)
; #pragma unroll
;             for (int m = 0; m < 4; ++m) { const int rl = ai * 128 + wr * 64 + m * 16 + fr; const f32x4 q = *(const LAS f32x4*)(xch + 1024 + rl * 4); const float inv = 256.0f / ((q[0] + q[1]) + (q[2] + q[3]));
;                 { const f32x4 v0 = acc[ai][0][m][0] * inv, v1 = acc[ai][0][m][1] * inv, v2 = acc[ai][1][m][0] * inv, v3 = acc[ai][1][m][1] * inv;
;                     *(u32x4*)(out + (size_t)(row0 + ai * 128 + m * 16) * D + col0) = (u32x4){pk4_fp8(v0[0], v0[1], v0[2], v0[3]), pk4_fp8(v1[0], v1[1], v1[2], v1[3]), pk4_fp8(v2[0], v2[1], v2[2], v2[3]), pk4_fp8(v3[0], v3[1], v3[2], v3[3])}; } }
	v_mov_b32_e32 v62, v125
	v_mov_b32_e32 v63, v126
	v_mov_b32_e32 v125, v127
	v_pk_add_f32 v[62:63], v[62:63], v[124:125]
	v_pk_mul_f32 v[88:89], v[88:89], v[110:111] op_sel_hi:[1,0]
	v_add_f32_e32 v62, v62, v63
	v_pk_mul_f32 v[100:101], v[100:101], v[110:111] op_sel_hi:[1,0]
	v_div_scale_f32 v63, s[2:3], v62, v62, s40
	v_cvt_pk_fp8_f32 v75, v114, v115 op_sel:[0,0,1]
	v_cvt_pk_fp8_f32 v76, v88, v89 op_sel:[0,0,1]
	v_cvt_pk_fp8_f32 v77, v100, v101 op_sel:[0,0,1]
	v_rcp_f32_e32 v80, v63
	v_lshlrev_b64 v[58:59], 10, v[98:99]
	v_lshl_add_u64 v[58:59], s[18:19], 0, v[58:59]
	v_lshl_add_u64 v[58:59], v[58:59], 0, v[112:113]
	global_store_dwordx4 v[58:59], v[74:77], off
	v_fma_f32 v58, -v63, v80, 1.0
	v_fmac_f32_e32 v80, v58, v80
	v_div_scale_f32 v58, vcc, s40, v62, s40
	v_mul_f32_e32 v59, v58, v80
	v_fma_f32 v74, -v63, v59, v58
	v_fmac_f32_e32 v59, v74, v80
	v_fma_f32 v58, -v63, v59, v58
	v_div_fmas_f32 v58, v58, v80, v59
	v_div_fixup_f32 v58, v58, v62, s40
	v_pk_mul_f32 v[76:77], v[86:87], v[58:59] op_sel_hi:[1,0]
	v_pk_mul_f32 v[90:91], v[90:91], v[58:59] op_sel_hi:[1,0]
	v_cvt_pk_fp8_f32 v74, v76, v77
	v_cvt_pk_fp8_f32 v76, v90, v91
	v_pk_mul_f32 v[62:63], v[96:97], v[58:59] op_sel_hi:[1,0]
	v_pk_mul_f32 v[80:81], v[102:103], v[58:59] op_sel_hi:[1,0]
	v_pk_mul_f32 v[86:87], v[92:93], v[58:59] op_sel_hi:[1,0]
	v_pk_mul_f32 v[88:89], v[106:107], v[58:59] op_sel_hi:[1,0]
	v_pk_mul_f32 v[92:93], v[108:109], v[58:59] op_sel_hi:[1,0]
	v_pk_mul_f32 v[58:59], v[104:105], v[58:59] op_sel_hi:[1,0]
	v_cvt_pk_fp8_f32 v77, v58, v59
	v_lshl_add_u32 v58, v203, 4, s39
	v_cvt_pk_fp8_f32 v75, v86, v87
	v_cvt_pk_fp8_f32 v76, v88, v89 op_sel:[0,0,1]
	ds_read_b128 v[86:89], v58
	v_cvt_pk_fp8_f32 v74, v62, v63 op_sel:[0,0,1]
	v_add_u32_e32 v62, 0x22100, v204
	v_cvt_pk_fp8_f32 v75, v80, v81 op_sel:[0,0,1]
	v_lshlrev_b64 v[58:59], 10, v[82:83]
	ds_read_b128 v[80:83], v62
	s_waitcnt lgkmcnt(1)
	v_mov_b32_e32 v62, v87
	v_mov_b32_e32 v63, v88
	v_mov_b32_e32 v87, v89
	v_pk_add_f32 v[62:63], v[62:63], v[86:87]
	v_cvt_pk_fp8_f32 v77, v92, v93 op_sel:[0,0,1]
	v_add_f32_e32 v62, v62, v63
	v_div_scale_f32 v63, s[2:3], v62, v62, s40
	v_rcp_f32_e32 v86, v63
	v_lshl_add_u64 v[58:59], s[18:19], 0, v[58:59]
	v_lshl_add_u64 v[58:59], v[58:59], 0, v[112:113]
	global_store_dwordx4 v[58:59], v[74:77], off
	v_fma_f32 v58, -v63, v86, 1.0
	v_fmac_f32_e32 v86, v58, v86
	v_div_scale_f32 v58, vcc, s40, v62, s40
	v_mul_f32_e32 v59, v58, v86
	v_fma_f32 v74, -v63, v59, v58
	v_fmac_f32_e32 v59, v74, v86
	v_fma_f32 v58, -v63, v59, v58
	v_div_fmas_f32 v58, v58, v86, v59
	v_div_fixup_f32 v58, v58, v62, s40
	v_pk_mul_f32 v[22:23], v[22:23], v[58:59] op_sel_hi:[1,0]
	v_pk_mul_f32 v[62:63], v[64:65], v[58:59] op_sel_hi:[1,0]
	v_pk_mul_f32 v[64:65], v[56:57], v[58:59] op_sel_hi:[1,0]
	v_cvt_pk_fp8_f32 v56, v22, v23
	v_pk_mul_f32 v[26:27], v[26:27], v[58:59] op_sel_hi:[1,0]
	v_pk_mul_f32 v[38:39], v[38:39], v[58:59] op_sel_hi:[1,0]
	v_pk_mul_f32 v[30:31], v[30:31], v[58:59] op_sel_hi:[1,0]
	v_pk_mul_f32 v[48:49], v[48:49], v[58:59] op_sel_hi:[1,0]
	v_pk_mul_f32 v[44:45], v[44:45], v[58:59] op_sel_hi:[1,0]
	v_cvt_pk_fp8_f32 v57, v30, v31
	v_cvt_pk_fp8_f32 v58, v44, v45
	v_cvt_pk_fp8_f32 v59, v64, v65
	v_cvt_pk_fp8_f32 v56, v26, v27 op_sel:[0,0,1]
	s_waitcnt lgkmcnt(0)
	v_mov_b32_e32 v26, v81
	v_mov_b32_e32 v27, v82
	v_mov_b32_e32 v81, v83
	v_pk_add_f32 v[26:27], v[26:27], v[80:81]
	v_cvt_pk_fp8_f32 v57, v38, v39 op_sel:[0,0,1]
	v_add_f32_e32 v26, v26, v27
	v_div_scale_f32 v27, s[2:3], v26, v26, s40
	v_cvt_pk_fp8_f32 v58, v48, v49 op_sel:[0,0,1]
	v_cvt_pk_fp8_f32 v59, v62, v63 op_sel:[0,0,1]
	v_rcp_f32_e32 v30, v27
	v_lshlrev_b64 v[22:23], 10, v[66:67]
	v_lshl_add_u64 v[22:23], s[18:19], 0, v[22:23]
	v_lshl_add_u64 v[22:23], v[22:23], 0, v[112:113]
	global_store_dwordx4 v[22:23], v[56:59], off
	v_fma_f32 v22, -v27, v30, 1.0
	v_fmac_f32_e32 v30, v22, v30
	v_div_scale_f32 v22, vcc, s40, v26, s40
	v_mul_f32_e32 v23, v22, v30
	v_fma_f32 v31, -v27, v23, v22
	v_fmac_f32_e32 v23, v31, v30
	v_fma_f32 v22, -v27, v23, v22
	v_div_fmas_f32 v22, v22, v30, v23
	v_div_fixup_f32 v22, v22, v26, s40
	v_pk_mul_f32 v[26:27], v[60:61], v[22:23] op_sel_hi:[1,0]
	v_pk_mul_f32 v[30:31], v[52:53], v[22:23] op_sel_hi:[1,0]
	v_pk_mul_f32 v[38:39], v[70:71], v[22:23] op_sel_hi:[1,0]
	v_pk_mul_f32 v[44:45], v[54:55], v[22:23] op_sel_hi:[1,0]
	v_pk_mul_f32 v[48:49], v[78:79], v[22:23] op_sel_hi:[1,0]
	v_pk_mul_f32 v[56:57], v[68:69], v[22:23] op_sel_hi:[1,0]
	v_pk_mul_f32 v[60:61], v[84:85], v[22:23] op_sel_hi:[1,0]
	v_pk_mul_f32 v[22:23], v[72:73], v[22:23] op_sel_hi:[1,0]
	v_cvt_pk_fp8_f32 v55, v22, v23
	v_add_u32_e32 v22, 0x22200, v204
	v_cvt_pk_fp8_f32 v52, v30, v31
	v_cvt_pk_fp8_f32 v54, v56, v57
	ds_read_b128 v[56:59], v22
	v_cvt_pk_fp8_f32 v52, v26, v27 op_sel:[0,0,1]
	v_add_u32_e32 v26, 0x22300, v204
	v_cvt_pk_fp8_f32 v53, v44, v45
	v_cvt_pk_fp8_f32 v54, v48, v49 op_sel:[0,0,1]
	v_lshlrev_b64 v[22:23], 10, v[50:51]
	ds_read_b128 v[48:51], v26
	s_waitcnt lgkmcnt(1)
; #define LAS __attribute__((address_space(3)))
; __device__ __forceinline__ unsigned pk4_fp8(float a, float b, float c, float d) { int w = __builtin_amdgcn_cvt_pk_fp8_f32(a, b, 0, false); w = __builtin_amdgcn_cvt_pk_fp8_f32(c, d, w, true); return (unsigned)w; }
;     __device__ __forceinline__ void operator()(f32x4 (&acc)[2][2][4][2], const pg8::Unit& u, int wr, int wc, int fr, int fq) const {
;     ...
; #pragma unroll
;         for (int ai = 0; ai < 2; ++ai)
; #pragma unroll
;             for (int m = 0; m < 4; ++m) { const int rl = ai * 128 + wr * 64 + m * 16 + fr; const f32x4 q = *(const LAS f32x4*)(xch + 1024 + rl * 4); const float inv = 256.0f / ((q[0] + q[1]) + (q[2] + q[3]));
;                 { const f32x4 v0 = acc[ai][0][m][0] * inv, v1 = acc[ai][0][m][1] * inv, v2 = acc[ai][1][m][0] * inv, v3 = acc[ai][1][m][1] * inv;
;                     *(u32x4*)(out + (size_t)(row0 + ai * 128 + m * 16) * D + col0) = (u32x4){pk4_fp8(v0[0], v0[1], v0[2], v0[3]), pk4_fp8(v1[0], v1[1], v1[2], v1[3]), pk4_fp8(v2[0], v2[1], v2[2], v2[3]), pk4_fp8(v3[0], v3[1], v3[2], v3[3])}; } }
	v_mov_b32_e32 v26, v57
	v_mov_b32_e32 v27, v58
	v_mov_b32_e32 v57, v59
	v_pk_add_f32 v[26:27], v[26:27], v[56:57]
	v_cvt_pk_fp8_f32 v53, v38, v39 op_sel:[0,0,1]
	v_add_f32_e32 v26, v26, v27
	v_div_scale_f32 v27, s[2:3], v26, v26, s40
	v_cvt_pk_fp8_f32 v55, v60, v61 op_sel:[0,0,1]
	v_rcp_f32_e32 v30, v27
	v_lshl_add_u64 v[22:23], s[18:19], 0, v[22:23]
	v_lshl_add_u64 v[22:23], v[22:23], 0, v[112:113]
	global_store_dwordx4 v[22:23], v[52:55], off
	v_fma_f32 v22, -v27, v30, 1.0
	v_fmac_f32_e32 v30, v22, v30
	v_div_scale_f32 v22, vcc, s40, v26, s40
	v_mul_f32_e32 v23, v22, v30
	v_fma_f32 v31, -v27, v23, v22
	v_fmac_f32_e32 v23, v31, v30
	v_fma_f32 v22, -v27, v23, v22
	v_div_fmas_f32 v22, v22, v30, v23
	v_div_fixup_f32 v22, v22, v26, s40
	v_pk_mul_f32 v[26:27], v[4:5], v[22:23] op_sel_hi:[1,0]
	v_pk_mul_f32 v[4:5], v[2:3], v[22:23] op_sel_hi:[1,0]
	v_pk_mul_f32 v[6:7], v[6:7], v[22:23] op_sel_hi:[1,0]
	v_cvt_pk_fp8_f32 v3, v6, v7
	v_pk_mul_f32 v[8:9], v[8:9], v[22:23] op_sel_hi:[1,0]
	v_pk_mul_f32 v[10:11], v[10:11], v[22:23] op_sel_hi:[1,0]
	v_pk_mul_f32 v[20:21], v[20:21], v[22:23] op_sel_hi:[1,0]
	v_cvt_pk_fp8_f32 v2, v4, v5
	v_cvt_pk_fp8_f32 v4, v10, v11
	v_cvt_pk_fp8_f32 v5, v20, v21
	v_cvt_pk_fp8_f32 v3, v8, v9 op_sel:[0,0,1]
	s_waitcnt lgkmcnt(0)
	v_mov_b32_e32 v8, v49
	v_mov_b32_e32 v9, v50
	v_mov_b32_e32 v49, v51
	v_pk_add_f32 v[8:9], v[8:9], v[48:49]
	v_pk_mul_f32 v[12:13], v[12:13], v[22:23] op_sel_hi:[1,0]
	v_add_f32_e32 v8, v8, v9
	v_pk_mul_f32 v[28:29], v[28:29], v[22:23] op_sel_hi:[1,0]
	v_div_scale_f32 v9, s[2:3], v8, v8, s40
	v_cvt_pk_fp8_f32 v2, v26, v27 op_sel:[0,0,1]
	v_cvt_pk_fp8_f32 v4, v12, v13 op_sel:[0,0,1]
	v_cvt_pk_fp8_f32 v5, v28, v29 op_sel:[0,0,1]
	v_rcp_f32_e32 v10, v9
	v_lshlrev_b64 v[6:7], 10, v[34:35]
	v_lshl_add_u64 v[6:7], s[18:19], 0, v[6:7]
	v_lshl_add_u64 v[6:7], v[6:7], 0, v[112:113]
	global_store_dwordx4 v[6:7], v[2:5], off
	s_nop 1
	v_fma_f32 v2, -v9, v10, 1.0
	v_fmac_f32_e32 v10, v2, v10
	v_div_scale_f32 v2, vcc, s40, v8, s40
	v_mul_f32_e32 v3, v2, v10
	v_fma_f32 v4, -v9, v3, v2
	v_fmac_f32_e32 v3, v4, v10
	v_fma_f32 v2, -v9, v3, v2
	v_div_fmas_f32 v2, v2, v10, v3
	v_div_fixup_f32 v2, v2, v8, s40
	v_pk_mul_f32 v[6:7], v[24:25], v[2:3] op_sel_hi:[1,0]
	v_pk_mul_f32 v[4:5], v[14:15], v[2:3] op_sel_hi:[1,0]
	v_pk_mul_f32 v[8:9], v[36:37], v[2:3] op_sel_hi:[1,0]
	v_pk_mul_f32 v[10:11], v[16:17], v[2:3] op_sel_hi:[1,0]
	v_pk_mul_f32 v[12:13], v[42:43], v[2:3] op_sel_hi:[1,0]
	v_pk_mul_f32 v[14:15], v[32:33], v[2:3] op_sel_hi:[1,0]
	v_pk_mul_f32 v[16:17], v[46:47], v[2:3] op_sel_hi:[1,0]
	v_pk_mul_f32 v[20:21], v[40:41], v[2:3] op_sel_hi:[1,0]
	v_cvt_pk_fp8_f32 v2, v4, v5
	v_cvt_pk_fp8_f32 v3, v10, v11
	v_cvt_pk_fp8_f32 v4, v14, v15
	v_cvt_pk_fp8_f32 v5, v20, v21
	v_cvt_pk_fp8_f32 v2, v6, v7 op_sel:[0,0,1]
	v_cvt_pk_fp8_f32 v3, v8, v9 op_sel:[0,0,1]
	v_cvt_pk_fp8_f32 v4, v12, v13 op_sel:[0,0,1]
	v_cvt_pk_fp8_f32 v5, v16, v17 op_sel:[0,0,1]
	v_lshlrev_b64 v[6:7], 10, v[18:19]
	v_lshl_add_u64 v[6:7], s[18:19], 0, v[6:7]
	v_lshl_add_u64 v[6:7], v[6:7], 0, v[112:113]
	s_and_b64 vcc, exec, s[0:1]
	global_store_dwordx4 v[6:7], v[2:5], off
	s_cbranch_vccnz .LBB0_639
	s_andn2_b64 vcc, exec, s[12:13]
	s_mov_b64 s[2:3], s[10:11]
	s_mov_b64 s[0:1], s[8:9]
	s_cbranch_vccnz .LBB0_685
	s_ashr_i32 s15, s14, 31
	s_lshl_b64 s[0:1], s[14:15], 18
	s_add_u32 s0, s27, s0
	s_addc_u32 s1, s28, s1
	s_ashr_i32 s2, s14, 1
	s_and_b32 s2, s2, -4
	s_add_i32 s2, s2, s7
	s_ashr_i32 s3, s2, 31
	s_lshl_b64 s[2:3], s[2:3], 18
	s_add_u32 s2, s56, s2
	s_addc_u32 s3, s57, s3

; #define GAS __attribute__((address_space(1)))
; #define LAS __attribute__((address_space(3)))
; __device__ __forceinline__ unsigned pk4_fp8(float a, float b, float c, float d) { int w = __builtin_amdgcn_cvt_pk_fp8_f32(a, b, 0, false); w = __builtin_amdgcn_cvt_pk_fp8_f32(c, d, w, true); return (unsigned)w; }
; __device__ __forceinline__ void p7_router(Frame& F, const Args& A) {
;     ...
; #pragma unroll 1
;         for (int q = 0; q < 4; ++q) {
;             __syncthreads();
; #pragma unroll
;             for (int i = 0; i < 4; ++i) { const int idx = tid + 512 * i, rho = idx >> 5, ch = idx & 31; *(LAS u32x4*)(Wt + rho * 512 + ch * 16) = wimg[i]; }
;             __syncthreads();
;             { const unsigned char* src = F.ws + WS_WR + (q < 3 ? q + 1 : 3) * 512;
; #pragma unroll
;               for (int i = 0; i < 4; ++i) { const int idx = tid + 512 * i, rho = idx >> 5, ch = idx & 31; wimg[i] = *(const GAS u32x4*)(src + rho * 2048 + ch * 16); } }
; #pragma unroll
;             for (int g = 0; g < 2; ++g) {
;                 asm volatile("s_waitcnt lgkmcnt(0)" ::: "memory");
; #pragma unroll
;                 for (int i = 0; i < 8; ++i)
;                     asm volatile("s_mov_b32 m0, %2\n\ts_nop 0\n\tglobal_load_lds_dwordx4 %0, %1" :: "v"(dvo[i] + (unsigned)(g * 16 * 2048 + q * 512)), "s"(xrow_u), "s"(xb_m0 + (unsigned)(i * 1024)) : "memory", "m0");
;                 asm volatile("s_waitcnt vmcnt(0)" ::: "memory");
;                 const float rr = g ? r1 : r0; unsigned char* xo = (g ? xo1 : xo0) + q * 256;
; #pragma unroll
;                 for (int ks = 0; ks < 8; ++ks) {
;                     const u32x4 c0 = *(const LAS u32x4*)(xbuf + tl * 512 + (((4 * ks + fq) ^ tl) << 4));
;                     *(GAS u32x2*)(xo + 32 * ks) = (u32x2){pk4_fp8(bflo(c0.x) * rr, bfhi(c0.x) * rr, bflo(c0.y) * rr, bfhi(c0.y) * rr), pk4_fp8(bflo(c0.z) * rr, bfhi(c0.z) * rr, bflo(c0.w) * rr, bfhi(c0.w) * rr)};
;                     const bf16x8 f0 = __builtin_bit_cast(bf16x8, c0);
; #pragma unroll
;                     for (int rb = 0; rb < 4; ++rb) { const int rho = 16 * rb + tl; const bf16x8 a = *(const LAS bf16x8*)(Wt + rho * 512 + (((4 * ks + fq) ^ tl) << 4));
;                         acc[rb][g] = __builtin_amdgcn_mfma_f32_16x16x32_bf16(a, f0, acc[rb][g], 0, 0, 0); }
;                 }
.LBB0_839:
	s_add_i32 s4, s24, 0x200
	s_cmpk_eq_i32 s24, 0x600
	s_cselect_b32 s14, s24, s4
	s_barrier
	s_waitcnt vmcnt(3)
	ds_write_b128 v140, v[22:25]
	s_waitcnt vmcnt(2)
	ds_write_b128 v140, v[18:21] offset:8192
	s_waitcnt vmcnt(1)
	ds_write_b128 v140, v[10:13] offset:16384
	s_waitcnt vmcnt(0)
	ds_write_b128 v140, v[14:17] offset:24576
	v_lshl_add_u64 v[14:15], v[72:73], 0, s[14:15]
	v_lshl_add_u64 v[10:11], v[14:15], 0, v[64:65]
	s_waitcnt lgkmcnt(0)
	s_barrier
	global_load_dwordx4 v[22:25], v[10:11], off
	v_lshl_add_u64 v[10:11], v[14:15], 0, v[66:67]
	global_load_dwordx4 v[18:21], v[10:11], off
	v_lshl_add_u64 v[10:11], v[14:15], 0, v[68:69]
	v_lshl_add_u64 v[14:15], v[14:15], 0, v[70:71]
	global_load_dwordx4 v[10:13], v[10:11], off
	v_add_u32_e32 v94, s24, v139
	global_load_dwordx4 v[14:17], v[14:15], off
	s_waitcnt lgkmcnt(0)
	s_mov_b32 m0, s36
	s_nop 0
	global_load_lds_dwordx4 v94, s[20:21]
	v_add_u32_e32 v95, s24, v138
	v_add_u32_e32 v87, 0x1000, v95
	s_mov_b32 m0, s43
	s_nop 0
	global_load_lds_dwordx4 v87, s[20:21]
	v_add_u32_e32 v154, s24, v137
	v_add_u32_e32 v87, 0x2000, v154
	s_mov_b32 m0, s44
	s_nop 0
	global_load_lds_dwordx4 v87, s[20:21]
	v_add_u32_e32 v159, s24, v136
	v_add_u32_e32 v87, 0x3000, v159
	s_mov_b32 m0, s45
	s_nop 0
	global_load_lds_dwordx4 v87, s[20:21]
	v_add_u32_e32 v161, s24, v135
	v_add_u32_e32 v87, 0x4000, v161
	s_mov_b32 m0, s46
	s_nop 0
	global_load_lds_dwordx4 v87, s[20:21]
	v_add_u32_e32 v162, s24, v134
	v_add_u32_e32 v87, 0x5000, v162
	s_mov_b32 m0, s47
	s_nop 0
	global_load_lds_dwordx4 v87, s[20:21]
	v_add_u32_e32 v163, s24, v133
	v_add_u32_e32 v87, 0x6000, v163
	s_mov_b32 m0, s22
	s_nop 0
	global_load_lds_dwordx4 v87, s[20:21]
	v_add_u32_e32 v164, s24, v59
	v_add_u32_e32 v87, 0x7000, v164
	s_mov_b32 m0, s23
	s_nop 0
	global_load_lds_dwordx4 v87, s[20:21]
	s_waitcnt vmcnt(0)
	v_add_u32_e32 v165, v132, v100
	ds_read_b128 v[146:149], v165 offset:32768
	v_add_u32_e32 v94, 0x8000, v94
	s_cmpk_eq_i32 s4, 0x800
	s_mov_b32 s24, s4
	s_waitcnt lgkmcnt(0)
	v_lshlrev_b32_e32 v150, 16, v147
	v_lshlrev_b32_e32 v87, 16, v146
	v_and_b32_e32 v145, 0xffff0000, v146
	v_mul_f32_e32 v151, v92, v150
	v_and_b32_e32 v150, 0xffff0000, v147
	v_mul_f32_e32 v87, v92, v87
	v_mul_f32_e32 v145, v92, v145
	v_mul_f32_e32 v152, v92, v150
	v_cvt_pk_fp8_f32 v150, v87, v145
	v_lshlrev_b32_e32 v87, 16, v148
	v_and_b32_e32 v145, 0xffff0000, v148
	v_mul_f32_e32 v87, v92, v87
	v_cvt_pk_fp8_f32 v150, v151, v152 op_sel:[0,0,1]
	v_lshlrev_b32_e32 v151, 16, v149
	v_mul_f32_e32 v152, v92, v151
	v_and_b32_e32 v151, 0xffff0000, v149
	v_mul_f32_e32 v145, v92, v145
	v_mul_f32_e32 v153, v92, v151
	v_cvt_pk_fp8_f32 v151, v87, v145
	v_add_u32_e32 v87, v96, v100
	v_cvt_pk_fp8_f32 v151, v152, v153 op_sel:[0,0,1]
	global_store_dwordx2 v[90:91], v[150:151], off
	ds_read_b128 v[150:153], v87
	s_waitcnt lgkmcnt(0)
	v_mfma_f32_16x16x32_bf16 v[42:45], v[150:153], v[146:149], v[42:45]
	ds_read_b128 v[150:153], v87 offset:8192
	s_waitcnt lgkmcnt(0)
	v_mfma_f32_16x16x32_bf16 v[46:49], v[150:153], v[146:149], v[46:49]
	ds_read_b128 v[150:153], v87 offset:16384
	s_waitcnt lgkmcnt(0)
	v_mfma_f32_16x16x32_bf16 v[50:53], v[150:153], v[146:149], v[50:53]
	ds_read_b128 v[150:153], v87 offset:24576
	s_waitcnt lgkmcnt(0)
	v_mfma_f32_16x16x32_bf16 v[54:57], v[150:153], v[146:149], v[54:57]
	v_add_u32_e32 v152, v132, v101
	ds_read_b128 v[146:149], v152 offset:32768
	s_waitcnt lgkmcnt(0)
	v_and_b32_e32 v150, 0xffff0000, v146
	v_mul_f32_e32 v151, v92, v150
	v_lshlrev_b32_e32 v150, 16, v147
	v_lshlrev_b32_e32 v145, 16, v146
	v_mul_f32_e32 v153, v92, v150
	v_and_b32_e32 v150, 0xffff0000, v147
	v_mul_f32_e32 v145, v92, v145
	v_mul_f32_e32 v155, v92, v150
	v_cvt_pk_fp8_f32 v150, v145, v151
	v_and_b32_e32 v151, 0xffff0000, v148
	v_lshlrev_b32_e32 v145, 16, v148
	v_mul_f32_e32 v145, v92, v145
	v_cvt_pk_fp8_f32 v150, v153, v155 op_sel:[0,0,1]
	v_mul_f32_e32 v153, v92, v151
	v_lshlrev_b32_e32 v151, 16, v149
	v_mul_f32_e32 v155, v92, v151
	v_and_b32_e32 v151, 0xffff0000, v149
	v_mul_f32_e32 v156, v92, v151
	v_cvt_pk_fp8_f32 v151, v145, v153
	v_add_u32_e32 v145, v96, v101
	ds_read_b128 v[166:169], v145
	s_waitcnt lgkmcnt(0)
	v_mfma_f32_16x16x32_bf16 v[42:45], v[166:169], v[146:149], v[42:45]
	ds_read_b128 v[166:169], v145 offset:8192
	v_cvt_pk_fp8_f32 v151, v155, v156 op_sel:[0,0,1]
	v_add_u32_e32 v153, v132, v102
	s_waitcnt lgkmcnt(0)
	v_mfma_f32_16x16x32_bf16 v[46:49], v[166:169], v[146:149], v[46:49]
	ds_read_b128 v[166:169], v145 offset:16384
	global_store_dwordx2 v[90:91], v[150:151], off offset:32
	s_waitcnt lgkmcnt(0)
	v_mfma_f32_16x16x32_bf16 v[50:53], v[166:169], v[146:149], v[50:53]
	ds_read_b128 v[166:169], v145 offset:24576
	s_waitcnt lgkmcnt(0)
	v_mfma_f32_16x16x32_bf16 v[54:57], v[166:169], v[146:149], v[54:57]
	ds_read_b128 v[148:151], v153 offset:32768
	s_waitcnt lgkmcnt(0)
	v_lshlrev_b32_e32 v146, 16, v148
	v_mul_f32_e32 v147, v92, v146
	v_and_b32_e32 v146, 0xffff0000, v148
	v_mul_f32_e32 v155, v92, v146
	v_lshlrev_b32_e32 v146, 16, v149
	v_mul_f32_e32 v156, v92, v146
	v_and_b32_e32 v146, 0xffff0000, v149
	v_mul_f32_e32 v157, v92, v146
	v_cvt_pk_fp8_f32 v146, v147, v155
	v_lshlrev_b32_e32 v147, 16, v150
	v_mul_f32_e32 v155, v92, v147
	v_and_b32_e32 v147, 0xffff0000, v150
	v_cvt_pk_fp8_f32 v146, v156, v157 op_sel:[0,0,1]
	v_mul_f32_e32 v156, v92, v147
	v_lshlrev_b32_e32 v147, 16, v151
	v_mul_f32_e32 v157, v92, v147
	v_and_b32_e32 v147, 0xffff0000, v151
	v_mul_f32_e32 v158, v92, v147
	v_cvt_pk_fp8_f32 v147, v155, v156
	v_add_u32_e32 v155, v132, v103
	v_cvt_pk_fp8_f32 v147, v157, v158 op_sel:[0,0,1]
	global_store_dwordx2 v[90:91], v[146:147], off offset:64
	v_add_u32_e32 v146, v96, v102
	ds_read_b128 v[166:169], v146
	s_waitcnt lgkmcnt(0)
; #define GAS __attribute__((address_space(1)))
; #define LAS __attribute__((address_space(3)))
; __device__ __forceinline__ unsigned pk4_fp8(float a, float b, float c, float d) { int w = __builtin_amdgcn_cvt_pk_fp8_f32(a, b, 0, false); w = __builtin_amdgcn_cvt_pk_fp8_f32(c, d, w, true); return (unsigned)w; }
; __device__ __forceinline__ void p7_router(Frame& F, const Args& A) {
;     ...
; #pragma unroll
;                 for (int ks = 0; ks < 8; ++ks) {
;                     const u32x4 c0 = *(const LAS u32x4*)(xbuf + tl * 512 + (((4 * ks + fq) ^ tl) << 4));
;                     *(GAS u32x2*)(xo + 32 * ks) = (u32x2){pk4_fp8(bflo(c0.x) * rr, bfhi(c0.x) * rr, bflo(c0.y) * rr, bfhi(c0.y) * rr), pk4_fp8(bflo(c0.z) * rr, bfhi(c0.z) * rr, bflo(c0.w) * rr, bfhi(c0.w) * rr)};
;                     const bf16x8 f0 = __builtin_bit_cast(bf16x8, c0);
; #pragma unroll
;                     for (int rb = 0; rb < 4; ++rb) { const int rho = 16 * rb + tl; const bf16x8 a = *(const LAS bf16x8*)(Wt + rho * 512 + (((4 * ks + fq) ^ tl) << 4));
;                         acc[rb][g] = __builtin_amdgcn_mfma_f32_16x16x32_bf16(a, f0, acc[rb][g], 0, 0, 0); }
;                 }
	v_mfma_f32_16x16x32_bf16 v[42:45], v[166:169], v[148:151], v[42:45]
	ds_read_b128 v[166:169], v146 offset:8192
	s_waitcnt lgkmcnt(0)
	v_mfma_f32_16x16x32_bf16 v[46:49], v[166:169], v[148:151], v[46:49]
	ds_read_b128 v[166:169], v146 offset:16384
	s_waitcnt lgkmcnt(0)
	v_mfma_f32_16x16x32_bf16 v[50:53], v[166:169], v[148:151], v[50:53]
	ds_read_b128 v[166:169], v146 offset:24576
	s_waitcnt lgkmcnt(0)
	v_mfma_f32_16x16x32_bf16 v[54:57], v[166:169], v[148:151], v[54:57]
	ds_read_b128 v[148:151], v155 offset:32768
	s_waitcnt lgkmcnt(0)
	v_and_b32_e32 v156, 0xffff0000, v148
	v_mul_f32_e32 v157, v92, v156
	v_lshlrev_b32_e32 v156, 16, v149
	v_lshlrev_b32_e32 v147, 16, v148
	v_mul_f32_e32 v158, v92, v156
	v_and_b32_e32 v156, 0xffff0000, v149
	v_mul_f32_e32 v147, v92, v147
	v_mul_f32_e32 v160, v92, v156
	v_cvt_pk_fp8_f32 v156, v147, v157
	v_and_b32_e32 v157, 0xffff0000, v150
	v_lshlrev_b32_e32 v147, 16, v150
	v_mul_f32_e32 v147, v92, v147
	v_cvt_pk_fp8_f32 v156, v158, v160 op_sel:[0,0,1]
	v_mul_f32_e32 v158, v92, v157
	v_lshlrev_b32_e32 v157, 16, v151
	v_mul_f32_e32 v160, v92, v157
	v_and_b32_e32 v157, 0xffff0000, v151
	v_mul_f32_e32 v166, v92, v157
	v_cvt_pk_fp8_f32 v157, v147, v158
	v_add_u32_e32 v147, v96, v103
	v_cvt_pk_fp8_f32 v157, v160, v166 op_sel:[0,0,1]
	ds_read_b128 v[166:169], v147
	s_waitcnt lgkmcnt(0)
	v_mfma_f32_16x16x32_bf16 v[42:45], v[166:169], v[148:151], v[42:45]
	ds_read_b128 v[166:169], v147 offset:8192
	global_store_dwordx2 v[90:91], v[156:157], off offset:96
	v_add_u32_e32 v156, v132, v104
	s_waitcnt lgkmcnt(0)
	v_mfma_f32_16x16x32_bf16 v[46:49], v[166:169], v[148:151], v[46:49]
	ds_read_b128 v[166:169], v147 offset:16384
	s_waitcnt lgkmcnt(0)
	v_mfma_f32_16x16x32_bf16 v[50:53], v[166:169], v[148:151], v[50:53]
	ds_read_b128 v[166:169], v147 offset:24576
	s_waitcnt lgkmcnt(0)
	v_mfma_f32_16x16x32_bf16 v[54:57], v[166:169], v[148:151], v[54:57]
	ds_read_b128 v[166:169], v156 offset:32768
	s_waitcnt lgkmcnt(0)
	v_lshlrev_b32_e32 v148, 16, v166
	v_mul_f32_e32 v149, v92, v148
	v_and_b32_e32 v148, 0xffff0000, v166
	v_mul_f32_e32 v150, v92, v148
	v_lshlrev_b32_e32 v148, 16, v167
	v_mul_f32_e32 v151, v92, v148
	v_and_b32_e32 v148, 0xffff0000, v167
	v_mul_f32_e32 v157, v92, v148
	v_cvt_pk_fp8_f32 v148, v149, v150
	v_lshlrev_b32_e32 v149, 16, v168
	v_mul_f32_e32 v150, v92, v149
	v_and_b32_e32 v149, 0xffff0000, v168
	v_cvt_pk_fp8_f32 v148, v151, v157 op_sel:[0,0,1]
	v_mul_f32_e32 v151, v92, v149
	v_lshlrev_b32_e32 v149, 16, v169
	v_mul_f32_e32 v157, v92, v149
	v_and_b32_e32 v149, 0xffff0000, v169
	v_mul_f32_e32 v158, v92, v149
	v_cvt_pk_fp8_f32 v149, v150, v151
	v_cvt_pk_fp8_f32 v149, v157, v158 op_sel:[0,0,1]
	v_add_u32_e32 v157, v132, v105
	global_store_dwordx2 v[90:91], v[148:149], off offset:128
	v_add_u32_e32 v148, v96, v104
	ds_read_b128 v[170:173], v148
	s_waitcnt lgkmcnt(0)
	v_mfma_f32_16x16x32_bf16 v[42:45], v[170:173], v[166:169], v[42:45]
	ds_read_b128 v[170:173], v148 offset:8192
	s_waitcnt lgkmcnt(0)
	v_mfma_f32_16x16x32_bf16 v[46:49], v[170:173], v[166:169], v[46:49]
	ds_read_b128 v[170:173], v148 offset:16384
	s_waitcnt lgkmcnt(0)
	v_mfma_f32_16x16x32_bf16 v[50:53], v[170:173], v[166:169], v[50:53]
	ds_read_b128 v[170:173], v148 offset:24576
	s_waitcnt lgkmcnt(0)
	v_mfma_f32_16x16x32_bf16 v[54:57], v[170:173], v[166:169], v[54:57]
	ds_read_b128 v[166:169], v157 offset:32768
	s_waitcnt lgkmcnt(0)
	v_and_b32_e32 v150, 0xffff0000, v166
	v_mul_f32_e32 v151, v92, v150
	v_lshlrev_b32_e32 v150, 16, v167
	v_lshlrev_b32_e32 v149, 16, v166
	v_mul_f32_e32 v158, v92, v150
	v_and_b32_e32 v150, 0xffff0000, v167
	v_mul_f32_e32 v149, v92, v149
	v_mul_f32_e32 v160, v92, v150
	v_cvt_pk_fp8_f32 v150, v149, v151
	v_and_b32_e32 v151, 0xffff0000, v168
	v_lshlrev_b32_e32 v149, 16, v168
	v_mul_f32_e32 v149, v92, v149
	v_cvt_pk_fp8_f32 v150, v158, v160 op_sel:[0,0,1]
	v_mul_f32_e32 v158, v92, v151
	v_lshlrev_b32_e32 v151, 16, v169
	v_mul_f32_e32 v160, v92, v151
	v_and_b32_e32 v151, 0xffff0000, v169
	v_mul_f32_e32 v170, v92, v151
	v_cvt_pk_fp8_f32 v151, v149, v158
	v_add_u32_e32 v149, v96, v105
	v_add_u32_e32 v158, v132, v106
	v_cvt_pk_fp8_f32 v151, v160, v170 op_sel:[0,0,1]
	ds_read_b128 v[170:173], v149
	s_waitcnt lgkmcnt(0)
	v_mfma_f32_16x16x32_bf16 v[42:45], v[170:173], v[166:169], v[42:45]
	ds_read_b128 v[170:173], v149 offset:8192
	global_store_dwordx2 v[90:91], v[150:151], off offset:160
	s_waitcnt lgkmcnt(0)
	v_mfma_f32_16x16x32_bf16 v[46:49], v[170:173], v[166:169], v[46:49]
	ds_read_b128 v[170:173], v149 offset:16384
	s_waitcnt lgkmcnt(0)
	v_mfma_f32_16x16x32_bf16 v[50:53], v[170:173], v[166:169], v[50:53]
	ds_read_b128 v[170:173], v149 offset:24576
	s_waitcnt lgkmcnt(0)
	v_mfma_f32_16x16x32_bf16 v[54:57], v[170:173], v[166:169], v[54:57]
	ds_read_b128 v[166:169], v158 offset:32768
	s_waitcnt lgkmcnt(0)
	v_lshlrev_b32_e32 v150, 16, v166
	v_mul_f32_e32 v151, v92, v150
	v_and_b32_e32 v150, 0xffff0000, v166
	v_mul_f32_e32 v160, v92, v150
	v_lshlrev_b32_e32 v150, 16, v167
	v_mul_f32_e32 v170, v92, v150
	v_and_b32_e32 v150, 0xffff0000, v167
	v_mul_f32_e32 v171, v92, v150
	v_cvt_pk_fp8_f32 v150, v151, v160
	v_lshlrev_b32_e32 v151, 16, v168
	v_mul_f32_e32 v160, v92, v151
	v_and_b32_e32 v151, 0xffff0000, v168
	v_cvt_pk_fp8_f32 v150, v170, v171 op_sel:[0,0,1]
	v_mul_f32_e32 v170, v92, v151
	v_lshlrev_b32_e32 v151, 16, v169
	v_mul_f32_e32 v171, v92, v151
	v_and_b32_e32 v151, 0xffff0000, v169
	v_mul_f32_e32 v172, v92, v151
	v_cvt_pk_fp8_f32 v151, v160, v170
	v_add_u32_e32 v160, v132, v107
	v_cvt_pk_fp8_f32 v151, v171, v172 op_sel:[0,0,1]
	global_store_dwordx2 v[90:91], v[150:151], off offset:192
	v_add_u32_e32 v150, v96, v106
	ds_read_b128 v[170:173], v150
	s_waitcnt lgkmcnt(0)
; #define GAS __attribute__((address_space(1)))
; #define LAS __attribute__((address_space(3)))
; __device__ __forceinline__ unsigned pk4_fp8(float a, float b, float c, float d) { int w = __builtin_amdgcn_cvt_pk_fp8_f32(a, b, 0, false); w = __builtin_amdgcn_cvt_pk_fp8_f32(c, d, w, true); return (unsigned)w; }
; __device__ __forceinline__ void p7_router(Frame& F, const Args& A) {
;     ...
;                 asm volatile("s_waitcnt lgkmcnt(0)" ::: "memory");
; #pragma unroll
;                 for (int i = 0; i < 8; ++i)
;                     asm volatile("s_mov_b32 m0, %2\n\ts_nop 0\n\tglobal_load_lds_dwordx4 %0, %1" :: "v"(dvo[i] + (unsigned)(g * 16 * 2048 + q * 512)), "s"(xrow_u), "s"(xb_m0 + (unsigned)(i * 1024)) : "memory", "m0");
;                 asm volatile("s_waitcnt vmcnt(0)" ::: "memory");
;                 const float rr = g ? r1 : r0; unsigned char* xo = (g ? xo1 : xo0) + q * 256;
; #pragma unroll
;                 for (int ks = 0; ks < 8; ++ks) {
;                     const u32x4 c0 = *(const LAS u32x4*)(xbuf + tl * 512 + (((4 * ks + fq) ^ tl) << 4));
;                     *(GAS u32x2*)(xo + 32 * ks) = (u32x2){pk4_fp8(bflo(c0.x) * rr, bfhi(c0.x) * rr, bflo(c0.y) * rr, bfhi(c0.y) * rr), pk4_fp8(bflo(c0.z) * rr, bfhi(c0.z) * rr, bflo(c0.w) * rr, bfhi(c0.w) * rr)};
;                     const bf16x8 f0 = __builtin_bit_cast(bf16x8, c0);
; #pragma unroll
;                     for (int rb = 0; rb < 4; ++rb) { const int rho = 16 * rb + tl; const bf16x8 a = *(const LAS bf16x8*)(Wt + rho * 512 + (((4 * ks + fq) ^ tl) << 4));
;                         acc[rb][g] = __builtin_amdgcn_mfma_f32_16x16x32_bf16(a, f0, acc[rb][g], 0, 0, 0); }
;                 }
	v_mfma_f32_16x16x32_bf16 v[42:45], v[170:173], v[166:169], v[42:45]
	ds_read_b128 v[170:173], v150 offset:8192
	s_waitcnt lgkmcnt(0)
	v_mfma_f32_16x16x32_bf16 v[46:49], v[170:173], v[166:169], v[46:49]
	ds_read_b128 v[170:173], v150 offset:16384
	s_waitcnt lgkmcnt(0)
	v_mfma_f32_16x16x32_bf16 v[50:53], v[170:173], v[166:169], v[50:53]
	ds_read_b128 v[170:173], v150 offset:24576
	s_waitcnt lgkmcnt(0)
	v_mfma_f32_16x16x32_bf16 v[54:57], v[170:173], v[166:169], v[54:57]
	ds_read_b128 v[166:169], v160 offset:32768
	s_waitcnt lgkmcnt(0)
	v_and_b32_e32 v170, 0xffff0000, v166
	v_mul_f32_e32 v171, v92, v170
	v_lshlrev_b32_e32 v170, 16, v167
	v_lshlrev_b32_e32 v151, 16, v166
	v_mul_f32_e32 v172, v92, v170
	v_and_b32_e32 v170, 0xffff0000, v167
	v_mul_f32_e32 v151, v92, v151
	v_mul_f32_e32 v173, v92, v170
	v_cvt_pk_fp8_f32 v170, v151, v171
	v_and_b32_e32 v171, 0xffff0000, v168
	v_lshlrev_b32_e32 v151, 16, v168
	v_mul_f32_e32 v151, v92, v151
	v_cvt_pk_fp8_f32 v170, v172, v173 op_sel:[0,0,1]
	v_mul_f32_e32 v172, v92, v171
	v_lshlrev_b32_e32 v171, 16, v169
	v_mul_f32_e32 v173, v92, v171
	v_and_b32_e32 v171, 0xffff0000, v169
	v_mul_f32_e32 v174, v92, v171
	v_cvt_pk_fp8_f32 v171, v151, v172
	v_add_u32_e32 v151, v96, v107
	v_cvt_pk_fp8_f32 v171, v173, v174 op_sel:[0,0,1]
	global_store_dwordx2 v[90:91], v[170:171], off offset:224
	ds_read_b128 v[170:173], v151
	s_waitcnt lgkmcnt(0)
	v_mfma_f32_16x16x32_bf16 v[42:45], v[170:173], v[166:169], v[42:45]
	ds_read_b128 v[170:173], v151 offset:8192
	s_waitcnt lgkmcnt(0)
	v_mfma_f32_16x16x32_bf16 v[46:49], v[170:173], v[166:169], v[46:49]
	ds_read_b128 v[170:173], v151 offset:16384
	s_waitcnt lgkmcnt(0)
	v_mfma_f32_16x16x32_bf16 v[50:53], v[170:173], v[166:169], v[50:53]
	ds_read_b128 v[170:173], v151 offset:24576
	s_waitcnt lgkmcnt(0)
	s_mov_b32 m0, s36
	s_nop 0
	global_load_lds_dwordx4 v94, s[20:21]
	v_add_u32_e32 v94, 0x9000, v95
	s_mov_b32 m0, s43
	s_nop 0
	global_load_lds_dwordx4 v94, s[20:21]
	v_add_u32_e32 v94, 0xa000, v154
	s_mov_b32 m0, s44
	s_nop 0
	global_load_lds_dwordx4 v94, s[20:21]
	v_add_u32_e32 v94, 0xb000, v159
	s_mov_b32 m0, s45
	s_nop 0
	global_load_lds_dwordx4 v94, s[20:21]
	v_add_u32_e32 v94, 0xc000, v161
	s_mov_b32 m0, s46
	s_nop 0
	global_load_lds_dwordx4 v94, s[20:21]
	v_add_u32_e32 v94, 0xd000, v162
	s_mov_b32 m0, s47
	s_nop 0
	global_load_lds_dwordx4 v94, s[20:21]
	v_add_u32_e32 v94, 0xe000, v163
	s_mov_b32 m0, s22
	s_nop 0
	global_load_lds_dwordx4 v94, s[20:21]
	v_add_u32_e32 v94, 0xf000, v164
	s_mov_b32 m0, s23
	s_nop 0
	global_load_lds_dwordx4 v94, s[20:21]
	s_waitcnt vmcnt(0)
	ds_read_b128 v[162:165], v165 offset:32768
	s_waitcnt lgkmcnt(1)
	v_mfma_f32_16x16x32_bf16 v[54:57], v[170:173], v[166:169], v[54:57]
	s_waitcnt lgkmcnt(0)
	v_lshlrev_b32_e32 v94, 16, v162
	v_and_b32_e32 v95, 0xffff0000, v162
	v_mul_f32_e32 v94, v62, v94
	v_mul_f32_e32 v95, v62, v95
	v_cvt_pk_fp8_f32 v166, v94, v95
	v_lshlrev_b32_e32 v94, 16, v164
	v_and_b32_e32 v95, 0xffff0000, v164
	v_mul_f32_e32 v94, v62, v94
	v_mul_f32_e32 v95, v62, v95
	v_lshlrev_b32_e32 v154, 16, v163
	v_and_b32_e32 v159, 0xffff0000, v163
	v_cvt_pk_fp8_f32 v167, v94, v95
	v_mul_f32_e32 v154, v62, v154
	v_mul_f32_e32 v159, v62, v159
	v_cvt_pk_fp8_f32 v166, v154, v159 op_sel:[0,0,1]
	v_lshlrev_b32_e32 v154, 16, v165
	v_and_b32_e32 v159, 0xffff0000, v165
	v_mul_f32_e32 v154, v62, v154
	v_mul_f32_e32 v159, v62, v159
	v_cvt_pk_fp8_f32 v167, v154, v159 op_sel:[0,0,1]
	v_add_co_u32_e32 v94, vcc, s39, v90
	s_nop 1
	v_addc_co_u32_e32 v95, vcc, 0, v91, vcc
	global_store_dwordx2 v[94:95], v[166:167], off
	ds_read_b128 v[166:169], v87
	s_waitcnt lgkmcnt(0)
	v_mfma_f32_16x16x32_bf16 v[26:29], v[166:169], v[162:165], v[26:29]
	ds_read_b128 v[166:169], v87 offset:8192
	v_lshl_add_u64 v[90:91], v[90:91], 0, s[18:19]
	s_waitcnt lgkmcnt(0)
	v_mfma_f32_16x16x32_bf16 v[30:33], v[166:169], v[162:165], v[30:33]
	ds_read_b128 v[166:169], v87 offset:16384
	s_waitcnt lgkmcnt(0)
	v_mfma_f32_16x16x32_bf16 v[34:37], v[166:169], v[162:165], v[34:37]
	ds_read_b128 v[166:169], v87 offset:24576
	s_waitcnt lgkmcnt(0)
	v_mfma_f32_16x16x32_bf16 v[38:41], v[166:169], v[162:165], v[38:41]
	ds_read_b128 v[162:165], v152 offset:32768
	s_waitcnt lgkmcnt(0)
	v_lshlrev_b32_e32 v87, 16, v162
	v_and_b32_e32 v152, 0xffff0000, v162
	v_mul_f32_e32 v87, v62, v87
	v_mul_f32_e32 v152, v62, v152
	v_cvt_pk_fp8_f32 v166, v87, v152
	v_lshlrev_b32_e32 v87, 16, v164
	v_and_b32_e32 v152, 0xffff0000, v164
	v_mul_f32_e32 v87, v62, v87
	v_mul_f32_e32 v152, v62, v152
	v_lshlrev_b32_e32 v154, 16, v163
	v_and_b32_e32 v159, 0xffff0000, v163
	v_cvt_pk_fp8_f32 v167, v87, v152
	v_mul_f32_e32 v154, v62, v154
	v_mul_f32_e32 v159, v62, v159
	v_cvt_pk_fp8_f32 v166, v154, v159 op_sel:[0,0,1]
	v_lshlrev_b32_e32 v154, 16, v165
	v_and_b32_e32 v159, 0xffff0000, v165
	v_mul_f32_e32 v154, v62, v154
	v_mul_f32_e32 v159, v62, v159
	v_cvt_pk_fp8_f32 v167, v154, v159 op_sel:[0,0,1]
	global_store_dwordx2 v[94:95], v[166:167], off offset:32
	ds_read_b128 v[166:169], v145
	s_waitcnt lgkmcnt(0)
	v_mfma_f32_16x16x32_bf16 v[26:29], v[166:169], v[162:165], v[26:29]
	ds_read_b128 v[166:169], v145 offset:8192
	s_waitcnt lgkmcnt(0)
	v_mfma_f32_16x16x32_bf16 v[30:33], v[166:169], v[162:165], v[30:33]
	ds_read_b128 v[166:169], v145 offset:16384
	s_waitcnt lgkmcnt(0)
	v_mfma_f32_16x16x32_bf16 v[34:37], v[166:169], v[162:165], v[34:37]
	ds_read_b128 v[166:169], v145 offset:24576
	s_waitcnt lgkmcnt(0)
	v_mfma_f32_16x16x32_bf16 v[38:41], v[166:169], v[162:165], v[38:41]
	ds_read_b128 v[162:165], v153 offset:32768
	ds_read_b128 v[166:169], v146
	s_waitcnt lgkmcnt(1)
; #define GAS __attribute__((address_space(1)))
; #define LAS __attribute__((address_space(3)))
; __device__ __forceinline__ unsigned pk4_fp8(float a, float b, float c, float d) { int w = __builtin_amdgcn_cvt_pk_fp8_f32(a, b, 0, false); w = __builtin_amdgcn_cvt_pk_fp8_f32(c, d, w, true); return (unsigned)w; }
; __device__ __forceinline__ void p7_router(Frame& F, const Args& A) {
;     ...
; #pragma unroll
;                 for (int ks = 0; ks < 8; ++ks) {
;                     const u32x4 c0 = *(const LAS u32x4*)(xbuf + tl * 512 + (((4 * ks + fq) ^ tl) << 4));
;                     *(GAS u32x2*)(xo + 32 * ks) = (u32x2){pk4_fp8(bflo(c0.x) * rr, bfhi(c0.x) * rr, bflo(c0.y) * rr, bfhi(c0.y) * rr), pk4_fp8(bflo(c0.z) * rr, bfhi(c0.z) * rr, bflo(c0.w) * rr, bfhi(c0.w) * rr)};
;                     const bf16x8 f0 = __builtin_bit_cast(bf16x8, c0);
; #pragma unroll
;                     for (int rb = 0; rb < 4; ++rb) { const int rho = 16 * rb + tl; const bf16x8 a = *(const LAS bf16x8*)(Wt + rho * 512 + (((4 * ks + fq) ^ tl) << 4));
;                         acc[rb][g] = __builtin_amdgcn_mfma_f32_16x16x32_bf16(a, f0, acc[rb][g], 0, 0, 0); }
;                 }
	v_lshlrev_b32_e32 v152, 16, v163
	v_lshlrev_b32_e32 v87, 16, v162
	v_and_b32_e32 v145, 0xffff0000, v162
	v_mul_f32_e32 v153, v62, v152
	v_and_b32_e32 v152, 0xffff0000, v163
	v_mul_f32_e32 v87, v62, v87
	v_mul_f32_e32 v145, v62, v145
	v_mul_f32_e32 v154, v62, v152
	v_cvt_pk_fp8_f32 v152, v87, v145
	v_lshlrev_b32_e32 v87, 16, v164
	v_and_b32_e32 v145, 0xffff0000, v164
	v_mul_f32_e32 v87, v62, v87
	v_cvt_pk_fp8_f32 v152, v153, v154 op_sel:[0,0,1]
	v_lshlrev_b32_e32 v153, 16, v165
	v_mul_f32_e32 v154, v62, v153
	v_and_b32_e32 v153, 0xffff0000, v165
	v_mul_f32_e32 v145, v62, v145
	v_mul_f32_e32 v159, v62, v153
	s_waitcnt lgkmcnt(0)
	v_mfma_f32_16x16x32_bf16 v[26:29], v[166:169], v[162:165], v[26:29]
	ds_read_b128 v[166:169], v146 offset:8192
	v_cvt_pk_fp8_f32 v153, v87, v145
	v_cvt_pk_fp8_f32 v153, v154, v159 op_sel:[0,0,1]
	global_store_dwordx2 v[94:95], v[152:153], off offset:64
	ds_read_b128 v[152:155], v155 offset:32768
	s_waitcnt lgkmcnt(1)
	v_mfma_f32_16x16x32_bf16 v[30:33], v[166:169], v[162:165], v[30:33]
	ds_read_b128 v[166:169], v146 offset:16384
	s_waitcnt lgkmcnt(1)
	v_lshlrev_b32_e32 v87, 16, v152
	s_waitcnt lgkmcnt(0)
	v_mfma_f32_16x16x32_bf16 v[34:37], v[166:169], v[162:165], v[34:37]
	ds_read_b128 v[166:169], v146 offset:24576
	v_and_b32_e32 v145, 0xffff0000, v152
	v_mul_f32_e32 v87, v62, v87
	s_waitcnt lgkmcnt(0)
	v_mfma_f32_16x16x32_bf16 v[38:41], v[166:169], v[162:165], v[38:41]
	v_mul_f32_e32 v145, v62, v145
	v_cvt_pk_fp8_f32 v162, v87, v145
	v_lshlrev_b32_e32 v87, 16, v154
	v_and_b32_e32 v145, 0xffff0000, v154
	v_mul_f32_e32 v87, v62, v87
	v_mul_f32_e32 v145, v62, v145
	v_lshlrev_b32_e32 v146, 16, v153
	v_and_b32_e32 v159, 0xffff0000, v153
	v_cvt_pk_fp8_f32 v163, v87, v145
	v_mul_f32_e32 v146, v62, v146
	v_mul_f32_e32 v159, v62, v159
	v_cvt_pk_fp8_f32 v162, v146, v159 op_sel:[0,0,1]
	v_lshlrev_b32_e32 v146, 16, v155
	v_and_b32_e32 v159, 0xffff0000, v155
	v_mul_f32_e32 v146, v62, v146
	v_mul_f32_e32 v159, v62, v159
	v_cvt_pk_fp8_f32 v163, v146, v159 op_sel:[0,0,1]
	global_store_dwordx2 v[94:95], v[162:163], off offset:96
	ds_read_b128 v[162:165], v147
	s_waitcnt lgkmcnt(0)
	v_mfma_f32_16x16x32_bf16 v[26:29], v[162:165], v[152:155], v[26:29]
	ds_read_b128 v[162:165], v147 offset:8192
	s_waitcnt lgkmcnt(0)
	v_mfma_f32_16x16x32_bf16 v[30:33], v[162:165], v[152:155], v[30:33]
	ds_read_b128 v[162:165], v147 offset:16384
	s_waitcnt lgkmcnt(0)
	v_mfma_f32_16x16x32_bf16 v[34:37], v[162:165], v[152:155], v[34:37]
	ds_read_b128 v[162:165], v147 offset:24576
	s_waitcnt lgkmcnt(0)
	v_mfma_f32_16x16x32_bf16 v[38:41], v[162:165], v[152:155], v[38:41]
	ds_read_b128 v[152:155], v156 offset:32768
	ds_read_b128 v[162:165], v148
	s_waitcnt lgkmcnt(1)
	v_lshlrev_b32_e32 v146, 16, v153
	s_waitcnt lgkmcnt(0)
	v_mfma_f32_16x16x32_bf16 v[26:29], v[162:165], v[152:155], v[26:29]
	ds_read_b128 v[162:165], v148 offset:8192
	v_lshlrev_b32_e32 v87, 16, v152
	v_and_b32_e32 v145, 0xffff0000, v152
	s_waitcnt lgkmcnt(0)
	v_mfma_f32_16x16x32_bf16 v[30:33], v[162:165], v[152:155], v[30:33]
	ds_read_b128 v[162:165], v148 offset:16384
	v_mul_f32_e32 v147, v62, v146
	v_and_b32_e32 v146, 0xffff0000, v153
	v_mul_f32_e32 v87, v62, v87
	v_mul_f32_e32 v145, v62, v145
	v_mul_f32_e32 v156, v62, v146
	v_cvt_pk_fp8_f32 v146, v87, v145
	s_waitcnt lgkmcnt(0)
	v_mfma_f32_16x16x32_bf16 v[34:37], v[162:165], v[152:155], v[34:37]
	ds_read_b128 v[162:165], v148 offset:24576
	v_cvt_pk_fp8_f32 v146, v147, v156 op_sel:[0,0,1]
	v_lshlrev_b32_e32 v147, 16, v155
	v_lshlrev_b32_e32 v87, 16, v154
	v_and_b32_e32 v145, 0xffff0000, v154
	v_mul_f32_e32 v156, v62, v147
	v_and_b32_e32 v147, 0xffff0000, v155
	v_mul_f32_e32 v87, v62, v87
	v_mul_f32_e32 v145, v62, v145
	v_mul_f32_e32 v159, v62, v147
	v_cvt_pk_fp8_f32 v147, v87, v145
	s_waitcnt lgkmcnt(0)
	v_mfma_f32_16x16x32_bf16 v[38:41], v[162:165], v[152:155], v[38:41]
	ds_read_b128 v[152:155], v157 offset:32768
	ds_read_b128 v[162:165], v149
	v_cvt_pk_fp8_f32 v147, v156, v159 op_sel:[0,0,1]
	s_waitcnt lgkmcnt(0)
	v_mfma_f32_16x16x32_bf16 v[26:29], v[162:165], v[152:155], v[26:29]
	global_store_dwordx2 v[94:95], v[146:147], off offset:128
	v_lshlrev_b32_e32 v146, 16, v153
	v_lshlrev_b32_e32 v87, 16, v152
	v_and_b32_e32 v145, 0xffff0000, v152
	v_mul_f32_e32 v147, v62, v146
	v_and_b32_e32 v146, 0xffff0000, v153
	v_mul_f32_e32 v87, v62, v87
	v_mul_f32_e32 v145, v62, v145
	v_mul_f32_e32 v148, v62, v146
	v_cvt_pk_fp8_f32 v146, v87, v145
	v_lshlrev_b32_e32 v87, 16, v154
	v_and_b32_e32 v145, 0xffff0000, v154
	v_mul_f32_e32 v87, v62, v87
	v_cvt_pk_fp8_f32 v146, v147, v148 op_sel:[0,0,1]
	v_lshlrev_b32_e32 v147, 16, v155
	v_mul_f32_e32 v148, v62, v147
	v_and_b32_e32 v147, 0xffff0000, v155
	v_mul_f32_e32 v145, v62, v145
	v_mul_f32_e32 v156, v62, v147
	ds_read_b128 v[162:165], v149 offset:8192
	v_cvt_pk_fp8_f32 v147, v87, v145
	s_waitcnt lgkmcnt(0)
; #define GAS __attribute__((address_space(1)))
; #define LAS __attribute__((address_space(3)))
; __device__ __forceinline__ unsigned pk4_fp8(float a, float b, float c, float d) { int w = __builtin_amdgcn_cvt_pk_fp8_f32(a, b, 0, false); w = __builtin_amdgcn_cvt_pk_fp8_f32(c, d, w, true); return (unsigned)w; }
; __device__ __forceinline__ void p7_router(Frame& F, const Args& A) {
;     ...
; #pragma unroll
;                 for (int ks = 0; ks < 8; ++ks) {
;                     const u32x4 c0 = *(const LAS u32x4*)(xbuf + tl * 512 + (((4 * ks + fq) ^ tl) << 4));
;                     *(GAS u32x2*)(xo + 32 * ks) = (u32x2){pk4_fp8(bflo(c0.x) * rr, bfhi(c0.x) * rr, bflo(c0.y) * rr, bfhi(c0.y) * rr), pk4_fp8(bflo(c0.z) * rr, bfhi(c0.z) * rr, bflo(c0.w) * rr, bfhi(c0.w) * rr)};
;                     const bf16x8 f0 = __builtin_bit_cast(bf16x8, c0);
; #pragma unroll
;                     for (int rb = 0; rb < 4; ++rb) { const int rho = 16 * rb + tl; const bf16x8 a = *(const LAS bf16x8*)(Wt + rho * 512 + (((4 * ks + fq) ^ tl) << 4));
;                         acc[rb][g] = __builtin_amdgcn_mfma_f32_16x16x32_bf16(a, f0, acc[rb][g], 0, 0, 0); }
;                 }
;     ...
;         for (int tb = 0; tb < 2; ++tb) {
;             const float r = tb ? r1 : r0; float v[8];
; #pragma unroll
;             for (int j = 0; j < 8; ++j) v[j] = (acc[j >> 2][tb][j & 3] + acc[2 + (j >> 2)][tb][j & 3]) * r + bias[j];
;             int idx[4]; float val[4];
; #pragma unroll
;             for (int k = 0; k < 4; ++k) {
;                 float best = v[0]; int bi = 4 * fq;
; #pragma unroll
;                 for (int j = 1; j < 8; ++j) { const int e = 16 * (j >> 2) + 4 * fq + (j & 3); const bool gt = v[j] > best; best = gt ? v[j] : best; bi = gt ? e : bi; }
; #pragma unroll
;                 for (int o = 16; o <= 32; o <<= 1) { const float ob = __shfl_xor(best, o); const int oi = __shfl_xor(bi, o); const bool take = (ob > best) || (ob == best && oi < bi); best = take ? ob : best; bi = take ? oi : bi; }
	v_mfma_f32_16x16x32_bf16 v[30:33], v[162:165], v[152:155], v[30:33]
	v_cvt_pk_fp8_f32 v147, v148, v156 op_sel:[0,0,1]
	ds_read_b128 v[162:165], v149 offset:16384
	global_store_dwordx2 v[94:95], v[146:147], off offset:160
	ds_read_b128 v[146:149], v149 offset:24576
	s_waitcnt lgkmcnt(0)
	v_mfma_f32_16x16x32_bf16 v[38:41], v[146:149], v[152:155], v[38:41]
	ds_read_b128 v[146:149], v158 offset:32768
	s_waitcnt lgkmcnt(0)
	v_lshlrev_b32_e32 v87, 16, v146
	v_mfma_f32_16x16x32_bf16 v[34:37], v[162:165], v[152:155], v[34:37]
	v_lshlrev_b32_e32 v152, 16, v147
	v_and_b32_e32 v145, 0xffff0000, v146
	v_mul_f32_e32 v153, v62, v152
	v_and_b32_e32 v152, 0xffff0000, v147
	v_mul_f32_e32 v87, v62, v87
	v_mul_f32_e32 v145, v62, v145
	v_mul_f32_e32 v154, v62, v152
	v_cvt_pk_fp8_f32 v152, v87, v145
	v_lshlrev_b32_e32 v87, 16, v148
	v_and_b32_e32 v145, 0xffff0000, v148
	v_mul_f32_e32 v87, v62, v87
	v_cvt_pk_fp8_f32 v152, v153, v154 op_sel:[0,0,1]
	v_lshlrev_b32_e32 v153, 16, v149
	v_mul_f32_e32 v154, v62, v153
	v_and_b32_e32 v153, 0xffff0000, v149
	v_mul_f32_e32 v145, v62, v145
	v_mul_f32_e32 v155, v62, v153
	v_cvt_pk_fp8_f32 v153, v87, v145
	v_cvt_pk_fp8_f32 v153, v154, v155 op_sel:[0,0,1]
	global_store_dwordx2 v[94:95], v[152:153], off offset:192
	ds_read_b128 v[152:155], v150
	s_waitcnt lgkmcnt(0)
	v_mfma_f32_16x16x32_bf16 v[26:29], v[152:155], v[146:149], v[26:29]
	ds_read_b128 v[152:155], v150 offset:8192
	s_waitcnt lgkmcnt(0)
	v_mfma_f32_16x16x32_bf16 v[30:33], v[152:155], v[146:149], v[30:33]
	ds_read_b128 v[152:155], v150 offset:16384
	s_waitcnt lgkmcnt(0)
	v_mfma_f32_16x16x32_bf16 v[34:37], v[152:155], v[146:149], v[34:37]
	ds_read_b128 v[152:155], v150 offset:24576
	s_waitcnt lgkmcnt(0)
	v_mfma_f32_16x16x32_bf16 v[38:41], v[152:155], v[146:149], v[38:41]
	ds_read_b128 v[146:149], v160 offset:32768
	s_waitcnt lgkmcnt(0)
	v_lshlrev_b32_e32 v87, 16, v146
	v_and_b32_e32 v145, 0xffff0000, v146
	v_and_b32_e32 v152, 0xffff0000, v147
	v_mul_f32_e32 v87, v62, v87
	v_mul_f32_e32 v145, v62, v145
	v_mul_f32_e32 v153, v62, v152
	v_cvt_pk_fp8_f32 v152, v87, v145
	v_lshlrev_b32_e32 v150, 16, v147
	v_mul_f32_e32 v150, v62, v150
	v_lshlrev_b32_e32 v87, 16, v148
	v_cvt_pk_fp8_f32 v152, v150, v153 op_sel:[0,0,1]
	v_and_b32_e32 v145, 0xffff0000, v148
	v_and_b32_e32 v153, 0xffff0000, v149
	v_mul_f32_e32 v87, v62, v87
	v_mul_f32_e32 v145, v62, v145
	v_mul_f32_e32 v154, v62, v153
	v_cvt_pk_fp8_f32 v153, v87, v145
	v_lshlrev_b32_e32 v150, 16, v149
	v_mul_f32_e32 v150, v62, v150
	v_cvt_pk_fp8_f32 v153, v150, v154 op_sel:[0,0,1]
	global_store_dwordx2 v[94:95], v[152:153], off offset:224
	ds_read_b128 v[152:155], v151
	s_waitcnt lgkmcnt(0)
	v_mfma_f32_16x16x32_bf16 v[26:29], v[152:155], v[146:149], v[26:29]
	ds_read_b128 v[152:155], v151 offset:8192
	s_waitcnt lgkmcnt(0)
	v_mfma_f32_16x16x32_bf16 v[30:33], v[152:155], v[146:149], v[30:33]
	ds_read_b128 v[152:155], v151 offset:16384
	s_waitcnt lgkmcnt(0)
	v_mfma_f32_16x16x32_bf16 v[34:37], v[152:155], v[146:149], v[34:37]
	ds_read_b128 v[150:153], v151 offset:24576
	s_waitcnt lgkmcnt(0)
	v_mfma_f32_16x16x32_bf16 v[38:41], v[150:153], v[146:149], v[38:41]
	s_cbranch_scc0 .LBB0_839
	s_waitcnt vmcnt(17)
	v_add_f32_e32 v12, v44, v52
	v_and_b32_e32 v10, 64, v141
	s_waitcnt vmcnt(16)
	v_fma_f32 v17, v92, v12, v4
	v_add_f32_e32 v12, v45, v53
	v_add_u32_e32 v13, 64, v10
	v_pk_add_f32 v[10:11], v[42:43], v[50:51]
	v_fma_f32 v18, v92, v12, v5
	v_add_f32_e32 v12, v46, v54
	v_pk_fma_f32 v[10:11], v[92:93], v[10:11], v[2:3] op_sel_hi:[0,1,1]
	v_fma_f32 v19, v92, v12, v6
	v_add_f32_e32 v12, v47, v55
	v_fma_f32 v20, v92, v12, v7
	v_add_f32_e32 v12, v48, v56
	v_cmp_gt_f32_e32 vcc, v11, v10
	v_fma_f32 v21, v92, v12, v8
	v_add_f32_e32 v12, v49, v57
	v_cndmask_b32_e32 v14, v10, v11, vcc
	v_fma_f32 v22, v92, v12, v9
	v_cndmask_b32_e32 v12, v60, v1, vcc
	v_cmp_gt_f32_e32 vcc, v17, v14
	s_mov_b64 s[20:21], -1
	s_mov_b64 s[4:5], -1
	v_cndmask_b32_e32 v14, v14, v17, vcc
	v_cndmask_b32_e32 v12, v12, v61, vcc
	v_cmp_gt_f32_e32 vcc, v18, v14
	s_nop 1
	v_cndmask_b32_e32 v14, v14, v18, vcc
	v_cndmask_b32_e32 v12, v12, v89, vcc
	v_cmp_gt_f32_e32 vcc, v19, v14
	s_nop 1
	v_cndmask_b32_e32 v14, v14, v19, vcc
	v_cndmask_b32_e32 v12, v12, v108, vcc
	v_cmp_gt_f32_e32 vcc, v20, v14
	s_nop 1
	v_cndmask_b32_e32 v14, v14, v20, vcc
	v_cndmask_b32_e32 v12, v12, v109, vcc
	v_cmp_gt_f32_e32 vcc, v21, v14
	s_nop 1
	v_cndmask_b32_e32 v15, v14, v21, vcc
	v_cndmask_b32_e32 v12, v12, v110, vcc
	v_cmp_gt_f32_e32 vcc, v22, v15
	s_nop 1
	v_cndmask_b32_e32 v14, v12, v111, vcc
	v_xor_b32_e32 v12, 16, v141
	v_cndmask_b32_e32 v15, v15, v22, vcc
	v_cmp_lt_i32_e32 vcc, v12, v13
	s_nop 1
	v_cndmask_b32_e32 v12, v141, v12, vcc
	v_lshlrev_b32_e32 v12, 2, v12
	ds_bpermute_b32 v16, v12, v15
	ds_bpermute_b32 v23, v12, v14
	s_waitcnt lgkmcnt(1)
	v_cmp_nlt_f32_e32 vcc, v15, v16
	s_and_saveexec_b64 s[22:23], vcc
	s_cbranch_execz .LBB0_842
	v_cmp_eq_f32_e32 vcc, v15, v16
	s_waitcnt lgkmcnt(0)
	v_cmp_lt_i32_e64 s[4:5], v23, v14
	s_and_b64 s[4:5], vcc, s[4:5]
	s_orn2_b64 s[4:5], s[4:5], exec

; __device__ __forceinline__ unsigned pk4_fp8(float a, float b, float c, float d) { int w = __builtin_amdgcn_cvt_pk_fp8_f32(a, b, 0, false); w = __builtin_amdgcn_cvt_pk_fp8_f32(c, d, w, true); return (unsigned)w; }
;     static __device__ __forceinline__ f32x2 act2(f32x2 g, f32x2 u) {
;         g.x = __builtin_amdgcn_fmed3f(g.x, -24.0f, 7.0f); g.y = __builtin_amdgcn_fmed3f(g.y, -24.0f, 7.0f);
;         u.x = __builtin_amdgcn_fmed3f(u.x, -7.0f, 7.0f); u.y = __builtin_amdgcn_fmed3f(u.y, -7.0f, 7.0f);
;         f32x2 z = g * (-1.702f * 1.4426950408889634f);
;         f32x2 d; d.x = __builtin_amdgcn_exp2f(z.x); d.y = __builtin_amdgcn_exp2f(z.y);
;         d = d + 1.0f;
;         const float r = __builtin_amdgcn_rcpf(d.x * d.y);
;         f32x2 sg; sg.x = r * d.y; sg.y = r * d.x;
;         return (u + 1.0f) * (g * sg);
;     }
;     __device__ __forceinline__ void operator()(const f32x4 (&acc)[2][2][4][2], const pg8::Unit& u, int wr, int wc, int fr, int fq) const {
;         const int e = u.aux;
;         unsigned char* Ht = ws + WS_H2 + (size_t)u.pm * TSF8;
;         const int hc = u.pn * 128 + wc * 32 + 8 * fq;
;         const f32x4 bg0 = *(const f32x4*)(bgate + e * FF + hc), bg1 = *(const f32x4*)(bgate + e * FF + hc + 4);
;         const f32x4 bu0 = *(const f32x4*)(bup + e * FF + hc), bu1 = *(const f32x4*)(bup + e * FF + hc + 4);
; #pragma unroll
;         for (int ai = 0; ai < 2; ++ai)
; #pragma unroll
;             for (int m = 0; m < 4; ++m) { const int rl = ai * 128 + wr * 64 + m * 16 + fr;
;                 const f32x4 g0 = acc[ai][0][m][0] * (1.0f / 64.0f) + bg0, g1 = acc[ai][0][m][1] * (1.0f / 64.0f) + bg1, u0 = acc[ai][1][m][0] * (1.0f / 64.0f) + bu0, u1 = acc[ai][1][m][1] * (1.0f / 64.0f) + bu1;
;                 const f32x2 h0 = act2((f32x2){g0[0], g0[1]}, (f32x2){u0[0], u0[1]}), h1 = act2((f32x2){g0[2], g0[3]}, (f32x2){u0[2], u0[3]});
;                 const f32x2 h2 = act2((f32x2){g1[0], g1[1]}, (f32x2){u1[0], u1[1]}), h3 = act2((f32x2){g1[2], g1[3]}, (f32x2){u1[2], u1[3]});
;                 *(u32x2*)(Ht + (size_t)rl * FF + hc) = (u32x2){pk4_fp8(h0.x, h0.y, h1.x, h1.y), pk4_fp8(h2.x, h2.y, h3.x, h3.y)}; }
.Lmy_nobar0:
	v_pk_fma_f32 v[218:219], v[218:219], v[238:239], v[238:239] op_sel:[0,0,1] op_sel_hi:[1,0,1]
	v_pk_fma_f32 v[220:221], v[220:221], v[238:239], v[238:239] op_sel:[0,0,1] op_sel_hi:[1,0,1]
	v_pk_fma_f32 v[222:223], v[222:223], v[238:239], v[238:239] op_sel:[0,0,1] op_sel_hi:[1,0,1]
	v_pk_fma_f32 v[224:225], v[224:225], v[238:239], v[238:239] op_sel:[0,0,1] op_sel_hi:[1,0,1]
	v_pk_fma_f32 v[214:215], v[214:215], v[240:241], v[240:241] op_sel:[0,0,1] op_sel_hi:[1,0,1]
	v_pk_fma_f32 v[216:217], v[216:217], v[240:241], v[240:241] op_sel:[0,0,1] op_sel_hi:[1,0,1]
	v_pk_fma_f32 v[226:227], v[226:227], v[240:241], v[240:241] op_sel:[0,0,1] op_sel_hi:[1,0,1]
	v_pk_fma_f32 v[228:229], v[228:229], v[240:241], v[240:241] op_sel:[0,0,1] op_sel_hi:[1,0,1]
	s_ashr_i32 s23, s22, 31
	s_lshl_b64 s[22:23], s[22:23], 18
	v_mov_b32_e32 v24, v0
	s_add_u32 s22, s46, s22
	s_addc_u32 s23, s47, s23
	s_lshl_b32 s24, s62, 7
	v_lshrrev_b32_e32 v6, 1, v24
	v_and_or_b32 v6, v6, 24, s24
	s_lshl_b32 s24, s61, 10
	s_ashr_i32 s25, s24, 31
	v_or_b32_e32 v22, s45, v6
	s_lshl_b64 s[24:25], s[24:25], 2
	s_add_u32 s26, s84, s24
	v_ashrrev_i32_e32 v23, 31, v22
	s_addc_u32 s27, s85, s25
	v_lshlrev_b64 v[6:7], 2, v[22:23]
	v_lshl_add_u64 v[8:9], s[26:27], 0, v[6:7]
	s_add_u32 s24, s88, s24
	s_addc_u32 s25, s89, s25
	v_lshl_add_u64 v[6:7], s[24:25], 0, v[6:7]
	s_nop 0
	v_and_or_b32 v26, v24, 15, s44
	v_ashrrev_i32_e32 v27, 31, v26
	v_lshlrev_b64 v[32:33], 10, v[26:27]
	v_lshl_add_u64 v[24:25], s[22:23], 0, v[22:23]
	v_lshl_add_u64 v[22:23], v[24:25], 0, v[32:33]
	v_or_b32_e32 v30, 16, v26
	v_pk_fma_f32 v[34:35], v[186:187], v[242:243], v[222:223] op_sel_hi:[1,0,1] clamp
	s_nop 0
	v_pk_fma_f32 v[34:35], v[34:35], v[234:235], v[234:235] op_sel:[0,0,1] op_sel_hi:[1,0,1]
	v_pk_mul_f32 v[56:57], v[34:35], s[18:19] op_sel_hi:[1,0]
	v_pk_fma_f32 v[32:33], v[188:189], v[242:243], v[224:225] op_sel_hi:[1,0,1] clamp
	v_exp_f32_e32 v56, v56
	v_exp_f32_e32 v57, v57
	v_pk_fma_f32 v[38:39], v[194:195], v[242:243], v[218:219] op_sel_hi:[1,0,1] clamp
	v_pk_fma_f32 v[32:33], v[32:33], v[234:235], v[234:235] op_sel:[0,0,1] op_sel_hi:[1,0,1]
	v_pk_fma_f32 v[38:39], v[38:39], v[234:235], v[234:235] op_sel:[0,0,1] op_sel_hi:[1,0,1]
	v_pk_mul_f32 v[58:59], v[32:33], s[18:19] op_sel_hi:[1,0]
	v_pk_mul_f32 v[60:61], v[38:39], s[18:19] op_sel_hi:[1,0]
	v_exp_f32_e32 v58, v58
	v_exp_f32_e32 v59, v59
	v_exp_f32_e32 v60, v60
	v_exp_f32_e32 v61, v61
	v_pk_add_f32 v[56:57], v[56:57], 1.0 op_sel_hi:[1,0]
	v_pk_fma_f32 v[36:37], v[196:197], v[242:243], v[220:221] op_sel_hi:[1,0,1] clamp
	v_mul_f32_e32 v27, v56, v57
	v_pk_fma_f32 v[36:37], v[36:37], v[234:235], v[234:235] op_sel:[0,0,1] op_sel_hi:[1,0,1]
	v_pk_fma_f32 v[64:65], v[172:173], v[242:243], v[228:229] op_sel:[0,1,0] op_sel_hi:[1,1,1] clamp
	v_rcp_f32_e32 v172, v27
	v_pk_mul_f32 v[62:63], v[36:37], s[18:19] op_sel_hi:[1,0]
	v_pk_add_f32 v[58:59], v[58:59], 1.0 op_sel_hi:[1,0]
	v_exp_f32_e32 v62, v62
	v_exp_f32_e32 v63, v63
	v_pk_add_f32 v[60:61], v[60:61], 1.0 op_sel_hi:[1,0]
	v_pk_fma_f32 v[50:51], v[174:175], v[242:243], v[226:227] op_sel:[0,1,0] op_sel_hi:[1,1,1] clamp
	v_mul_f32_e32 v31, v58, v59
	v_mul_f32_e32 v173, v60, v61
	v_pk_fma_f32 v[50:51], v[50:51], v[236:237], v[236:237] op_sel:[0,0,1] op_sel_hi:[1,0,1]
	v_rcp_f32_e32 v174, v31
	v_pk_mul_f32 v[56:57], v[56:57], v[172:173] op_sel:[1,0] op_sel_hi:[0,0]
	v_pk_mul_f32 v[34:35], v[34:35], v[56:57]
	v_pk_add_f32 v[62:63], v[62:63], 1.0 op_sel_hi:[1,0]
	v_pk_mul_f32 v[34:35], v[50:51], v[34:35]
	v_pk_fma_f32 v[48:49], v[176:177], v[242:243], v[228:229] op_sel:[0,1,0] op_sel_hi:[1,1,1] clamp
	v_mul_f32_e32 v175, v62, v63
	v_cvt_pk_fp8_f32 v28, v34, v35
	v_pk_fma_f32 v[48:49], v[48:49], v[236:237], v[236:237] op_sel:[0,0,1] op_sel_hi:[1,0,1]
	v_pk_mul_f32 v[58:59], v[58:59], v[174:175] op_sel:[1,0] op_sel_hi:[0,0]
	v_pk_fma_f32 v[42:43], v[190:191], v[242:243], v[222:223] op_sel_hi:[1,0,1] clamp
	v_rcp_f32_e32 v176, v173
	v_pk_mul_f32 v[32:33], v[32:33], v[58:59]
	v_pk_fma_f32 v[42:43], v[42:43], v[234:235], v[234:235] op_sel:[0,0,1] op_sel_hi:[1,0,1]
	v_pk_mul_f32 v[32:33], v[48:49], v[32:33]
	v_pk_fma_f32 v[54:55], v[178:179], v[242:243], v[214:215] op_sel:[0,1,0] op_sel_hi:[1,1,1] clamp
	v_cvt_pk_fp8_f32 v28, v32, v33 op_sel:[0,0,1]
	v_pk_mul_f32 v[32:33], v[42:43], s[18:19] op_sel_hi:[1,0]
	v_rcp_f32_e32 v178, v175
	v_exp_f32_e32 v32, v32
	v_exp_f32_e32 v33, v33
	v_pk_fma_f32 v[54:55], v[54:55], v[236:237], v[236:237] op_sel:[0,0,1] op_sel_hi:[1,0,1]
	v_pk_mul_f32 v[60:61], v[60:61], v[176:177] op_sel:[1,0] op_sel_hi:[0,0]
	v_pk_mul_f32 v[38:39], v[38:39], v[60:61]
	v_pk_fma_f32 v[40:41], v[192:193], v[242:243], v[224:225] op_sel_hi:[1,0,1] clamp
	v_pk_fma_f32 v[52:53], v[180:181], v[242:243], v[216:217] op_sel:[0,1,0] op_sel_hi:[1,1,1] clamp
	v_pk_mul_f32 v[38:39], v[54:55], v[38:39]
	v_pk_fma_f32 v[52:53], v[52:53], v[236:237], v[236:237] op_sel:[0,0,1] op_sel_hi:[1,0,1]
	v_pk_mul_f32 v[62:63], v[62:63], v[178:179] op_sel:[1,0] op_sel_hi:[0,0]
	v_cvt_pk_fp8_f32 v29, v38, v39
	v_pk_add_f32 v[32:33], v[32:33], 1.0 op_sel_hi:[1,0]
	v_pk_fma_f32 v[38:39], v[40:41], v[234:235], v[234:235] op_sel:[0,0,1] op_sel_hi:[1,0,1]
	v_pk_mul_f32 v[36:37], v[36:37], v[62:63]
	v_mul_f32_e32 v27, v32, v33
	v_pk_mul_f32 v[40:41], v[38:39], s[18:19] op_sel_hi:[1,0]
	v_pk_mul_f32 v[34:35], v[52:53], v[36:37]
	v_rcp_f32_e32 v36, v27
	v_exp_f32_e32 v40, v40
	v_exp_f32_e32 v41, v41
	v_pk_fma_f32 v[46:47], v[182:183], v[242:243], v[218:219] op_sel_hi:[1,0,1] clamp
	v_pk_mul_f32 v[32:33], v[32:33], v[36:37] op_sel:[1,0] op_sel_hi:[0,0]
	v_pk_fma_f32 v[170:171], v[170:171], v[242:243], v[226:227] op_sel:[0,1,0] op_sel_hi:[1,1,1] clamp
; __device__ __forceinline__ unsigned pk4_fp8(float a, float b, float c, float d) { int w = __builtin_amdgcn_cvt_pk_fp8_f32(a, b, 0, false); w = __builtin_amdgcn_cvt_pk_fp8_f32(c, d, w, true); return (unsigned)w; }
;     static __device__ __forceinline__ f32x2 act2(f32x2 g, f32x2 u) {
;         g.x = __builtin_amdgcn_fmed3f(g.x, -24.0f, 7.0f); g.y = __builtin_amdgcn_fmed3f(g.y, -24.0f, 7.0f);
;         u.x = __builtin_amdgcn_fmed3f(u.x, -7.0f, 7.0f); u.y = __builtin_amdgcn_fmed3f(u.y, -7.0f, 7.0f);
;         f32x2 z = g * (-1.702f * 1.4426950408889634f);
;         f32x2 d; d.x = __builtin_amdgcn_exp2f(z.x); d.y = __builtin_amdgcn_exp2f(z.y);
;         d = d + 1.0f;
;         const float r = __builtin_amdgcn_rcpf(d.x * d.y);
;         f32x2 sg; sg.x = r * d.y; sg.y = r * d.x;
;         return (u + 1.0f) * (g * sg);
;     }
;     __device__ __forceinline__ void operator()(const f32x4 (&acc)[2][2][4][2], const pg8::Unit& u, int wr, int wc, int fr, int fq) const {
;         const int e = u.aux;
;         unsigned char* Ht = ws + WS_H2 + (size_t)u.pm * TSF8;
;         const int hc = u.pn * 128 + wc * 32 + 8 * fq;
;         const f32x4 bg0 = *(const f32x4*)(bgate + e * FF + hc), bg1 = *(const f32x4*)(bgate + e * FF + hc + 4);
;         const f32x4 bu0 = *(const f32x4*)(bup + e * FF + hc), bu1 = *(const f32x4*)(bup + e * FF + hc + 4);
; #pragma unroll
;         for (int ai = 0; ai < 2; ++ai)
; #pragma unroll
;             for (int m = 0; m < 4; ++m) { const int rl = ai * 128 + wr * 64 + m * 16 + fr;
;                 const f32x4 g0 = acc[ai][0][m][0] * (1.0f / 64.0f) + bg0, g1 = acc[ai][0][m][1] * (1.0f / 64.0f) + bg1, u0 = acc[ai][1][m][0] * (1.0f / 64.0f) + bu0, u1 = acc[ai][1][m][1] * (1.0f / 64.0f) + bu1;
;                 const f32x2 h0 = act2((f32x2){g0[0], g0[1]}, (f32x2){u0[0], u0[1]}), h1 = act2((f32x2){g0[2], g0[3]}, (f32x2){u0[2], u0[3]});
;                 const f32x2 h2 = act2((f32x2){g1[0], g1[1]}, (f32x2){u1[0], u1[1]}), h3 = act2((f32x2){g1[2], g1[3]}, (f32x2){u1[2], u1[3]});
;                 *(u32x2*)(Ht + (size_t)rl * FF + hc) = (u32x2){pk4_fp8(h0.x, h0.y, h1.x, h1.y), pk4_fp8(h2.x, h2.y, h3.x, h3.y)}; }
	v_pk_add_f32 v[36:37], v[40:41], 1.0 op_sel_hi:[1,0]
	v_cvt_pk_fp8_f32 v29, v34, v35 op_sel:[0,0,1]
	v_mul_f32_e32 v27, v36, v37
	v_rcp_f32_e32 v40, v27
	v_pk_fma_f32 v[34:35], v[170:171], v[236:237], v[236:237] op_sel:[0,0,1] op_sel_hi:[1,0,1]
	v_pk_mul_f32 v[36:37], v[36:37], v[40:41] op_sel:[1,0] op_sel_hi:[0,0]
	v_pk_mul_f32 v[36:37], v[38:39], v[36:37]
	v_pk_fma_f32 v[38:39], v[46:47], v[234:235], v[234:235] op_sel:[0,0,1] op_sel_hi:[1,0,1]
	v_pk_mul_f32 v[40:41], v[38:39], s[18:19] op_sel_hi:[1,0]
	v_pk_mul_f32 v[32:33], v[42:43], v[32:33]
	v_exp_f32_e32 v40, v40
	v_exp_f32_e32 v41, v41
	v_pk_mul_f32 v[32:33], v[34:35], v[32:33]
	v_pk_fma_f32 v[34:35], v[64:65], v[236:237], v[236:237] op_sel:[0,0,1] op_sel_hi:[1,0,1]
	v_pk_fma_f32 v[44:45], v[184:185], v[242:243], v[220:221] op_sel_hi:[1,0,1] clamp
	v_pk_mul_f32 v[34:35], v[34:35], v[36:37]
	v_pk_add_f32 v[36:37], v[40:41], 1.0 op_sel_hi:[1,0]
	v_pk_fma_f32 v[42:43], v[44:45], v[234:235], v[234:235] op_sel:[0,0,1] op_sel_hi:[1,0,1]
	v_mul_f32_e32 v27, v36, v37
	v_rcp_f32_e32 v40, v27
	v_pk_mul_f32 v[44:45], v[42:43], s[18:19] op_sel_hi:[1,0]
	global_store_dwordx2 v[22:23], v[28:29], off
	v_exp_f32_e32 v44, v44
	v_exp_f32_e32 v45, v45
	v_pk_mul_f32 v[36:37], v[36:37], v[40:41] op_sel:[1,0] op_sel_hi:[0,0]
	v_pk_mul_f32 v[36:37], v[38:39], v[36:37]
	v_pk_fma_f32 v[28:29], v[166:167], v[242:243], v[214:215] op_sel:[0,1,0] op_sel_hi:[1,1,1] clamp
	v_pk_add_f32 v[38:39], v[44:45], 1.0 op_sel_hi:[1,0]
	v_pk_fma_f32 v[28:29], v[28:29], v[236:237], v[236:237] op_sel:[0,0,1] op_sel_hi:[1,0,1]
	v_mul_f32_e32 v27, v38, v39
	v_rcp_f32_e32 v40, v27
	v_pk_fma_f32 v[168:169], v[168:169], v[242:243], v[216:217] op_sel:[0,1,0] op_sel_hi:[1,1,1] clamp
	v_pk_mul_f32 v[38:39], v[38:39], v[40:41] op_sel:[1,0] op_sel_hi:[0,0]
	v_cvt_pk_fp8_f32 v40, v32, v33
	v_pk_fma_f32 v[32:33], v[154:155], v[242:243], v[222:223] op_sel_hi:[1,0,1] clamp
	v_pk_mul_f32 v[28:29], v[28:29], v[36:37]
	v_pk_fma_f32 v[32:33], v[32:33], v[234:235], v[234:235] op_sel:[0,0,1] op_sel_hi:[1,0,1]
	v_pk_mul_f32 v[44:45], v[32:33], s[18:19] op_sel_hi:[1,0]
	v_cvt_pk_fp8_f32 v41, v28, v29
	v_exp_f32_e32 v44, v44
	v_exp_f32_e32 v45, v45
	v_pk_fma_f32 v[36:37], v[168:169], v[236:237], v[236:237] op_sel:[0,0,1] op_sel_hi:[1,0,1]
	v_pk_mul_f32 v[28:29], v[42:43], v[38:39]
	v_ashrrev_i32_e32 v31, 31, v30
	v_pk_mul_f32 v[28:29], v[36:37], v[28:29]
	v_pk_add_f32 v[44:45], v[44:45], 1.0 op_sel_hi:[1,0]
	v_cvt_pk_fp8_f32 v41, v28, v29 op_sel:[0,0,1]
	v_lshlrev_b64 v[28:29], 10, v[30:31]
	v_pk_fma_f32 v[30:31], v[156:157], v[242:243], v[224:225] op_sel_hi:[1,0,1] clamp
	v_mul_f32_e32 v27, v44, v45
	v_pk_fma_f32 v[30:31], v[30:31], v[234:235], v[234:235] op_sel:[0,0,1] op_sel_hi:[1,0,1]
	v_rcp_f32_e32 v48, v27
	v_pk_mul_f32 v[50:51], v[30:31], s[18:19] op_sel_hi:[1,0]
	v_cvt_pk_fp8_f32 v40, v34, v35 op_sel:[0,0,1]
	v_exp_f32_e32 v50, v50
	v_exp_f32_e32 v51, v51
	v_pk_mul_f32 v[44:45], v[44:45], v[48:49] op_sel:[1,0] op_sel_hi:[0,0]
	v_pk_mul_f32 v[32:33], v[32:33], v[44:45]
	v_lshl_add_u64 v[28:29], v[24:25], 0, v[28:29]
	v_pk_add_f32 v[44:45], v[50:51], 1.0 op_sel_hi:[1,0]
	global_store_dwordx2 v[28:29], v[40:41], off
	v_mul_f32_e32 v27, v44, v45
	v_rcp_f32_e32 v48, v27
	v_pk_fma_f32 v[40:41], v[162:163], v[242:243], v[226:227] op_sel:[0,1,0] op_sel_hi:[1,1,1] clamp
	v_pk_fma_f32 v[36:37], v[150:151], v[242:243], v[218:219] op_sel_hi:[1,0,1] clamp
	v_pk_fma_f32 v[40:41], v[40:41], v[236:237], v[236:237] op_sel:[0,0,1] op_sel_hi:[1,0,1]
	v_pk_fma_f32 v[36:37], v[36:37], v[234:235], v[234:235] op_sel:[0,0,1] op_sel_hi:[1,0,1]
	v_pk_mul_f32 v[32:33], v[40:41], v[32:33]
	v_pk_mul_f32 v[40:41], v[44:45], v[48:49] op_sel:[1,0] op_sel_hi:[0,0]
	v_pk_mul_f32 v[30:31], v[30:31], v[40:41]
	v_pk_mul_f32 v[40:41], v[36:37], s[18:19] op_sel_hi:[1,0]
	v_pk_fma_f32 v[38:39], v[164:165], v[242:243], v[228:229] op_sel:[0,1,0] op_sel_hi:[1,1,1] clamp
	v_exp_f32_e32 v40, v40
	v_exp_f32_e32 v41, v41
	v_pk_fma_f32 v[34:35], v[152:153], v[242:243], v[220:221] op_sel_hi:[1,0,1] clamp
	v_pk_fma_f32 v[38:39], v[38:39], v[236:237], v[236:237] op_sel:[0,0,1] op_sel_hi:[1,0,1]
	v_pk_add_f32 v[40:41], v[40:41], 1.0 op_sel_hi:[1,0]
	v_pk_fma_f32 v[46:47], v[158:159], v[242:243], v[214:215] op_sel:[0,1,0] op_sel_hi:[1,1,1] clamp
	v_mul_f32_e32 v27, v40, v41
	v_pk_fma_f32 v[34:35], v[34:35], v[234:235], v[234:235] op_sel:[0,0,1] op_sel_hi:[1,0,1]
	v_pk_mul_f32 v[30:31], v[38:39], v[30:31]
	v_pk_fma_f32 v[38:39], v[46:47], v[236:237], v[236:237] op_sel:[0,0,1] op_sel_hi:[1,0,1]
	v_rcp_f32_e32 v44, v27
	v_pk_mul_f32 v[46:47], v[34:35], s[18:19] op_sel_hi:[1,0]
	v_pk_fma_f32 v[42:43], v[160:161], v[242:243], v[216:217] op_sel:[0,1,0] op_sel_hi:[1,1,1] clamp
	v_exp_f32_e32 v46, v46
	v_exp_f32_e32 v47, v47
	v_pk_mul_f32 v[40:41], v[40:41], v[44:45] op_sel:[1,0] op_sel_hi:[0,0]
	v_pk_mul_f32 v[36:37], v[36:37], v[40:41]
	v_pk_add_f32 v[40:41], v[46:47], 1.0 op_sel_hi:[1,0]
	v_pk_mul_f32 v[36:37], v[38:39], v[36:37]
	v_mul_f32_e32 v27, v40, v41
	v_rcp_f32_e32 v44, v27
	v_pk_fma_f32 v[38:39], v[42:43], v[236:237], v[236:237] op_sel:[0,0,1] op_sel_hi:[1,0,1]
	v_cvt_pk_fp8_f32 v42, v32, v33
	v_cvt_pk_fp8_f32 v43, v36, v37
	v_pk_mul_f32 v[40:41], v[40:41], v[44:45] op_sel:[1,0] op_sel_hi:[0,0]
	v_pk_mul_f32 v[32:33], v[34:35], v[40:41]
	v_or_b32_e32 v28, 32, v26
	v_pk_mul_f32 v[32:33], v[38:39], v[32:33]
	v_cvt_pk_fp8_f32 v42, v30, v31 op_sel:[0,0,1]
	v_cvt_pk_fp8_f32 v43, v32, v33 op_sel:[0,0,1]
	v_ashrrev_i32_e32 v29, 31, v28
	v_lshlrev_b64 v[28:29], 10, v[28:29]
	v_pk_fma_f32 v[30:31], v[138:139], v[242:243], v[222:223] op_sel_hi:[1,0,1] clamp
	v_lshl_add_u64 v[28:29], v[24:25], 0, v[28:29]
; __device__ __forceinline__ unsigned pk4_fp8(float a, float b, float c, float d) { int w = __builtin_amdgcn_cvt_pk_fp8_f32(a, b, 0, false); w = __builtin_amdgcn_cvt_pk_fp8_f32(c, d, w, true); return (unsigned)w; }
;     static __device__ __forceinline__ f32x2 act2(f32x2 g, f32x2 u) {
;         g.x = __builtin_amdgcn_fmed3f(g.x, -24.0f, 7.0f); g.y = __builtin_amdgcn_fmed3f(g.y, -24.0f, 7.0f);
;         u.x = __builtin_amdgcn_fmed3f(u.x, -7.0f, 7.0f); u.y = __builtin_amdgcn_fmed3f(u.y, -7.0f, 7.0f);
;         f32x2 z = g * (-1.702f * 1.4426950408889634f);
;         f32x2 d; d.x = __builtin_amdgcn_exp2f(z.x); d.y = __builtin_amdgcn_exp2f(z.y);
;         d = d + 1.0f;
;         const float r = __builtin_amdgcn_rcpf(d.x * d.y);
;         f32x2 sg; sg.x = r * d.y; sg.y = r * d.x;
;         return (u + 1.0f) * (g * sg);
;     }
;     __device__ __forceinline__ void operator()(const f32x4 (&acc)[2][2][4][2], const pg8::Unit& u, int wr, int wc, int fr, int fq) const {
;         const int e = u.aux;
;         unsigned char* Ht = ws + WS_H2 + (size_t)u.pm * TSF8;
;         const int hc = u.pn * 128 + wc * 32 + 8 * fq;
;         const f32x4 bg0 = *(const f32x4*)(bgate + e * FF + hc), bg1 = *(const f32x4*)(bgate + e * FF + hc + 4);
;         const f32x4 bu0 = *(const f32x4*)(bup + e * FF + hc), bu1 = *(const f32x4*)(bup + e * FF + hc + 4);
; #pragma unroll
;         for (int ai = 0; ai < 2; ++ai)
; #pragma unroll
;             for (int m = 0; m < 4; ++m) { const int rl = ai * 128 + wr * 64 + m * 16 + fr;
;                 const f32x4 g0 = acc[ai][0][m][0] * (1.0f / 64.0f) + bg0, g1 = acc[ai][0][m][1] * (1.0f / 64.0f) + bg1, u0 = acc[ai][1][m][0] * (1.0f / 64.0f) + bu0, u1 = acc[ai][1][m][1] * (1.0f / 64.0f) + bu1;
;                 const f32x2 h0 = act2((f32x2){g0[0], g0[1]}, (f32x2){u0[0], u0[1]}), h1 = act2((f32x2){g0[2], g0[3]}, (f32x2){u0[2], u0[3]});
;                 const f32x2 h2 = act2((f32x2){g1[0], g1[1]}, (f32x2){u1[0], u1[1]}), h3 = act2((f32x2){g1[2], g1[3]}, (f32x2){u1[2], u1[3]});
;                 *(u32x2*)(Ht + (size_t)rl * FF + hc) = (u32x2){pk4_fp8(h0.x, h0.y, h1.x, h1.y), pk4_fp8(h2.x, h2.y, h3.x, h3.y)}; }
	v_pk_fma_f32 v[30:31], v[30:31], v[234:235], v[234:235] op_sel:[0,0,1] op_sel_hi:[1,0,1]
	global_store_dwordx2 v[28:29], v[42:43], off
	v_pk_mul_f32 v[42:43], v[30:31], s[18:19] op_sel_hi:[1,0]
	v_pk_fma_f32 v[28:29], v[140:141], v[242:243], v[224:225] op_sel_hi:[1,0,1] clamp
	v_exp_f32_e32 v42, v42
	v_exp_f32_e32 v43, v43
	v_pk_fma_f32 v[28:29], v[28:29], v[234:235], v[234:235] op_sel:[0,0,1] op_sel_hi:[1,0,1]
	v_pk_mul_f32 v[48:49], v[28:29], s[18:19] op_sel_hi:[1,0]
	v_pk_add_f32 v[42:43], v[42:43], 1.0 op_sel_hi:[1,0]
	v_exp_f32_e32 v48, v48
	v_mul_f32_e32 v27, v42, v43
	v_rcp_f32_e32 v46, v27
	v_exp_f32_e32 v49, v49
	v_pk_fma_f32 v[38:39], v[146:147], v[242:243], v[226:227] op_sel:[0,1,0] op_sel_hi:[1,1,1] clamp
	v_pk_fma_f32 v[34:35], v[134:135], v[242:243], v[218:219] op_sel_hi:[1,0,1] clamp
	v_pk_mul_f32 v[42:43], v[42:43], v[46:47] op_sel:[1,0] op_sel_hi:[0,0]
	v_pk_mul_f32 v[30:31], v[30:31], v[42:43]
	v_pk_add_f32 v[42:43], v[48:49], 1.0 op_sel_hi:[1,0]
	v_pk_fma_f32 v[38:39], v[38:39], v[236:237], v[236:237] op_sel:[0,0,1] op_sel_hi:[1,0,1]
	v_mul_f32_e32 v27, v42, v43
	v_rcp_f32_e32 v46, v27
	v_pk_fma_f32 v[34:35], v[34:35], v[234:235], v[234:235] op_sel:[0,0,1] op_sel_hi:[1,0,1]
	v_pk_mul_f32 v[30:31], v[38:39], v[30:31]
	v_pk_mul_f32 v[38:39], v[42:43], v[46:47] op_sel:[1,0] op_sel_hi:[0,0]
	v_pk_mul_f32 v[28:29], v[28:29], v[38:39]
	v_pk_mul_f32 v[38:39], v[34:35], s[18:19] op_sel_hi:[1,0]
	v_pk_fma_f32 v[36:37], v[148:149], v[242:243], v[228:229] op_sel:[0,1,0] op_sel_hi:[1,1,1] clamp
	v_exp_f32_e32 v38, v38
	v_exp_f32_e32 v39, v39
	v_pk_fma_f32 v[32:33], v[136:137], v[242:243], v[220:221] op_sel_hi:[1,0,1] clamp
	v_pk_fma_f32 v[36:37], v[36:37], v[236:237], v[236:237] op_sel:[0,0,1] op_sel_hi:[1,0,1]
	v_pk_add_f32 v[38:39], v[38:39], 1.0 op_sel_hi:[1,0]
	v_pk_fma_f32 v[44:45], v[142:143], v[242:243], v[214:215] op_sel:[0,1,0] op_sel_hi:[1,1,1] clamp
	v_mul_f32_e32 v27, v38, v39
	v_pk_fma_f32 v[32:33], v[32:33], v[234:235], v[234:235] op_sel:[0,0,1] op_sel_hi:[1,0,1]
	v_pk_mul_f32 v[28:29], v[36:37], v[28:29]
	v_pk_fma_f32 v[36:37], v[44:45], v[236:237], v[236:237] op_sel:[0,0,1] op_sel_hi:[1,0,1]
	v_rcp_f32_e32 v42, v27
	v_pk_mul_f32 v[44:45], v[32:33], s[18:19] op_sel_hi:[1,0]
	v_or_b32_e32 v26, 48, v26
	v_exp_f32_e32 v44, v44
	v_exp_f32_e32 v45, v45
	v_pk_mul_f32 v[38:39], v[38:39], v[42:43] op_sel:[1,0] op_sel_hi:[0,0]
	v_pk_mul_f32 v[34:35], v[34:35], v[38:39]
	v_pk_fma_f32 v[40:41], v[144:145], v[242:243], v[216:217] op_sel:[0,1,0] op_sel_hi:[1,1,1] clamp
	v_pk_add_f32 v[38:39], v[44:45], 1.0 op_sel_hi:[1,0]
	v_mul_f32_e32 v27, v38, v39
	v_rcp_f32_e32 v42, v27
	v_pk_mul_f32 v[34:35], v[36:37], v[34:35]
	v_pk_fma_f32 v[36:37], v[40:41], v[236:237], v[236:237] op_sel:[0,0,1] op_sel_hi:[1,0,1]
	v_ashrrev_i32_e32 v27, 31, v26
	v_cvt_pk_fp8_f32 v40, v30, v31
	v_cvt_pk_fp8_f32 v41, v34, v35
	v_lshlrev_b64 v[26:27], 10, v[26:27]
	v_pk_mul_f32 v[38:39], v[38:39], v[42:43] op_sel:[1,0] op_sel_hi:[0,0]
	v_lshl_add_u64 v[24:25], v[24:25], 0, v[26:27]
	v_pk_fma_f32 v[26:27], v[122:123], v[242:243], v[222:223] op_sel_hi:[1,0,1] clamp
	v_pk_mul_f32 v[30:31], v[32:33], v[38:39]
	v_pk_fma_f32 v[26:27], v[26:27], v[234:235], v[234:235] op_sel:[0,0,1] op_sel_hi:[1,0,1]
	v_pk_mul_f32 v[30:31], v[36:37], v[30:31]
	v_pk_mul_f32 v[38:39], v[26:27], s[18:19] op_sel_hi:[1,0]
	v_cvt_pk_fp8_f32 v40, v28, v29 op_sel:[0,0,1]
	v_cvt_pk_fp8_f32 v41, v30, v31 op_sel:[0,0,1]
	v_exp_f32_e32 v38, v38
	v_exp_f32_e32 v39, v39
	v_pk_fma_f32 v[34:35], v[130:131], v[242:243], v[226:227] op_sel:[0,1,0] op_sel_hi:[1,1,1] clamp
	global_store_dwordx2 v[24:25], v[40:41], off
	v_pk_fma_f32 v[24:25], v[124:125], v[242:243], v[224:225] op_sel_hi:[1,0,1] clamp
	v_pk_add_f32 v[38:39], v[38:39], 1.0 op_sel_hi:[1,0]
	v_pk_fma_f32 v[24:25], v[24:25], v[234:235], v[234:235] op_sel:[0,0,1] op_sel_hi:[1,0,1]
	v_mul_f32_e32 v42, v38, v39
	v_rcp_f32_e32 v42, v42
	v_pk_mul_f32 v[44:45], v[24:25], s[18:19] op_sel_hi:[1,0]
	v_pk_fma_f32 v[34:35], v[34:35], v[236:237], v[236:237] op_sel:[0,0,1] op_sel_hi:[1,0,1]
	v_exp_f32_e32 v44, v44
	v_exp_f32_e32 v45, v45
	v_pk_mul_f32 v[38:39], v[38:39], v[42:43] op_sel:[1,0] op_sel_hi:[0,0]
	v_pk_mul_f32 v[26:27], v[26:27], v[38:39]
	v_pk_add_f32 v[38:39], v[44:45], 1.0 op_sel_hi:[1,0]
	v_pk_fma_f32 v[30:31], v[118:119], v[242:243], v[218:219] op_sel_hi:[1,0,1] clamp
	v_mul_f32_e32 v42, v38, v39
	v_rcp_f32_e32 v42, v42
	v_pk_fma_f32 v[30:31], v[30:31], v[234:235], v[234:235] op_sel:[0,0,1] op_sel_hi:[1,0,1]
	v_pk_mul_f32 v[26:27], v[34:35], v[26:27]
	v_pk_mul_f32 v[34:35], v[38:39], v[42:43] op_sel:[1,0] op_sel_hi:[0,0]
	v_pk_mul_f32 v[24:25], v[24:25], v[34:35]
	v_pk_mul_f32 v[34:35], v[30:31], s[18:19] op_sel_hi:[1,0]
	v_pk_fma_f32 v[32:33], v[132:133], v[242:243], v[228:229] op_sel:[0,1,0] op_sel_hi:[1,1,1] clamp
	v_exp_f32_e32 v34, v34
	v_exp_f32_e32 v35, v35
	v_pk_fma_f32 v[28:29], v[120:121], v[242:243], v[220:221] op_sel_hi:[1,0,1] clamp
	v_pk_fma_f32 v[32:33], v[32:33], v[236:237], v[236:237] op_sel:[0,0,1] op_sel_hi:[1,0,1]
	v_pk_add_f32 v[34:35], v[34:35], 1.0 op_sel_hi:[1,0]
	v_pk_fma_f32 v[40:41], v[126:127], v[242:243], v[214:215] op_sel:[0,1,0] op_sel_hi:[1,1,1] clamp
	v_mul_f32_e32 v38, v34, v35
	v_pk_fma_f32 v[28:29], v[28:29], v[234:235], v[234:235] op_sel:[0,0,1] op_sel_hi:[1,0,1]
	v_pk_mul_f32 v[24:25], v[32:33], v[24:25]
	v_pk_fma_f32 v[32:33], v[40:41], v[236:237], v[236:237] op_sel:[0,0,1] op_sel_hi:[1,0,1]
	v_rcp_f32_e32 v38, v38
	v_pk_mul_f32 v[40:41], v[28:29], s[18:19] op_sel_hi:[1,0]
	v_pk_fma_f32 v[36:37], v[128:129], v[242:243], v[216:217] op_sel:[0,1,0] op_sel_hi:[1,1,1] clamp
	v_exp_f32_e32 v40, v40
; __device__ __forceinline__ unsigned pk4_fp8(float a, float b, float c, float d) { int w = __builtin_amdgcn_cvt_pk_fp8_f32(a, b, 0, false); w = __builtin_amdgcn_cvt_pk_fp8_f32(c, d, w, true); return (unsigned)w; }
;     static __device__ __forceinline__ f32x2 act2(f32x2 g, f32x2 u) {
;         g.x = __builtin_amdgcn_fmed3f(g.x, -24.0f, 7.0f); g.y = __builtin_amdgcn_fmed3f(g.y, -24.0f, 7.0f);
;         u.x = __builtin_amdgcn_fmed3f(u.x, -7.0f, 7.0f); u.y = __builtin_amdgcn_fmed3f(u.y, -7.0f, 7.0f);
;         f32x2 z = g * (-1.702f * 1.4426950408889634f);
;         f32x2 d; d.x = __builtin_amdgcn_exp2f(z.x); d.y = __builtin_amdgcn_exp2f(z.y);
;         d = d + 1.0f;
;         const float r = __builtin_amdgcn_rcpf(d.x * d.y);
;         f32x2 sg; sg.x = r * d.y; sg.y = r * d.x;
;         return (u + 1.0f) * (g * sg);
;     }
;     __device__ __forceinline__ void operator()(const f32x4 (&acc)[2][2][4][2], const pg8::Unit& u, int wr, int wc, int fr, int fq) const {
;         const int e = u.aux;
;         unsigned char* Ht = ws + WS_H2 + (size_t)u.pm * TSF8;
;         const int hc = u.pn * 128 + wc * 32 + 8 * fq;
;         const f32x4 bg0 = *(const f32x4*)(bgate + e * FF + hc), bg1 = *(const f32x4*)(bgate + e * FF + hc + 4);
;         const f32x4 bu0 = *(const f32x4*)(bup + e * FF + hc), bu1 = *(const f32x4*)(bup + e * FF + hc + 4);
; #pragma unroll
;         for (int ai = 0; ai < 2; ++ai)
; #pragma unroll
;             for (int m = 0; m < 4; ++m) { const int rl = ai * 128 + wr * 64 + m * 16 + fr;
;                 const f32x4 g0 = acc[ai][0][m][0] * (1.0f / 64.0f) + bg0, g1 = acc[ai][0][m][1] * (1.0f / 64.0f) + bg1, u0 = acc[ai][1][m][0] * (1.0f / 64.0f) + bu0, u1 = acc[ai][1][m][1] * (1.0f / 64.0f) + bu1;
;                 const f32x2 h0 = act2((f32x2){g0[0], g0[1]}, (f32x2){u0[0], u0[1]}), h1 = act2((f32x2){g0[2], g0[3]}, (f32x2){u0[2], u0[3]});
;                 const f32x2 h2 = act2((f32x2){g1[0], g1[1]}, (f32x2){u1[0], u1[1]}), h3 = act2((f32x2){g1[2], g1[3]}, (f32x2){u1[2], u1[3]});
;                 *(u32x2*)(Ht + (size_t)rl * FF + hc) = (u32x2){pk4_fp8(h0.x, h0.y, h1.x, h1.y), pk4_fp8(h2.x, h2.y, h3.x, h3.y)}; }
	v_exp_f32_e32 v41, v41
	v_pk_mul_f32 v[34:35], v[34:35], v[38:39] op_sel:[1,0] op_sel_hi:[0,0]
	v_pk_mul_f32 v[30:31], v[30:31], v[34:35]
	v_pk_add_f32 v[34:35], v[40:41], 1.0 op_sel_hi:[1,0]
	v_pk_mul_f32 v[30:31], v[32:33], v[30:31]
	v_mul_f32_e32 v38, v34, v35
	v_rcp_f32_e32 v38, v38
	v_pk_fma_f32 v[32:33], v[36:37], v[236:237], v[236:237] op_sel:[0,0,1] op_sel_hi:[1,0,1]
	v_cvt_pk_fp8_f32 v37, v30, v31
	v_pk_mul_f32 v[34:35], v[34:35], v[38:39] op_sel:[1,0] op_sel_hi:[0,0]
	v_cvt_pk_fp8_f32 v36, v26, v27
	v_pk_mul_f32 v[26:27], v[28:29], v[34:35]
	v_pk_fma_f32 v[34:35], v[114:115], v[242:243], v[226:227] op_sel:[0,1,0] op_sel_hi:[1,1,1] clamp
	v_pk_mul_f32 v[26:27], v[32:33], v[26:27]
	v_cvt_pk_fp8_f32 v36, v24, v25 op_sel:[0,0,1]
	v_cvt_pk_fp8_f32 v37, v26, v27 op_sel:[0,0,1]
	v_pk_fma_f32 v[26:27], v[106:107], v[242:243], v[222:223] op_sel_hi:[1,0,1] clamp
	v_add_co_u32_e32 v24, vcc, s50, v22
	v_pk_fma_f32 v[26:27], v[26:27], v[234:235], v[234:235] op_sel:[0,0,1] op_sel_hi:[1,0,1]
	v_pk_mul_f32 v[38:39], v[26:27], s[18:19] op_sel_hi:[1,0]
	v_addc_co_u32_e32 v25, vcc, 0, v23, vcc
	v_exp_f32_e32 v38, v38
	v_exp_f32_e32 v39, v39
	global_store_dwordx2 v[24:25], v[36:37], off
	v_pk_fma_f32 v[24:25], v[108:109], v[242:243], v[224:225] op_sel_hi:[1,0,1] clamp
	v_pk_fma_f32 v[34:35], v[34:35], v[236:237], v[236:237] op_sel:[0,0,1] op_sel_hi:[1,0,1]
	v_pk_add_f32 v[38:39], v[38:39], 1.0 op_sel_hi:[1,0]
	v_pk_fma_f32 v[24:25], v[24:25], v[234:235], v[234:235] op_sel:[0,0,1] op_sel_hi:[1,0,1]
	v_mul_f32_e32 v42, v38, v39
	v_rcp_f32_e32 v42, v42
	v_pk_mul_f32 v[44:45], v[24:25], s[18:19] op_sel_hi:[1,0]
	v_exp_f32_e32 v44, v44
	v_exp_f32_e32 v45, v45
	v_pk_mul_f32 v[38:39], v[38:39], v[42:43] op_sel:[1,0] op_sel_hi:[0,0]
	v_pk_mul_f32 v[26:27], v[26:27], v[38:39]
	v_pk_fma_f32 v[30:31], v[102:103], v[242:243], v[218:219] op_sel_hi:[1,0,1] clamp
	v_pk_add_f32 v[38:39], v[44:45], 1.0 op_sel_hi:[1,0]
	v_mul_f32_e32 v42, v38, v39
	v_rcp_f32_e32 v42, v42
	v_pk_mul_f32 v[26:27], v[34:35], v[26:27]
	v_pk_fma_f32 v[30:31], v[30:31], v[234:235], v[234:235] op_sel:[0,0,1] op_sel_hi:[1,0,1]
	v_pk_mul_f32 v[34:35], v[38:39], v[42:43] op_sel:[1,0] op_sel_hi:[0,0]
	v_pk_mul_f32 v[24:25], v[24:25], v[34:35]
	v_pk_mul_f32 v[34:35], v[30:31], s[18:19] op_sel_hi:[1,0]
	v_pk_fma_f32 v[32:33], v[116:117], v[242:243], v[228:229] op_sel:[0,1,0] op_sel_hi:[1,1,1] clamp
	v_exp_f32_e32 v34, v34
	v_exp_f32_e32 v35, v35
	v_pk_fma_f32 v[28:29], v[104:105], v[242:243], v[220:221] op_sel_hi:[1,0,1] clamp
	v_pk_fma_f32 v[32:33], v[32:33], v[236:237], v[236:237] op_sel:[0,0,1] op_sel_hi:[1,0,1]
	v_pk_add_f32 v[34:35], v[34:35], 1.0 op_sel_hi:[1,0]
	v_pk_fma_f32 v[40:41], v[110:111], v[242:243], v[214:215] op_sel:[0,1,0] op_sel_hi:[1,1,1] clamp
	v_mul_f32_e32 v38, v34, v35
	v_pk_fma_f32 v[28:29], v[28:29], v[234:235], v[234:235] op_sel:[0,0,1] op_sel_hi:[1,0,1]
	v_pk_mul_f32 v[24:25], v[32:33], v[24:25]
	v_pk_fma_f32 v[32:33], v[40:41], v[236:237], v[236:237] op_sel:[0,0,1] op_sel_hi:[1,0,1]
	v_rcp_f32_e32 v38, v38
	v_pk_mul_f32 v[40:41], v[28:29], s[18:19] op_sel_hi:[1,0]
	v_pk_fma_f32 v[36:37], v[112:113], v[242:243], v[216:217] op_sel:[0,1,0] op_sel_hi:[1,1,1] clamp
	v_exp_f32_e32 v40, v40
	v_exp_f32_e32 v41, v41
	v_pk_mul_f32 v[34:35], v[34:35], v[38:39] op_sel:[1,0] op_sel_hi:[0,0]
	v_pk_mul_f32 v[30:31], v[30:31], v[34:35]
	v_pk_add_f32 v[34:35], v[40:41], 1.0 op_sel_hi:[1,0]
	v_pk_mul_f32 v[30:31], v[32:33], v[30:31]
	v_mul_f32_e32 v38, v34, v35
	v_rcp_f32_e32 v38, v38
	v_pk_fma_f32 v[32:33], v[36:37], v[236:237], v[236:237] op_sel:[0,0,1] op_sel_hi:[1,0,1]
	v_cvt_pk_fp8_f32 v37, v30, v31
	v_pk_mul_f32 v[34:35], v[34:35], v[38:39] op_sel:[1,0] op_sel_hi:[0,0]
	v_cvt_pk_fp8_f32 v36, v26, v27
	v_pk_mul_f32 v[26:27], v[28:29], v[34:35]
	v_pk_fma_f32 v[34:35], v[98:99], v[242:243], v[226:227] op_sel:[0,1,0] op_sel_hi:[1,1,1] clamp
	v_pk_mul_f32 v[26:27], v[32:33], v[26:27]
	v_cvt_pk_fp8_f32 v36, v24, v25 op_sel:[0,0,1]
	v_cvt_pk_fp8_f32 v37, v26, v27 op_sel:[0,0,1]
	v_pk_fma_f32 v[26:27], v[90:91], v[242:243], v[222:223] op_sel_hi:[1,0,1] clamp
	v_add_co_u32_e32 v24, vcc, s51, v22
	v_pk_fma_f32 v[26:27], v[26:27], v[234:235], v[234:235] op_sel:[0,0,1] op_sel_hi:[1,0,1]
	v_pk_mul_f32 v[38:39], v[26:27], s[18:19] op_sel_hi:[1,0]
	v_addc_co_u32_e32 v25, vcc, 0, v23, vcc
	v_exp_f32_e32 v38, v38
	v_exp_f32_e32 v39, v39
	global_store_dwordx2 v[24:25], v[36:37], off
	v_pk_fma_f32 v[24:25], v[92:93], v[242:243], v[224:225] op_sel_hi:[1,0,1] clamp
	v_pk_fma_f32 v[34:35], v[34:35], v[236:237], v[236:237] op_sel:[0,0,1] op_sel_hi:[1,0,1]
	v_pk_add_f32 v[38:39], v[38:39], 1.0 op_sel_hi:[1,0]
	v_pk_fma_f32 v[24:25], v[24:25], v[234:235], v[234:235] op_sel:[0,0,1] op_sel_hi:[1,0,1]
	v_mul_f32_e32 v42, v38, v39
	v_rcp_f32_e32 v42, v42
	v_pk_mul_f32 v[44:45], v[24:25], s[18:19] op_sel_hi:[1,0]
	v_exp_f32_e32 v44, v44
	v_exp_f32_e32 v45, v45
	v_pk_mul_f32 v[38:39], v[38:39], v[42:43] op_sel:[1,0] op_sel_hi:[0,0]
	v_pk_mul_f32 v[26:27], v[26:27], v[38:39]
	v_pk_fma_f32 v[30:31], v[86:87], v[242:243], v[218:219] op_sel_hi:[1,0,1] clamp
	v_pk_add_f32 v[38:39], v[44:45], 1.0 op_sel_hi:[1,0]
	v_mul_f32_e32 v42, v38, v39
	v_rcp_f32_e32 v42, v42
	v_pk_mul_f32 v[26:27], v[34:35], v[26:27]
	v_pk_fma_f32 v[30:31], v[30:31], v[234:235], v[234:235] op_sel:[0,0,1] op_sel_hi:[1,0,1]
	v_pk_mul_f32 v[34:35], v[38:39], v[42:43] op_sel:[1,0] op_sel_hi:[0,0]
; template <class Epi, class Sched, bool F8 = false, bool PF = false, bool I8 = false, int PID = -1>
; __device__ __forceinline__ void gemm_phase(LAS unsigned char* lds, LAS unsigned char* xlds, const int RP, const int RPB, const int nt, const Sched& S, const Epi& E, const int stagger_ticks) {
;     ...
;         if (!has_next) break;
;         PROF_BEGIN(3);
;         cur = nxt; cA = nA; cB = nB; ++ui;
;         has_next = has_nn; nxt = nn;
;     static __device__ __forceinline__ f32x2 act2(f32x2 g, f32x2 u) {
;         g.x = __builtin_amdgcn_fmed3f(g.x, -24.0f, 7.0f); g.y = __builtin_amdgcn_fmed3f(g.y, -24.0f, 7.0f);
;         u.x = __builtin_amdgcn_fmed3f(u.x, -7.0f, 7.0f); u.y = __builtin_amdgcn_fmed3f(u.y, -7.0f, 7.0f);
;         f32x2 z = g * (-1.702f * 1.4426950408889634f);
;         f32x2 d; d.x = __builtin_amdgcn_exp2f(z.x); d.y = __builtin_amdgcn_exp2f(z.y);
;         d = d + 1.0f;
;         const float r = __builtin_amdgcn_rcpf(d.x * d.y);
;         f32x2 sg; sg.x = r * d.y; sg.y = r * d.x;
;         return (u + 1.0f) * (g * sg);
;     }
;     __device__ __forceinline__ void operator()(const f32x4 (&acc)[2][2][4][2], const pg8::Unit& u, int wr, int wc, int fr, int fq) const {
;         const int e = u.aux;
;         unsigned char* Ht = ws + WS_H2 + (size_t)u.pm * TSF8;
;         const int hc = u.pn * 128 + wc * 32 + 8 * fq;
;         const f32x4 bg0 = *(const f32x4*)(bgate + e * FF + hc), bg1 = *(const f32x4*)(bgate + e * FF + hc + 4);
;         const f32x4 bu0 = *(const f32x4*)(bup + e * FF + hc), bu1 = *(const f32x4*)(bup + e * FF + hc + 4);
; #pragma unroll
;         for (int ai = 0; ai < 2; ++ai)
; #pragma unroll
;             for (int m = 0; m < 4; ++m) { const int rl = ai * 128 + wr * 64 + m * 16 + fr;
;                 const f32x4 g0 = acc[ai][0][m][0] * (1.0f / 64.0f) + bg0, g1 = acc[ai][0][m][1] * (1.0f / 64.0f) + bg1, u0 = acc[ai][1][m][0] * (1.0f / 64.0f) + bu0, u1 = acc[ai][1][m][1] * (1.0f / 64.0f) + bu1;
;                 const f32x2 h0 = act2((f32x2){g0[0], g0[1]}, (f32x2){u0[0], u0[1]}), h1 = act2((f32x2){g0[2], g0[3]}, (f32x2){u0[2], u0[3]});
;                 const f32x2 h2 = act2((f32x2){g1[0], g1[1]}, (f32x2){u1[0], u1[1]}), h3 = act2((f32x2){g1[2], g1[3]}, (f32x2){u1[2], u1[3]});
;                 *(u32x2*)(Ht + (size_t)rl * FF + hc) = (u32x2){pk4_fp8(h0.x, h0.y, h1.x, h1.y), pk4_fp8(h2.x, h2.y, h3.x, h3.y)}; }
	v_pk_mul_f32 v[24:25], v[24:25], v[34:35]
	v_pk_mul_f32 v[34:35], v[30:31], s[18:19] op_sel_hi:[1,0]
	v_pk_fma_f32 v[32:33], v[100:101], v[242:243], v[228:229] op_sel:[0,1,0] op_sel_hi:[1,1,1] clamp
	v_exp_f32_e32 v34, v34
	v_exp_f32_e32 v35, v35
	v_pk_fma_f32 v[28:29], v[88:89], v[242:243], v[220:221] op_sel_hi:[1,0,1] clamp
	v_pk_fma_f32 v[32:33], v[32:33], v[236:237], v[236:237] op_sel:[0,0,1] op_sel_hi:[1,0,1]
	v_pk_add_f32 v[34:35], v[34:35], 1.0 op_sel_hi:[1,0]
	v_pk_fma_f32 v[40:41], v[94:95], v[242:243], v[214:215] op_sel:[0,1,0] op_sel_hi:[1,1,1] clamp
	v_mul_f32_e32 v38, v34, v35
	v_pk_fma_f32 v[28:29], v[28:29], v[234:235], v[234:235] op_sel:[0,0,1] op_sel_hi:[1,0,1]
	v_pk_mul_f32 v[24:25], v[32:33], v[24:25]
	v_pk_fma_f32 v[32:33], v[40:41], v[236:237], v[236:237] op_sel:[0,0,1] op_sel_hi:[1,0,1]
	v_rcp_f32_e32 v38, v38
	v_pk_mul_f32 v[40:41], v[28:29], s[18:19] op_sel_hi:[1,0]
	v_pk_fma_f32 v[36:37], v[96:97], v[242:243], v[216:217] op_sel:[0,1,0] op_sel_hi:[1,1,1] clamp
	v_exp_f32_e32 v40, v40
	v_exp_f32_e32 v41, v41
	v_pk_mul_f32 v[34:35], v[34:35], v[38:39] op_sel:[1,0] op_sel_hi:[0,0]
	v_pk_mul_f32 v[30:31], v[30:31], v[34:35]
	v_pk_add_f32 v[34:35], v[40:41], 1.0 op_sel_hi:[1,0]
	v_pk_mul_f32 v[30:31], v[32:33], v[30:31]
	v_mul_f32_e32 v38, v34, v35
	v_rcp_f32_e32 v38, v38
	v_pk_fma_f32 v[32:33], v[36:37], v[236:237], v[236:237] op_sel:[0,0,1] op_sel_hi:[1,0,1]
	v_cvt_pk_fp8_f32 v36, v26, v27
	v_cvt_pk_fp8_f32 v37, v30, v31
	v_pk_mul_f32 v[34:35], v[34:35], v[38:39] op_sel:[1,0] op_sel_hi:[0,0]
	v_pk_mul_f32 v[26:27], v[28:29], v[34:35]
	v_cvt_pk_fp8_f32 v36, v24, v25 op_sel:[0,0,1]
	v_pk_mul_f32 v[26:27], v[32:33], v[26:27]
	v_add_co_u32_e32 v24, vcc, s60, v22
	v_cvt_pk_fp8_f32 v37, v26, v27 op_sel:[0,0,1]
	v_pk_fma_f32 v[14:15], v[74:75], v[242:243], v[222:223] op_sel_hi:[1,0,1] clamp
	v_addc_co_u32_e32 v25, vcc, 0, v23, vcc
	v_pk_fma_f32 v[14:15], v[14:15], v[234:235], v[234:235] op_sel:[0,0,1] op_sel_hi:[1,0,1]
	global_store_dwordx2 v[24:25], v[36:37], off
	v_pk_mul_f32 v[24:25], v[14:15], s[18:19] op_sel_hi:[1,0]
	v_pk_fma_f32 v[16:17], v[76:77], v[242:243], v[224:225] op_sel_hi:[1,0,1] clamp
	v_exp_f32_e32 v24, v24
	v_exp_f32_e32 v25, v25
	v_pk_fma_f32 v[16:17], v[16:17], v[234:235], v[234:235] op_sel:[0,0,1] op_sel_hi:[1,0,1]
	v_pk_mul_f32 v[28:29], v[16:17], s[18:19] op_sel_hi:[1,0]
	v_pk_add_f32 v[24:25], v[24:25], 1.0 op_sel_hi:[1,0]
	v_exp_f32_e32 v28, v28
	v_mul_f32_e32 v26, v24, v25
	v_rcp_f32_e32 v26, v26
	v_exp_f32_e32 v29, v29
	v_pk_fma_f32 v[18:19], v[82:83], v[242:243], v[226:227] op_sel:[0,1,0] op_sel_hi:[1,1,1] clamp
	v_pk_fma_f32 v[10:11], v[70:71], v[242:243], v[218:219] op_sel_hi:[1,0,1] clamp
	v_pk_mul_f32 v[24:25], v[24:25], v[26:27] op_sel:[1,0] op_sel_hi:[0,0]
	v_pk_mul_f32 v[14:15], v[14:15], v[24:25]
	v_pk_add_f32 v[24:25], v[28:29], 1.0 op_sel_hi:[1,0]
	v_pk_fma_f32 v[18:19], v[18:19], v[236:237], v[236:237] op_sel:[0,0,1] op_sel_hi:[1,0,1]
	v_mul_f32_e32 v26, v24, v25
	v_rcp_f32_e32 v26, v26
	v_pk_fma_f32 v[20:21], v[84:85], v[242:243], v[228:229] op_sel:[0,1,0] op_sel_hi:[1,1,1] clamp
	v_pk_fma_f32 v[10:11], v[10:11], v[234:235], v[234:235] op_sel:[0,0,1] op_sel_hi:[1,0,1]
	v_pk_mul_f32 v[14:15], v[18:19], v[14:15]
	v_pk_fma_f32 v[18:19], v[20:21], v[236:237], v[236:237] op_sel:[0,0,1] op_sel_hi:[1,0,1]
	v_pk_mul_f32 v[20:21], v[24:25], v[26:27] op_sel:[1,0] op_sel_hi:[0,0]
	v_pk_mul_f32 v[16:17], v[16:17], v[20:21]
	v_pk_mul_f32 v[20:21], v[10:11], s[18:19] op_sel_hi:[1,0]
	v_exp_f32_e32 v20, v20
	v_exp_f32_e32 v21, v21
	v_pk_fma_f32 v[12:13], v[72:73], v[242:243], v[220:221] op_sel_hi:[1,0,1] clamp
	v_pk_mul_f32 v[16:17], v[18:19], v[16:17]
	v_pk_fma_f32 v[12:13], v[12:13], v[234:235], v[234:235] op_sel:[0,0,1] op_sel_hi:[1,0,1]
	v_pk_add_f32 v[18:19], v[20:21], 1.0 op_sel_hi:[1,0]
	v_mul_f32_e32 v20, v18, v19
	v_rcp_f32_e32 v20, v20
	v_pk_mul_f32 v[24:25], v[12:13], s[18:19] op_sel_hi:[1,0]
	v_pk_fma_f32 v[6:7], v[78:79], v[242:243], v[214:215] op_sel:[0,1,0] op_sel_hi:[1,1,1] clamp
	v_exp_f32_e32 v24, v24
	v_exp_f32_e32 v25, v25
	v_pk_mul_f32 v[18:19], v[18:19], v[20:21] op_sel:[1,0] op_sel_hi:[0,0]
	v_pk_mul_f32 v[10:11], v[10:11], v[18:19]
	v_pk_fma_f32 v[6:7], v[6:7], v[236:237], v[236:237] op_sel:[0,0,1] op_sel_hi:[1,0,1]
	v_pk_add_f32 v[18:19], v[24:25], 1.0 op_sel_hi:[1,0]
	v_mul_f32_e32 v20, v18, v19
	v_rcp_f32_e32 v20, v20
	v_pk_fma_f32 v[8:9], v[80:81], v[242:243], v[216:217] op_sel:[0,1,0] op_sel_hi:[1,1,1] clamp
	v_pk_mul_f32 v[6:7], v[6:7], v[10:11]
	v_pk_mul_f32 v[10:11], v[18:19], v[20:21] op_sel:[1,0] op_sel_hi:[0,0]
	v_cvt_pk_fp8_f32 v18, v14, v15
	v_cvt_pk_fp8_f32 v19, v6, v7
	v_pk_fma_f32 v[8:9], v[8:9], v[236:237], v[236:237] op_sel:[0,0,1] op_sel_hi:[1,0,1]
	v_pk_mul_f32 v[6:7], v[12:13], v[10:11]
	v_cvt_pk_fp8_f32 v18, v16, v17 op_sel:[0,0,1]
	v_pk_mul_f32 v[6:7], v[8:9], v[6:7]
	s_nop 0
	v_cvt_pk_fp8_f32 v19, v6, v7 op_sel:[0,0,1]
	v_add_co_u32_e32 v6, vcc, 0x2c000, v22
	s_nop 1
	v_addc_co_u32_e32 v7, vcc, 0, v23, vcc
	s_and_b64 vcc, exec, s[2:3]
	s_mov_b64 s[2:3], -1
	global_store_dwordx2 v[6:7], v[18:19], off
	s_cbranch_vccnz .LBB0_956
	s_andn2_b64 vcc, exec, s[10:11]
	s_mov_b64 s[22:23], s[8:9]
	s_mov_b64 s[24:25], s[20:21]
	s_cbranch_vccnz .LBB0_972
	s_lshl_b32 s2, s41, 3
	s_add_i32 s2, s2, s39
	s_ashr_i32 s3, s2, 31
	s_lshl_b64 s[2:3], s[2:3], 18
	s_add_u32 s22, s37, s2
	s_addc_u32 s23, s38, s3
	s_mov_b64 s[24:25], s[6:7]

; #define LAS __attribute__((address_space(3)))
; __device__ __forceinline__ unsigned pk4_fp8(float a, float b, float c, float d) { int w = __builtin_amdgcn_cvt_pk_fp8_f32(a, b, 0, false); w = __builtin_amdgcn_cvt_pk_fp8_f32(c, d, w, true); return (unsigned)w; }
;     __device__ __forceinline__ void operator()(const f32x4 (&acc)[2][2][4][2], const pg8::Unit& u, int wr, int wc, int fr, int fq) const {
;         const int col0 = u.pn * 256 + wc * 64 + 16 * fq;
;         unsigned char* Yt = ws + WS_Y + (size_t)u.pm * TSF8;
;         f32x4 bd[2][2];
; #pragma unroll
;         for (int bj = 0; bj < 2; ++bj) { const LAS float* bt = (const LAS float*)(btab + u.par * 1024) + wc * 64 + 16 * fq + bj * 8; bd[bj][0] = *(const LAS f32x4*)bt; bd[bj][1] = *(const LAS f32x4*)(bt + 4); }
; #pragma unroll
;         for (int ai = 0; ai < 2; ++ai)
; #pragma unroll
;             for (int m = 0; m < 4; ++m) { const int rl = ai * 128 + wr * 64 + m * 16 + fr;
;                 { const f32x4 v0 = acc[ai][0][m][0] * (1.0f / 64.0f) + bd[0][0], v1 = acc[ai][0][m][1] * (1.0f / 64.0f) + bd[0][1], v2 = acc[ai][1][m][0] * (1.0f / 64.0f) + bd[1][0], v3 = acc[ai][1][m][1] * (1.0f / 64.0f) + bd[1][1];
;                     *(u32x4*)(Yt + (size_t)rl * D + col0) = (u32x4){pk4_fp8(v0[0], v0[1], v0[2], v0[3]), pk4_fp8(v1[0], v1[1], v1[2], v1[3]), pk4_fp8(v2[0], v2[1], v2[2], v2[3]), pk4_fp8(v3[0], v3[1], v3[2], v3[3])}; } }
;     }
.Lmy_nobar1:
	v_mov_b32_e32 v19, v0
	s_lshl_b32 s15, s15, 8
	s_or_b32 s15, s15, s61
	v_and_b32_e32 v2, 48, v19
	v_or_b32_e32 v18, s15, v2
	s_add_i32 s15, s62, s70
	v_lshl_add_u32 v2, v2, 2, s15
	ds_read_b128 v[14:17], v2
	ds_read_b128 v[10:13], v2 offset:16
	ds_read_b128 v[6:9], v2 offset:32
	ds_read_b128 v[2:5], v2 offset:48
	s_waitcnt lgkmcnt(3)
	v_pk_fma_f32 v[22:23], v[150:151], s[22:23], v[14:15] op_sel_hi:[1,0,1]
	s_ashr_i32 s25, s24, 31
	s_waitcnt lgkmcnt(2)
	v_pk_fma_f32 v[30:31], v[146:147], s[22:23], v[10:11] op_sel_hi:[1,0,1]
	s_waitcnt lgkmcnt(1)
	v_pk_fma_f32 v[146:147], v[158:159], s[22:23], v[6:7] op_sel_hi:[1,0,1]
	s_waitcnt lgkmcnt(0)
	v_pk_fma_f32 v[150:151], v[154:155], s[22:23], v[2:3] op_sel_hi:[1,0,1]
	v_cvt_pk_fp8_f32 v20, v22, v23
	s_lshl_b64 s[24:25], s[24:25], 18
	v_cvt_pk_fp8_f32 v21, v30, v31
	v_cvt_pk_fp8_f32 v22, v146, v147
	v_cvt_pk_fp8_f32 v23, v150, v151
	s_add_u32 s24, s50, s24
	s_addc_u32 s25, s51, s25
	v_and_or_b32 v24, v19, 15, s49
	v_ashrrev_i32_e32 v19, 31, v18
	v_lshl_add_u64 v[26:27], s[24:25], 0, v[18:19]
	v_pk_fma_f32 v[18:19], v[152:153], s[22:23], v[16:17] op_sel_hi:[1,0,1]
	v_pk_fma_f32 v[28:29], v[148:149], s[22:23], v[12:13] op_sel_hi:[1,0,1]
	v_pk_fma_f32 v[32:33], v[160:161], s[22:23], v[8:9] op_sel_hi:[1,0,1]
	v_pk_fma_f32 v[148:149], v[156:157], s[22:23], v[4:5] op_sel_hi:[1,0,1]
	v_cvt_pk_fp8_f32 v20, v18, v19 op_sel:[0,0,1]
	v_cvt_pk_fp8_f32 v21, v28, v29 op_sel:[0,0,1]
	v_cvt_pk_fp8_f32 v22, v32, v33 op_sel:[0,0,1]
	v_cvt_pk_fp8_f32 v23, v148, v149 op_sel:[0,0,1]
	v_ashrrev_i32_e32 v25, 31, v24
	v_lshlrev_b64 v[18:19], 10, v[24:25]
	v_lshl_add_u64 v[18:19], v[26:27], 0, v[18:19]
	global_store_dwordx4 v[18:19], v[20:23], off
	v_pk_fma_f32 v[130:131], v[130:131], s[22:23], v[10:11] op_sel_hi:[1,0,1]
	v_pk_fma_f32 v[138:139], v[138:139], s[22:23], v[2:3] op_sel_hi:[1,0,1]
	v_pk_fma_f32 v[22:23], v[134:135], s[22:23], v[14:15] op_sel_hi:[1,0,1]
	v_pk_fma_f32 v[134:135], v[142:143], s[22:23], v[6:7] op_sel_hi:[1,0,1]
	v_cvt_pk_fp8_f32 v20, v22, v23
	v_cvt_pk_fp8_f32 v21, v130, v131
	v_cvt_pk_fp8_f32 v22, v134, v135
	v_cvt_pk_fp8_f32 v23, v138, v139
	v_pk_fma_f32 v[30:31], v[136:137], s[22:23], v[16:17] op_sel_hi:[1,0,1]
	v_pk_fma_f32 v[32:33], v[132:133], s[22:23], v[12:13] op_sel_hi:[1,0,1]
	v_pk_fma_f32 v[132:133], v[144:145], s[22:23], v[8:9] op_sel_hi:[1,0,1]
	v_pk_fma_f32 v[136:137], v[140:141], s[22:23], v[4:5] op_sel_hi:[1,0,1]
	v_or_b32_e32 v28, 16, v24
	v_cvt_pk_fp8_f32 v20, v30, v31 op_sel:[0,0,1]
	v_cvt_pk_fp8_f32 v21, v32, v33 op_sel:[0,0,1]
	v_cvt_pk_fp8_f32 v22, v132, v133 op_sel:[0,0,1]
	v_cvt_pk_fp8_f32 v23, v136, v137 op_sel:[0,0,1]
	v_ashrrev_i32_e32 v29, 31, v28
	v_lshlrev_b64 v[28:29], 10, v[28:29]
	v_lshl_add_u64 v[28:29], v[26:27], 0, v[28:29]
	global_store_dwordx4 v[28:29], v[20:23], off
	v_pk_fma_f32 v[114:115], v[114:115], s[22:23], v[10:11] op_sel_hi:[1,0,1]
	v_pk_fma_f32 v[122:123], v[122:123], s[22:23], v[2:3] op_sel_hi:[1,0,1]
	v_pk_fma_f32 v[22:23], v[118:119], s[22:23], v[14:15] op_sel_hi:[1,0,1]
	v_pk_fma_f32 v[118:119], v[126:127], s[22:23], v[6:7] op_sel_hi:[1,0,1]
	v_cvt_pk_fp8_f32 v20, v22, v23
	v_cvt_pk_fp8_f32 v21, v114, v115
	v_cvt_pk_fp8_f32 v22, v118, v119
	v_cvt_pk_fp8_f32 v23, v122, v123
	v_pk_fma_f32 v[30:31], v[120:121], s[22:23], v[16:17] op_sel_hi:[1,0,1]
	v_pk_fma_f32 v[32:33], v[116:117], s[22:23], v[12:13] op_sel_hi:[1,0,1]
	v_pk_fma_f32 v[116:117], v[128:129], s[22:23], v[8:9] op_sel_hi:[1,0,1]
	v_pk_fma_f32 v[120:121], v[124:125], s[22:23], v[4:5] op_sel_hi:[1,0,1]
	v_or_b32_e32 v28, 32, v24
	v_cvt_pk_fp8_f32 v20, v30, v31 op_sel:[0,0,1]
	v_cvt_pk_fp8_f32 v21, v32, v33 op_sel:[0,0,1]
	v_cvt_pk_fp8_f32 v22, v116, v117 op_sel:[0,0,1]
	v_cvt_pk_fp8_f32 v23, v120, v121 op_sel:[0,0,1]
	v_ashrrev_i32_e32 v29, 31, v28
	v_lshlrev_b64 v[28:29], 10, v[28:29]
	v_lshl_add_u64 v[28:29], v[26:27], 0, v[28:29]
	global_store_dwordx4 v[28:29], v[20:23], off
	v_pk_fma_f32 v[28:29], v[104:105], s[22:23], v[16:17] op_sel_hi:[1,0,1]
	v_pk_fma_f32 v[30:31], v[100:101], s[22:23], v[12:13] op_sel_hi:[1,0,1]
	v_pk_fma_f32 v[22:23], v[102:103], s[22:23], v[14:15] op_sel_hi:[1,0,1]
	v_pk_fma_f32 v[32:33], v[98:99], s[22:23], v[10:11] op_sel_hi:[1,0,1]
	v_pk_fma_f32 v[100:101], v[110:111], s[22:23], v[6:7] op_sel_hi:[1,0,1]
	v_pk_fma_f32 v[104:105], v[106:107], s[22:23], v[2:3] op_sel_hi:[1,0,1]
	v_cvt_pk_fp8_f32 v20, v22, v23
	v_cvt_pk_fp8_f32 v21, v32, v33
	v_cvt_pk_fp8_f32 v22, v100, v101
	v_cvt_pk_fp8_f32 v23, v104, v105
	v_pk_fma_f32 v[98:99], v[112:113], s[22:23], v[8:9] op_sel_hi:[1,0,1]
	v_pk_fma_f32 v[102:103], v[108:109], s[22:23], v[4:5] op_sel_hi:[1,0,1]
	v_or_b32_e32 v24, 48, v24
	v_cvt_pk_fp8_f32 v20, v28, v29 op_sel:[0,0,1]
	v_cvt_pk_fp8_f32 v21, v30, v31 op_sel:[0,0,1]
; #define LAS __attribute__((address_space(3)))
; __device__ __forceinline__ unsigned pk4_fp8(float a, float b, float c, float d) { int w = __builtin_amdgcn_cvt_pk_fp8_f32(a, b, 0, false); w = __builtin_amdgcn_cvt_pk_fp8_f32(c, d, w, true); return (unsigned)w; }
; #define PG8_UNI64(p) ((const char*)((((unsigned long long)(unsigned)__builtin_amdgcn_readfirstlane((int)((unsigned long long)(p) >> 32))) << 32) | (unsigned long long)(unsigned)__builtin_amdgcn_readfirstlane((int)(unsigned)(unsigned long long)(p))))
; template <class Epi, class Sched, bool F8 = false, bool PF = false, bool I8 = false, int PID = -1>
; __device__ __forceinline__ void gemm_phase(LAS unsigned char* lds, LAS unsigned char* xlds, const int RP, const int RPB, const int nt, const Sched& S, const Epi& E, const int stagger_ticks) {
;     ...
;         if (!has_next) break;
;         PROF_BEGIN(3);
;         cur = nxt; cA = nA; cB = nB; ++ui;
;         has_next = has_nn; nxt = nn;
;         if (has_next) { nA = PG8_UNI64(S.Abase(nxt)); nB = PG8_UNI64(S.Bbase(nxt)); }
;         if (Sched::GATHER) { *nslot = (u32x4){gv[0], gv[1], gv[2], gv[3]}; asm volatile("" ::: "memory"); }
;         PG8_ZERO_ACC();
;     __device__ __forceinline__ void operator()(const f32x4 (&acc)[2][2][4][2], const pg8::Unit& u, int wr, int wc, int fr, int fq) const {
;         const int col0 = u.pn * 256 + wc * 64 + 16 * fq;
;         unsigned char* Yt = ws + WS_Y + (size_t)u.pm * TSF8;
;         f32x4 bd[2][2];
; #pragma unroll
;         for (int bj = 0; bj < 2; ++bj) { const LAS float* bt = (const LAS float*)(btab + u.par * 1024) + wc * 64 + 16 * fq + bj * 8; bd[bj][0] = *(const LAS f32x4*)bt; bd[bj][1] = *(const LAS f32x4*)(bt + 4); }
; #pragma unroll
;         for (int ai = 0; ai < 2; ++ai)
; #pragma unroll
;             for (int m = 0; m < 4; ++m) { const int rl = ai * 128 + wr * 64 + m * 16 + fr;
;                 { const f32x4 v0 = acc[ai][0][m][0] * (1.0f / 64.0f) + bd[0][0], v1 = acc[ai][0][m][1] * (1.0f / 64.0f) + bd[0][1], v2 = acc[ai][1][m][0] * (1.0f / 64.0f) + bd[1][0], v3 = acc[ai][1][m][1] * (1.0f / 64.0f) + bd[1][1];
;                     *(u32x4*)(Yt + (size_t)rl * D + col0) = (u32x4){pk4_fp8(v0[0], v0[1], v0[2], v0[3]), pk4_fp8(v1[0], v1[1], v1[2], v1[3]), pk4_fp8(v2[0], v2[1], v2[2], v2[3]), pk4_fp8(v3[0], v3[1], v3[2], v3[3])}; } }
;     }
	v_cvt_pk_fp8_f32 v22, v98, v99 op_sel:[0,0,1]
	v_cvt_pk_fp8_f32 v23, v102, v103 op_sel:[0,0,1]
	v_ashrrev_i32_e32 v25, 31, v24
	v_lshlrev_b64 v[24:25], 10, v[24:25]
	v_lshl_add_u64 v[24:25], v[26:27], 0, v[24:25]
	global_store_dwordx4 v[24:25], v[20:23], off
	v_pk_fma_f32 v[26:27], v[84:85], s[22:23], v[12:13] op_sel_hi:[1,0,1]
	v_pk_fma_f32 v[28:29], v[82:83], s[22:23], v[10:11] op_sel_hi:[1,0,1]
	v_pk_fma_f32 v[22:23], v[86:87], s[22:23], v[14:15] op_sel_hi:[1,0,1]
	v_pk_fma_f32 v[32:33], v[94:95], s[22:23], v[6:7] op_sel_hi:[1,0,1]
	v_pk_fma_f32 v[84:85], v[90:91], s[22:23], v[2:3] op_sel_hi:[1,0,1]
	v_cvt_pk_fp8_f32 v20, v22, v23
	v_cvt_pk_fp8_f32 v21, v28, v29
	v_cvt_pk_fp8_f32 v22, v32, v33
	v_cvt_pk_fp8_f32 v23, v84, v85
	v_pk_fma_f32 v[24:25], v[88:89], s[22:23], v[16:17] op_sel_hi:[1,0,1]
	v_pk_fma_f32 v[30:31], v[96:97], s[22:23], v[8:9] op_sel_hi:[1,0,1]
	v_pk_fma_f32 v[82:83], v[92:93], s[22:23], v[4:5] op_sel_hi:[1,0,1]
	v_cvt_pk_fp8_f32 v20, v24, v25 op_sel:[0,0,1]
	v_cvt_pk_fp8_f32 v21, v26, v27 op_sel:[0,0,1]
	v_cvt_pk_fp8_f32 v22, v30, v31 op_sel:[0,0,1]
	v_cvt_pk_fp8_f32 v23, v82, v83 op_sel:[0,0,1]
	v_add_co_u32_e32 v24, vcc, s67, v18
	v_pk_fma_f32 v[26:27], v[68:69], s[22:23], v[12:13] op_sel_hi:[1,0,1]
	s_nop 0
	v_addc_co_u32_e32 v25, vcc, 0, v19, vcc
	global_store_dwordx4 v[24:25], v[20:23], off
	v_pk_fma_f32 v[28:29], v[66:67], s[22:23], v[10:11] op_sel_hi:[1,0,1]
	v_pk_fma_f32 v[32:33], v[78:79], s[22:23], v[6:7] op_sel_hi:[1,0,1]
	v_pk_fma_f32 v[22:23], v[70:71], s[22:23], v[14:15] op_sel_hi:[1,0,1]
	v_pk_fma_f32 v[68:69], v[74:75], s[22:23], v[2:3] op_sel_hi:[1,0,1]
	v_cvt_pk_fp8_f32 v20, v22, v23
	v_cvt_pk_fp8_f32 v21, v28, v29
	v_cvt_pk_fp8_f32 v22, v32, v33
	v_cvt_pk_fp8_f32 v23, v68, v69
	v_pk_fma_f32 v[24:25], v[72:73], s[22:23], v[16:17] op_sel_hi:[1,0,1]
	v_pk_fma_f32 v[30:31], v[80:81], s[22:23], v[8:9] op_sel_hi:[1,0,1]
	v_pk_fma_f32 v[66:67], v[76:77], s[22:23], v[4:5] op_sel_hi:[1,0,1]
	v_cvt_pk_fp8_f32 v20, v24, v25 op_sel:[0,0,1]
	v_cvt_pk_fp8_f32 v21, v26, v27 op_sel:[0,0,1]
	v_cvt_pk_fp8_f32 v22, v30, v31 op_sel:[0,0,1]
	v_cvt_pk_fp8_f32 v23, v66, v67 op_sel:[0,0,1]
	v_add_co_u32_e32 v24, vcc, s68, v18
	v_pk_fma_f32 v[26:27], v[52:53], s[22:23], v[12:13] op_sel_hi:[1,0,1]
	s_nop 0
	v_addc_co_u32_e32 v25, vcc, 0, v19, vcc
	global_store_dwordx4 v[24:25], v[20:23], off
	v_pk_fma_f32 v[28:29], v[50:51], s[22:23], v[10:11] op_sel_hi:[1,0,1]
	v_pk_fma_f32 v[32:33], v[62:63], s[22:23], v[6:7] op_sel_hi:[1,0,1]
	v_pk_fma_f32 v[22:23], v[54:55], s[22:23], v[14:15] op_sel_hi:[1,0,1]
	v_pk_fma_f32 v[52:53], v[58:59], s[22:23], v[2:3] op_sel_hi:[1,0,1]
	v_cvt_pk_fp8_f32 v20, v22, v23
	v_cvt_pk_fp8_f32 v21, v28, v29
	v_cvt_pk_fp8_f32 v22, v32, v33
	v_cvt_pk_fp8_f32 v23, v52, v53
	v_pk_fma_f32 v[24:25], v[56:57], s[22:23], v[16:17] op_sel_hi:[1,0,1]
	v_pk_fma_f32 v[30:31], v[64:65], s[22:23], v[8:9] op_sel_hi:[1,0,1]
	v_pk_fma_f32 v[50:51], v[60:61], s[22:23], v[4:5] op_sel_hi:[1,0,1]
	v_cvt_pk_fp8_f32 v20, v24, v25 op_sel:[0,0,1]
	v_cvt_pk_fp8_f32 v21, v26, v27 op_sel:[0,0,1]
	v_cvt_pk_fp8_f32 v22, v30, v31 op_sel:[0,0,1]
	v_cvt_pk_fp8_f32 v23, v50, v51 op_sel:[0,0,1]
	v_add_co_u32_e32 v24, vcc, s69, v18
	v_pk_fma_f32 v[14:15], v[38:39], s[22:23], v[14:15] op_sel_hi:[1,0,1]
	s_nop 0
	v_addc_co_u32_e32 v25, vcc, 0, v19, vcc
	global_store_dwordx4 v[24:25], v[20:23], off
	v_pk_fma_f32 v[10:11], v[34:35], s[22:23], v[10:11] op_sel_hi:[1,0,1]
	v_pk_fma_f32 v[6:7], v[46:47], s[22:23], v[6:7] op_sel_hi:[1,0,1]
	v_pk_fma_f32 v[20:21], v[44:45], s[22:23], v[4:5] op_sel_hi:[1,0,1]
	v_pk_fma_f32 v[22:23], v[42:43], s[22:23], v[2:3] op_sel_hi:[1,0,1]
	v_cvt_pk_fp8_f32 v2, v14, v15
	v_cvt_pk_fp8_f32 v3, v10, v11
	v_cvt_pk_fp8_f32 v4, v6, v7
	v_cvt_pk_fp8_f32 v5, v22, v23
	v_pk_fma_f32 v[16:17], v[40:41], s[22:23], v[16:17] op_sel_hi:[1,0,1]
	v_pk_fma_f32 v[12:13], v[36:37], s[22:23], v[12:13] op_sel_hi:[1,0,1]
	v_pk_fma_f32 v[8:9], v[48:49], s[22:23], v[8:9] op_sel_hi:[1,0,1]
	v_cvt_pk_fp8_f32 v2, v16, v17 op_sel:[0,0,1]
	v_cvt_pk_fp8_f32 v3, v12, v13 op_sel:[0,0,1]
	v_cvt_pk_fp8_f32 v4, v8, v9 op_sel:[0,0,1]
	v_cvt_pk_fp8_f32 v5, v20, v21 op_sel:[0,0,1]
	v_add_co_u32_e32 v6, vcc, 0x2c000, v18
	s_mov_b64 s[26:27], -1
	s_nop 0
	v_addc_co_u32_e32 v7, vcc, 0, v19, vcc
	s_and_b64 vcc, exec, s[2:3]
	global_store_dwordx4 v[6:7], v[2:5], off
	s_cbranch_vccnz .LBB0_1060
	s_andn2_b64 vcc, exec, s[10:11]
	s_mov_b64 s[24:25], s[8:9]
	s_mov_b64 s[2:3], s[6:7]
	s_cbranch_vccnz .LBB0_1078
	s_ashr_i32 s15, s14, 31
	s_lshl_b64 s[2:3], s[14:15], 18
	s_add_u32 s2, s42, s2
	s_addc_u32 s3, s43, s3
	s_lshl_b32 s15, s46, 2
	s_add_i32 s24, s15, s5
	s_ashr_i32 s25, s24, 31
	s_lshl_b64 s[24:25], s[24:25], 18
	s_add_u32 s24, s44, s24
	s_addc_u32 s25, s45, s25
